# swa tile bodies: K/V fragment + 32 bias-table LDS reads software-pipelined (12 in flight, counted lgkmcnt); two s_nop hazard pads fixed in chunk phase
# baseline (speedup 1.0000x reference)
; #define R2_ZERO(M) do { _Pragma("unroll") for (int _a = 0; _a < 2; ++_a) _Pragma("unroll") for (int _b = 0; _b < 2; ++_b) _Pragma("unroll") for (int _r = 0; _r < 16; ++_r) M[_a][_b][_r] = 0.f; } while (0)
; #define R2_PACK(Bpk, M) do { _Pragma("unroll") for (int _ks = 0; _ks < 4; ++_ks) _Pragma("unroll") for (int _cb = 0; _cb < 2; ++_cb) Bpk[_ks][_cb] = pack_acc(M[_ks >> 1][_cb], _ks & 1); } while (0)
; __device__ __forceinline__ void ph_rwkv_chunk(const Params& p, int l, LAS unsigned char* lds, const int wvid) {
;     ...
;             for (int it = 0; it < 5; ++it) {
;                 { M64 A2; R2_ZERO(A2); R2_MM_LP(A2, X, Apk);
;                   asm volatile("" ::: "memory");
;                   R2_TO_LDS(X, A2); R2_PACK(Apk, A2); }
;                 R2_PACK(Tpk, Tm);
;                 R2_MM_LP(Tm, X, Tpk);
;                 asm volatile("" ::: "memory");
;             }
.LBB0_651:
	ds_read_b128 v[66:69], v225
	s_nop 4
	v_cvt_pk_bf16_f32 v166, v34, v35
	v_cvt_pk_bf16_f32 v167, v36, v37
	v_cvt_pk_bf16_f32 v168, v38, v39
	v_cvt_pk_bf16_f32 v169, v40, v41
	v_cvt_pk_bf16_f32 v162, v2, v3
	v_cvt_pk_bf16_f32 v163, v4, v5
	v_cvt_pk_bf16_f32 v164, v6, v7
	v_cvt_pk_bf16_f32 v165, v8, v9
	s_waitcnt lgkmcnt(0)
	v_mfma_f32_32x32x16_bf16 v[114:129], v[66:69], v[142:145], 0
	v_cvt_pk_bf16_f32 v170, v42, v43
	v_cvt_pk_bf16_f32 v171, v44, v45
	v_cvt_pk_bf16_f32 v172, v46, v47
	v_cvt_pk_bf16_f32 v173, v48, v49
	v_cvt_pk_bf16_f32 v174, v10, v11
	v_cvt_pk_bf16_f32 v175, v12, v13
	v_cvt_pk_bf16_f32 v176, v14, v15
	v_mfma_f32_32x32x16_bf16 v[98:113], v[66:69], v[154:157], 0
	ds_read_b128 v[66:69], v225 offset:4608
	v_cvt_pk_bf16_f32 v177, v16, v17
	v_cvt_pk_bf16_f32 v178, v50, v51
	v_cvt_pk_bf16_f32 v179, v52, v53
	v_cvt_pk_bf16_f32 v180, v54, v55
	v_cvt_pk_bf16_f32 v181, v56, v57
	s_add_i32 s40, s40, -1
	s_waitcnt lgkmcnt(0)
	v_mfma_f32_32x32x16_bf16 v[82:97], v[66:69], v[142:145], 0
	ds_read_b128 v[142:145], v225 offset:32
	s_cmp_lg_u32 s40, 0
	s_waitcnt lgkmcnt(0)
	v_mfma_f32_32x32x16_bf16 v[114:129], v[142:145], v[138:141], v[114:129]
	v_mfma_f32_32x32x16_bf16 v[98:113], v[142:145], v[146:149], v[98:113]
	ds_read_b128 v[142:145], v225 offset:4640
	s_waitcnt lgkmcnt(0)
	v_mfma_f32_32x32x16_bf16 v[82:97], v[142:145], v[138:141], v[82:97]
	ds_read_b128 v[138:141], v225 offset:64
	v_mfma_f32_32x32x16_bf16 v[66:81], v[66:69], v[154:157], 0
	s_waitcnt lgkmcnt(0)
	v_mfma_f32_32x32x16_bf16 v[114:129], v[138:141], v[158:161], v[114:129]
	v_mfma_f32_32x32x16_bf16 v[98:113], v[138:141], v[150:153], v[98:113]
	ds_read_b128 v[138:141], v225 offset:4672
	v_mfma_f32_32x32x16_bf16 v[66:81], v[142:145], v[146:149], v[66:81]
	s_waitcnt lgkmcnt(0)
	v_mfma_f32_32x32x16_bf16 v[82:97], v[138:141], v[158:161], v[82:97]
	v_mfma_f32_32x32x16_bf16 v[66:81], v[138:141], v[150:153], v[66:81]
	ds_read_b128 v[138:141], v225 offset:96
	s_waitcnt lgkmcnt(0)
	v_mfma_f32_32x32x16_bf16 v[114:129], v[138:141], v[134:137], v[114:129]
	v_mfma_f32_32x32x16_bf16 v[98:113], v[138:141], v[130:133], v[98:113]
	ds_read_b128 v[138:141], v225 offset:4704
	s_nop 9
	v_cvt_pk_bf16_f32 v142, v114, v115
	v_cvt_pk_bf16_f32 v143, v116, v117
	v_cvt_pk_bf16_f32 v144, v118, v119
	v_cvt_pk_bf16_f32 v145, v120, v121
	s_waitcnt lgkmcnt(0)
	v_mfma_f32_32x32x16_bf16 v[82:97], v[138:141], v[134:137], v[82:97]
	v_cvt_pk_bf16_f32 v154, v98, v99
	v_cvt_pk_bf16_f32 v155, v100, v101
	v_cvt_pk_bf16_f32 v156, v102, v103
	v_cvt_pk_bf16_f32 v157, v104, v105
	v_cvt_pk_bf16_f32 v146, v106, v107
	v_cvt_pk_bf16_f32 v147, v108, v109
	v_cvt_pk_bf16_f32 v148, v110, v111
	v_mfma_f32_32x32x16_bf16 v[66:81], v[138:141], v[130:133], v[66:81]
	v_cvt_pk_bf16_f32 v138, v122, v123
	v_cvt_pk_bf16_f32 v139, v124, v125
	v_cvt_pk_bf16_f32 v140, v126, v127
	v_cvt_pk_bf16_f32 v141, v128, v129
	v_cvt_pk_bf16_f32 v149, v112, v113
	v_cvt_pk_bf16_f32 v158, v82, v83
	v_cvt_pk_bf16_f32 v159, v84, v85
	v_cvt_pk_bf16_f32 v160, v86, v87
	v_cvt_pk_bf16_f32 v161, v88, v89
	v_cvt_pk_bf16_f32 v134, v90, v91
	v_cvt_pk_bf16_f32 v135, v92, v93
	v_cvt_pk_bf16_f32 v136, v94, v95
	v_cvt_pk_bf16_f32 v137, v96, v97
	v_cvt_pk_bf16_f32 v150, v66, v67
	v_cvt_pk_bf16_f32 v151, v68, v69
	v_cvt_pk_bf16_f32 v152, v70, v71
	v_cvt_pk_bf16_f32 v153, v72, v73
	v_cvt_pk_bf16_f32 v130, v74, v75
	v_cvt_pk_bf16_f32 v131, v76, v77
	v_cvt_pk_bf16_f32 v132, v78, v79
	v_cvt_pk_bf16_f32 v133, v80, v81
	ds_write_b16 v194, v142
	ds_write_b16_d16_hi v194, v142 offset:144
	ds_write_b16 v224, v143
	ds_write_b16_d16_hi v224, v143 offset:144
	ds_write_b16 v223, v144
	ds_write_b16_d16_hi v223, v144 offset:144
	ds_write_b16 v199, v145
	ds_write_b16_d16_hi v199, v145 offset:144
	ds_write_b16 v198, v138
	ds_write_b16_d16_hi v198, v138 offset:144
	ds_write_b16 v197, v139
	ds_write_b16_d16_hi v197, v139 offset:144
	ds_write_b16 v196, v140
	ds_write_b16_d16_hi v196, v140 offset:144
	ds_write_b16 v195, v141
	ds_write_b16_d16_hi v195, v141 offset:144
	ds_write_b16 v194, v154 offset:64
	ds_write_b16_d16_hi v194, v154 offset:208
	ds_write_b16 v224, v155 offset:64
	ds_write_b16_d16_hi v224, v155 offset:208
	ds_write_b16 v223, v156 offset:64
	ds_write_b16_d16_hi v223, v156 offset:208
	ds_write_b16 v199, v157 offset:64
	ds_write_b16_d16_hi v199, v157 offset:208
	ds_write_b16 v198, v146 offset:64
	ds_write_b16_d16_hi v198, v146 offset:208
	ds_write_b16 v197, v147 offset:64
	ds_write_b16_d16_hi v197, v147 offset:208
	ds_write_b16 v196, v148 offset:64
	ds_write_b16_d16_hi v196, v148 offset:208
	ds_write_b16 v195, v149 offset:64
	ds_write_b16_d16_hi v195, v149 offset:208
	ds_write_b16 v194, v158 offset:4608
	ds_write_b16_d16_hi v194, v158 offset:4752
	ds_write_b16 v193, v159
	ds_write_b16_d16_hi v193, v159 offset:144
	ds_write_b16 v193, v160 offset:864
	ds_write_b16_d16_hi v193, v160 offset:1008
	ds_write_b16 v193, v161 offset:1152
	ds_write_b16_d16_hi v193, v161 offset:1296
	ds_write_b16 v193, v134 offset:2016
	ds_write_b16_d16_hi v193, v134 offset:2160
	ds_write_b16 v193, v135 offset:2304
	ds_write_b16_d16_hi v193, v135 offset:2448
	ds_write_b16 v193, v136 offset:3168
	ds_write_b16_d16_hi v193, v136 offset:3312
	ds_write_b16 v193, v137 offset:3456
	ds_write_b16_d16_hi v193, v137 offset:3600
	ds_write_b16 v194, v150 offset:4672
	ds_write_b16_d16_hi v194, v150 offset:4816
	ds_write_b16 v193, v151 offset:64
	ds_write_b16_d16_hi v193, v151 offset:208
	ds_write_b16 v193, v152 offset:928
	ds_write_b16_d16_hi v193, v152 offset:1072
	ds_write_b16 v193, v153 offset:1216
	ds_write_b16_d16_hi v193, v153 offset:1360
	ds_write_b16 v193, v130 offset:2080
	ds_write_b16_d16_hi v193, v130 offset:2224
	ds_write_b16 v193, v131 offset:2368
	ds_write_b16_d16_hi v193, v131 offset:2512
	ds_write_b16 v193, v132 offset:3232
	ds_write_b16_d16_hi v193, v132 offset:3376
	ds_write_b16 v193, v133 offset:3520
	ds_write_b16_d16_hi v193, v133 offset:3664
	ds_read_b128 v[66:69], v225
	s_waitcnt lgkmcnt(0)
; #define R2_PACK(Bpk, M) do { _Pragma("unroll") for (int _ks = 0; _ks < 4; ++_ks) _Pragma("unroll") for (int _cb = 0; _cb < 2; ++_cb) Bpk[_ks][_cb] = pack_acc(M[_ks >> 1][_cb], _ks & 1); } while (0)
; __device__ __forceinline__ void ph_rwkv_chunk(const Params& p, int l, LAS unsigned char* lds, const int wvid) {
;     ...
;                 R2_MM_LP(Tm, X, Tpk);
;                 asm volatile("" ::: "memory");
;             }
;             R2_PACK(Tpk, Tm);
;         }
;         {
;             R2_RAW(X, ATg); R2_TRANS_L(Y, X);
	v_mfma_f32_32x32x16_bf16 v[34:49], v[66:69], v[166:169], v[34:49]
	v_cvt_pk_bf16_f32 v70, v18, v19
	v_cvt_pk_bf16_f32 v74, v58, v59
	v_cvt_pk_bf16_f32 v75, v60, v61
	v_cvt_pk_bf16_f32 v76, v62, v63
	v_cvt_pk_bf16_f32 v77, v64, v65
	v_cvt_pk_bf16_f32 v71, v20, v21
	v_cvt_pk_bf16_f32 v72, v22, v23
	v_mfma_f32_32x32x16_bf16 v[2:17], v[66:69], v[162:165], v[2:17]
	ds_read_b128 v[66:69], v225 offset:4608
	v_cvt_pk_bf16_f32 v73, v24, v25
	v_cvt_pk_bf16_f32 v78, v26, v27
	v_cvt_pk_bf16_f32 v79, v28, v29
	v_cvt_pk_bf16_f32 v80, v30, v31
	v_cvt_pk_bf16_f32 v81, v32, v33
	s_waitcnt lgkmcnt(0)
	v_mfma_f32_32x32x16_bf16 v[50:65], v[66:69], v[166:169], v[50:65]
	v_mfma_f32_32x32x16_bf16 v[18:33], v[66:69], v[162:165], v[18:33]
	ds_read_b128 v[66:69], v225 offset:32
	s_waitcnt lgkmcnt(0)
	v_mfma_f32_32x32x16_bf16 v[34:49], v[66:69], v[170:173], v[34:49]
	v_mfma_f32_32x32x16_bf16 v[2:17], v[66:69], v[174:177], v[2:17]
	ds_read_b128 v[66:69], v225 offset:4640
	s_waitcnt lgkmcnt(0)
	v_mfma_f32_32x32x16_bf16 v[50:65], v[66:69], v[170:173], v[50:65]
	v_mfma_f32_32x32x16_bf16 v[18:33], v[66:69], v[174:177], v[18:33]
	ds_read_b128 v[66:69], v225 offset:64
	s_waitcnt lgkmcnt(0)
	v_mfma_f32_32x32x16_bf16 v[34:49], v[66:69], v[178:181], v[34:49]
	v_mfma_f32_32x32x16_bf16 v[2:17], v[66:69], v[70:73], v[2:17]
	ds_read_b128 v[66:69], v225 offset:4672
	s_waitcnt lgkmcnt(0)
	v_mfma_f32_32x32x16_bf16 v[50:65], v[66:69], v[178:181], v[50:65]
	v_mfma_f32_32x32x16_bf16 v[18:33], v[66:69], v[70:73], v[18:33]
	ds_read_b128 v[66:69], v225 offset:96
	s_waitcnt lgkmcnt(0)
	v_mfma_f32_32x32x16_bf16 v[34:49], v[66:69], v[74:77], v[34:49]
	v_mfma_f32_32x32x16_bf16 v[2:17], v[66:69], v[78:81], v[2:17]
	ds_read_b128 v[66:69], v225 offset:4704
	s_waitcnt lgkmcnt(0)
	v_mfma_f32_32x32x16_bf16 v[50:65], v[66:69], v[74:77], v[50:65]
	v_mfma_f32_32x32x16_bf16 v[18:33], v[66:69], v[78:81], v[18:33]
	s_cbranch_scc1 .LBB0_651
	v_lshlrev_b32_e32 v0, 4, v183
	v_lshl_add_u64 v[82:83], s[86:87], 0, v[0:1]
	s_movk_i32 s44, 0x1000
	v_add_co_u32_e32 v94, vcc, s44, v82
	global_load_dwordx4 v[66:69], v0, s[86:87]
	global_load_dwordx4 v[70:73], v0, s[86:87] offset:1024
	global_load_dwordx4 v[74:77], v0, s[86:87] offset:2048
	global_load_dwordx4 v[78:81], v0, s[86:87] offset:3072
	v_addc_co_u32_e32 v95, vcc, 0, v83, vcc
	global_load_dwordx4 v[82:85], v[94:95], off
	global_load_dwordx4 v[86:89], v[94:95], off offset:1024
	global_load_dwordx4 v[90:93], v[94:95], off offset:2048
	s_nop 0
	global_load_dwordx4 v[94:97], v[94:95], off offset:3072
	v_lshlrev_b32_e32 v0, 4, v182
	v_lshrrev_b32_e32 v98, 1, v183
	v_bfe_u32 v99, v182, 1, 5
	v_and_b32_e32 v0, 16, v0
	v_mul_u32_u24_e32 v98, 0x90, v98
	v_mul_u32_u24_e32 v99, 0x90, v99
	v_add3_u32 v98, s48, v98, v0
	v_add3_u32 v0, s48, v99, v0
	v_lshl_add_u32 v100, v183, 1, s48
	v_mov_b32_e32 v191, s48
	v_mad_u32_u24 v101, v183, s83, v191
	v_cvt_pk_bf16_f32 v166, v2, v3
	v_cvt_pk_bf16_f32 v167, v4, v5
	v_cvt_pk_bf16_f32 v162, v34, v35
	v_cvt_pk_bf16_f32 v163, v36, v37
	v_cvt_pk_bf16_f32 v164, v38, v39
	v_cvt_pk_bf16_f32 v165, v40, v41
	v_cvt_pk_bf16_f32 v168, v6, v7
	v_cvt_pk_bf16_f32 v169, v8, v9
	v_cvt_pk_bf16_f32 v154, v42, v43
	v_cvt_pk_bf16_f32 v155, v44, v45
	v_cvt_pk_bf16_f32 v156, v46, v47
	v_cvt_pk_bf16_f32 v157, v48, v49
	v_cvt_pk_bf16_f32 v158, v10, v11
	v_cvt_pk_bf16_f32 v159, v12, v13
	v_cvt_pk_bf16_f32 v160, v14, v15
	v_cvt_pk_bf16_f32 v161, v16, v17
	v_cvt_pk_bf16_f32 v182, v50, v51
	v_cvt_pk_bf16_f32 v183, v52, v53
	v_cvt_pk_bf16_f32 v184, v54, v55
	v_cvt_pk_bf16_f32 v185, v56, v57
	v_cvt_pk_bf16_f32 v186, v18, v19
	v_cvt_pk_bf16_f32 v187, v20, v21
	v_cvt_pk_bf16_f32 v188, v22, v23
	v_cvt_pk_bf16_f32 v189, v24, v25
	v_cvt_pk_bf16_f32 v178, v58, v59
	v_cvt_pk_bf16_f32 v179, v60, v61
	v_cvt_pk_bf16_f32 v180, v62, v63
	v_cvt_pk_bf16_f32 v181, v64, v65
	v_cvt_pk_bf16_f32 v150, v26, v27
	v_cvt_pk_bf16_f32 v151, v28, v29
	v_cvt_pk_bf16_f32 v152, v30, v31
	v_cvt_pk_bf16_f32 v153, v32, v33
	s_lshl_b64 s[38:39], s[42:43], 1
	s_add_u32 s72, s94, s38
	s_addc_u32 s73, s52, s39
	s_add_u32 s36, s53, s38
	s_addc_u32 s37, s59, s39
	s_add_u32 s54, s46, s38
	s_addc_u32 s55, s77, s39
	s_mov_b32 s42, s41
	s_mov_b32 s43, s41
	s_mov_b32 s40, s41
	s_waitcnt vmcnt(7)
	ds_write_b128 v98, v[66:69]
	s_waitcnt vmcnt(6)
	ds_write_b128 v98, v[70:73] offset:4608
	s_waitcnt vmcnt(5)
	ds_write_b128 v98, v[74:77] offset:32
	s_waitcnt vmcnt(4)
	ds_write_b128 v0, v[78:81] offset:4640
	s_waitcnt vmcnt(3)
	ds_write_b128 v98, v[82:85] offset:64
	s_waitcnt vmcnt(2)
	ds_write_b128 v0, v[86:89] offset:4672
	s_waitcnt vmcnt(1)
	ds_write_b128 v98, v[90:93] offset:96
	s_waitcnt vmcnt(0)
	ds_write_b128 v0, v[94:97] offset:4704
	ds_read_u16 v0, v100
	ds_read_u16 v66, v100 offset:144
	ds_read_u16 v67, v100 offset:288
	ds_read_u16 v68, v100 offset:432
	ds_read_u16 v70, v100 offset:576
	ds_read_u16 v71, v100 offset:720
	ds_read_u16 v72, v100 offset:864
	ds_read_u16 v73, v100 offset:1008
	ds_read_u16 v69, v100 offset:1152
	ds_read_u16 v74, v100 offset:1296
	ds_read_u16 v75, v100 offset:1440
	ds_read_u16 v76, v100 offset:1584
	ds_read_u16 v77, v100 offset:1728
	ds_read_u16 v78, v100 offset:1872
	ds_read_u16 v79, v100 offset:2016
	ds_read_u16 v80, v100 offset:2160
	ds_read_u16 v81, v100 offset:2304
	ds_read_u16 v82, v100 offset:2448
	ds_read_u16 v83, v100 offset:2592
	ds_read_u16 v84, v100 offset:2736
	ds_read_u16 v85, v100 offset:2880
	ds_read_u16 v86, v100 offset:3024
	ds_read_u16 v87, v100 offset:3168
	ds_read_u16 v88, v100 offset:3312
	ds_read_u16 v89, v100 offset:3456
	ds_read_u16 v90, v100 offset:3600
	ds_read_u16 v91, v100 offset:3744
	ds_read_u16 v92, v100 offset:3888
	ds_read_u16 v93, v100 offset:4032
	ds_read_u16 v94, v100 offset:4176
	ds_read_u16 v95, v100 offset:4320
	ds_read_u16 v96, v100 offset:4464
	ds_read_u16 v97, v100 offset:4608
	ds_read_u16 v98, v100 offset:4752
	ds_read_u16 v99, v100 offset:4896
	ds_read_u16 v102, v100 offset:5040
	ds_read_u16 v103, v100 offset:5184
	ds_read_u16 v104, v100 offset:5328
	s_waitcnt lgkmcnt(14)
; #define R2_ZERO(M) do { _Pragma("unroll") for (int _a = 0; _a < 2; ++_a) _Pragma("unroll") for (int _b = 0; _b < 2; ++_b) _Pragma("unroll") for (int _r = 0; _r < 16; ++_r) M[_a][_b][_r] = 0.f; } while (0)
; __device__ __forceinline__ void ph_rwkv_chunk(const Params& p, int l, LAS unsigned char* lds, const int wvid) {
;     ...
;             R2_RAW(X, ATg); R2_TRANS_L(Y, X);
;             M64 W; R2_ZERO(W); R2_MM_LP(W, Y, Tpk);
;             R2_TO_LDS(X, W);
	v_lshl_or_b32 v66, v66, 16, v0
	v_lshl_or_b32 v67, v68, 16, v67
	v_lshl_or_b32 v68, v74, 16, v69
	v_lshl_or_b32 v69, v76, 16, v75
	v_lshl_or_b32 v70, v71, 16, v70
	v_lshl_or_b32 v71, v73, 16, v72
	v_lshl_or_b32 v72, v78, 16, v77
	v_lshl_or_b32 v73, v80, 16, v79
	v_lshl_or_b32 v74, v82, 16, v81
	v_lshl_or_b32 v75, v84, 16, v83
	s_waitcnt lgkmcnt(12)
	v_lshl_or_b32 v76, v90, 16, v89
	s_waitcnt lgkmcnt(10)
	v_lshl_or_b32 v77, v92, 16, v91
	v_lshl_or_b32 v78, v86, 16, v85
	v_lshl_or_b32 v79, v88, 16, v87
	s_waitcnt lgkmcnt(8)
	v_lshl_or_b32 v80, v94, 16, v93
	s_waitcnt lgkmcnt(6)
	v_lshl_or_b32 v81, v96, 16, v95
	ds_write_b128 v101, v[66:69] offset:9216
	ds_write_b128 v101, v[70:73] offset:9232
	ds_write_b128 v101, v[74:77] offset:9248
	ds_write_b128 v101, v[78:81] offset:9264
	ds_read_u16 v0, v100 offset:5472
	ds_read_u16 v70, v100 offset:5616
	ds_read_u16 v68, v100 offset:5760
	ds_read_u16 v69, v100 offset:5904
	ds_read_u16 v71, v100 offset:6048
	ds_read_u16 v72, v100 offset:6192
	ds_read_u16 v73, v100 offset:6336
	ds_read_u16 v74, v100 offset:6480
	ds_read_u16 v75, v100 offset:6624
	ds_read_u16 v76, v100 offset:6768
	s_waitcnt lgkmcnt(14)
	v_lshl_or_b32 v66, v98, 16, v97
	v_lshl_or_b32 v67, v102, 16, v99
	s_waitcnt lgkmcnt(6)
	v_lshl_or_b32 v68, v69, 16, v68
	s_waitcnt lgkmcnt(4)
	v_lshl_or_b32 v69, v72, 16, v71
	ds_write_b128 v101, v[66:69] offset:9280
	v_lshl_or_b32 v66, v104, 16, v103
	v_lshl_or_b32 v67, v70, 16, v0
	s_waitcnt lgkmcnt(3)
	v_lshl_or_b32 v68, v74, 16, v73
	s_waitcnt lgkmcnt(1)
	v_lshl_or_b32 v69, v76, 16, v75
	ds_write_b128 v101, v[66:69] offset:9296
	ds_read_u16 v0, v100 offset:6912
	ds_read_u16 v66, v100 offset:7056
	ds_read_u16 v67, v100 offset:7200
	ds_read_u16 v68, v100 offset:7344
	ds_read_u16 v70, v100 offset:7488
	ds_read_u16 v71, v100 offset:7632
	ds_read_u16 v72, v100 offset:7776
	ds_read_u16 v73, v100 offset:7920
	s_waitcnt lgkmcnt(6)
	v_lshl_or_b32 v66, v66, 16, v0
	s_waitcnt lgkmcnt(4)
	v_lshl_or_b32 v67, v68, 16, v67
	ds_read_u16 v0, v100 offset:8064
	ds_read_u16 v68, v100 offset:8208
	ds_read_u16 v69, v100 offset:8352
	ds_read_u16 v74, v100 offset:8496
	ds_read_u16 v75, v100 offset:8640
	ds_read_u16 v76, v100 offset:8784
	ds_read_u16 v77, v100 offset:8928
	ds_read_u16 v78, v100 offset:9072
	s_waitcnt lgkmcnt(6)
	v_lshl_or_b32 v68, v68, 16, v0
	s_waitcnt lgkmcnt(4)
	v_lshl_or_b32 v69, v74, 16, v69
	ds_write_b128 v101, v[66:69] offset:9312
	v_lshl_or_b32 v66, v71, 16, v70
	v_lshl_or_b32 v67, v73, 16, v72
	s_waitcnt lgkmcnt(3)
	v_lshl_or_b32 v68, v76, 16, v75
	s_waitcnt lgkmcnt(1)
	v_lshl_or_b32 v69, v78, 16, v77
	ds_write_b128 v101, v[66:69] offset:9328
	ds_read_b128 v[66:69], v225 offset:9216
	ds_read_b128 v[2:5], v225 offset:13824
	s_waitcnt lgkmcnt(1)
	v_mfma_f32_32x32x16_bf16 v[114:129], v[66:69], v[162:165], 0
	v_mfma_f32_32x32x16_bf16 v[98:113], v[66:69], v[166:169], 0
	s_waitcnt lgkmcnt(0)
	v_mfma_f32_32x32x16_bf16 v[82:97], v[2:5], v[162:165], 0
	v_mfma_f32_32x32x16_bf16 v[66:81], v[2:5], v[166:169], 0
	ds_read_b128 v[2:5], v225 offset:9248
	s_waitcnt lgkmcnt(0)
	v_mfma_f32_32x32x16_bf16 v[114:129], v[2:5], v[154:157], v[114:129]
	v_mfma_f32_32x32x16_bf16 v[98:113], v[2:5], v[158:161], v[98:113]
	ds_read_b128 v[2:5], v225 offset:13856
	s_waitcnt lgkmcnt(0)
	v_mfma_f32_32x32x16_bf16 v[82:97], v[2:5], v[154:157], v[82:97]
	v_mfma_f32_32x32x16_bf16 v[66:81], v[2:5], v[158:161], v[66:81]
	ds_read_b128 v[2:5], v225 offset:9280
	s_waitcnt lgkmcnt(0)
	v_mfma_f32_32x32x16_bf16 v[114:129], v[2:5], v[182:185], v[114:129]
	v_mfma_f32_32x32x16_bf16 v[98:113], v[2:5], v[186:189], v[98:113]
	ds_read_b128 v[2:5], v225 offset:13888
	s_waitcnt lgkmcnt(0)
	v_mfma_f32_32x32x16_bf16 v[82:97], v[2:5], v[182:185], v[82:97]
	v_mfma_f32_32x32x16_bf16 v[66:81], v[2:5], v[186:189], v[66:81]
	ds_read_b128 v[2:5], v225 offset:9312
	s_waitcnt lgkmcnt(0)
	v_mfma_f32_32x32x16_bf16 v[114:129], v[2:5], v[178:181], v[114:129]
	v_mfma_f32_32x32x16_bf16 v[98:113], v[2:5], v[150:153], v[98:113]
	ds_read_b128 v[2:5], v225 offset:13920
	s_nop 9
	v_cvt_pk_bf16_f32 v0, v114, v115
	ds_write_b16 v194, v0
	ds_write_b16_d16_hi v194, v0 offset:144
	v_cvt_pk_bf16_f32 v0, v116, v117
	ds_write_b16 v224, v0
	ds_write_b16_d16_hi v224, v0 offset:144
	v_cvt_pk_bf16_f32 v0, v118, v119
	ds_write_b16 v223, v0
	ds_write_b16_d16_hi v223, v0 offset:144
	v_cvt_pk_bf16_f32 v0, v120, v121
	ds_write_b16 v199, v0
	ds_write_b16_d16_hi v199, v0 offset:144
	v_cvt_pk_bf16_f32 v0, v122, v123
	ds_write_b16 v198, v0
	ds_write_b16_d16_hi v198, v0 offset:144
	v_cvt_pk_bf16_f32 v0, v124, v125
	ds_write_b16 v197, v0
	ds_write_b16_d16_hi v197, v0 offset:144
	v_cvt_pk_bf16_f32 v0, v126, v127
	ds_write_b16 v196, v0
	ds_write_b16_d16_hi v196, v0 offset:144
	v_cvt_pk_bf16_f32 v0, v128, v129
	s_waitcnt lgkmcnt(14)
; #define R2_ZERO(M) do { _Pragma("unroll") for (int _a = 0; _a < 2; ++_a) _Pragma("unroll") for (int _b = 0; _b < 2; ++_b) _Pragma("unroll") for (int _r = 0; _r < 16; ++_r) M[_a][_b][_r] = 0.f; } while (0)
; #define R2_PACK(Bpk, M) do { _Pragma("unroll") for (int _ks = 0; _ks < 4; ++_ks) _Pragma("unroll") for (int _cb = 0; _cb < 2; ++_cb) Bpk[_ks][_cb] = pack_acc(M[_ks >> 1][_cb], _ks & 1); } while (0)
; #define R2_MASK(M, STRICT) do { _Pragma("unroll") for (int _rb = 0; _rb < 2; ++_rb) _Pragma("unroll") for (int _cb = 0; _cb < 2; ++_cb) _Pragma("unroll") for (int _r = 0; _r < 16; ++_r) { \
;         const int _row = 32 * _rb + (_r & 3) + 8 * (_r >> 2) + 4 * hi, _col = 32 * _cb + l31; if (STRICT ? !(_row < _col) : !(_row <= _col)) M[_rb][_cb][_r] = 0.f; } } while (0)
; #define R2_RELANE() do { lane = lt_tid(wvid) & 63; l31 = lane & 31; hi = lane >> 5; } while (0)
; __device__ __forceinline__ void ph_rwkv_chunk(const Params& p, int l, LAS unsigned char* lds, const int wvid) {
;     ...
;             R2_TO_LDS(X, W);
;         }
;         R2_RELANE();
;         {
;             M64 B; R2_ZERO(B); R2_MM_GG(B, BTg, RTg); R2_MASK(B, false); R2_PACK(ABR, B);
	v_mfma_f32_32x32x16_bf16 v[82:97], v[2:5], v[178:181], v[82:97]
	ds_write_b16 v195, v0
	ds_write_b16_d16_hi v195, v0 offset:144
	v_cvt_pk_bf16_f32 v0, v98, v99
	ds_write_b16 v194, v0 offset:64
	ds_write_b16_d16_hi v194, v0 offset:208
	v_cvt_pk_bf16_f32 v0, v100, v101
	ds_write_b16 v224, v0 offset:64
	ds_write_b16_d16_hi v224, v0 offset:208
	v_cvt_pk_bf16_f32 v0, v102, v103
	ds_write_b16 v223, v0 offset:64
	ds_write_b16_d16_hi v223, v0 offset:208
	v_cvt_pk_bf16_f32 v0, v104, v105
	ds_write_b16 v199, v0 offset:64
	ds_write_b16_d16_hi v199, v0 offset:208
	v_cvt_pk_bf16_f32 v0, v106, v107
	ds_write_b16 v198, v0 offset:64
	ds_write_b16_d16_hi v198, v0 offset:208
	v_cvt_pk_bf16_f32 v0, v108, v109
	ds_write_b16 v197, v0 offset:64
	ds_write_b16_d16_hi v197, v0 offset:208
	v_cvt_pk_bf16_f32 v0, v110, v111
	ds_write_b16 v196, v0 offset:64
	ds_write_b16_d16_hi v196, v0 offset:208
	v_cvt_pk_bf16_f32 v0, v112, v113
	v_mfma_f32_32x32x16_bf16 v[66:81], v[2:5], v[150:153], v[66:81]
	ds_write_b16 v195, v0 offset:64
	ds_write_b16_d16_hi v195, v0 offset:208
	v_cvt_pk_bf16_f32 v0, v82, v83
	ds_write_b16 v194, v0 offset:4608
	ds_write_b16_d16_hi v194, v0 offset:4752
	v_cvt_pk_bf16_f32 v0, v84, v85
	ds_write_b16 v193, v0
	ds_write_b16_d16_hi v193, v0 offset:144
	v_cvt_pk_bf16_f32 v0, v86, v87
	ds_write_b16 v193, v0 offset:864
	ds_write_b16_d16_hi v193, v0 offset:1008
	v_cvt_pk_bf16_f32 v0, v88, v89
	ds_write_b16 v193, v0 offset:1152
	ds_write_b16_d16_hi v193, v0 offset:1296
	v_cvt_pk_bf16_f32 v0, v90, v91
	ds_write_b16 v193, v0 offset:2016
	ds_write_b16_d16_hi v193, v0 offset:2160
	v_cvt_pk_bf16_f32 v0, v92, v93
	ds_write_b16 v193, v0 offset:2304
	ds_write_b16_d16_hi v193, v0 offset:2448
	v_cvt_pk_bf16_f32 v0, v94, v95
	ds_write_b16 v193, v0 offset:3168
	ds_write_b16_d16_hi v193, v0 offset:3312
	v_cvt_pk_bf16_f32 v0, v96, v97
	ds_write_b16 v193, v0 offset:3456
	ds_write_b16_d16_hi v193, v0 offset:3600
	v_cvt_pk_bf16_f32 v0, v66, v67
	ds_write_b16 v194, v0 offset:4672
	ds_write_b16_d16_hi v194, v0 offset:4816
	v_cvt_pk_bf16_f32 v0, v68, v69
	ds_write_b16 v193, v0 offset:64
	ds_write_b16_d16_hi v193, v0 offset:208
	v_cvt_pk_bf16_f32 v0, v70, v71
	ds_write_b16 v193, v0 offset:928
	ds_write_b16_d16_hi v193, v0 offset:1072
	v_cvt_pk_bf16_f32 v0, v72, v73
	ds_write_b16 v193, v0 offset:1216
	ds_write_b16_d16_hi v193, v0 offset:1360
	v_cvt_pk_bf16_f32 v0, v74, v75
	ds_write_b16 v193, v0 offset:2080
	ds_write_b16_d16_hi v193, v0 offset:2224
	v_cvt_pk_bf16_f32 v0, v76, v77
	ds_write_b16 v193, v0 offset:2368
	ds_write_b16_d16_hi v193, v0 offset:2512
	v_cvt_pk_bf16_f32 v0, v78, v79
	ds_write_b16 v193, v0 offset:3232
	ds_write_b16_d16_hi v193, v0 offset:3376
	v_cvt_pk_bf16_f32 v0, v80, v81
	ds_write_b16 v193, v0 offset:3520
	ds_write_b16_d16_hi v193, v0 offset:3664
	v_mbcnt_lo_u32_b32 v199, -1, 0
	v_mbcnt_hi_u32_b32 v199, -1, v199
	s_nop 0
	v_and_b32_e32 v119, 31, v199
	v_bfe_u32 v198, v199, 5, 1
	v_lshlrev_b32_e32 v62, 5, v119
	v_lshlrev_b32_e32 v0, 4, v198
	v_or_b32_e32 v114, v0, v62
	v_or_b32_e32 v200, 0x1000, v114
	v_or_b32_e32 v201, 0x1400, v114
	v_or_b32_e32 v202, 0x1800, v114
	v_or_b32_e32 v203, 0x1c00, v114
	global_load_dwordx4 v[72:75], v114, s[70:71]
	global_load_dwordx4 v[76:79], v114, s[54:55]
	global_load_dwordx4 v[80:83], v114, s[54:55] offset:1024
	global_load_dwordx4 v[84:87], v114, s[70:71] offset:1024
	global_load_dwordx4 v[88:91], v114, s[70:71] offset:2048
	global_load_dwordx4 v[92:95], v114, s[54:55] offset:2048
	global_load_dwordx4 v[96:99], v200, s[70:71]
	global_load_dwordx4 v[100:103], v114, s[54:55] offset:3072
	global_load_dwordx4 v[104:107], v114, s[70:71] offset:3072
	global_load_dwordx4 v[108:111], v200, s[54:55]
	global_load_dwordx4 v[132:135], v201, s[70:71]
	global_load_dwordx4 v[136:139], v201, s[54:55]
	global_load_dwordx4 v[140:143], v202, s[70:71]
	global_load_dwordx4 v[144:147], v202, s[54:55]
	global_load_dwordx4 v[232:235], v203, s[70:71]
	global_load_dwordx4 v[236:239], v203, s[54:55]
	s_waitcnt vmcnt(0)
	v_mfma_f32_32x32x16_bf16 v[18:33], v[72:75], v[76:79], 0
	v_or_b32_e32 v117, 0x1000, v114
	v_or_b32_e32 v115, 0x1400, v114
	v_or_b32_e32 v118, 0x1800, v114
	v_or_b32_e32 v116, 0x1c00, v114
	v_lshlrev_b32_e32 v120, 2, v198
	v_cmp_gt_u32_e32 vcc, v120, v119
	s_waitcnt vmcnt(0)
	v_mfma_f32_32x32x16_bf16 v[34:49], v[72:75], v[80:83], 0
	v_cmp_lt_u32_e64 s[0:1], v120, v119
	v_or_b32_e32 v121, 2, v120
	v_lshl_or_b32 v66, v198, 3, v62
	v_or_b32_e32 v122, 3, v120
	s_waitcnt vmcnt(1)
	v_mfma_f32_32x32x16_bf16 v[18:33], v[88:91], v[92:95], v[18:33]
	v_or_b32_e32 v124, 8, v120
	v_or_b32_e32 v123, 9, v120
	v_or_b32_e32 v125, 10, v120
	v_or_b32_e32 v127, 11, v120
	v_or_b32_e32 v126, 16, v120
	v_or_b32_e32 v64, 0x1800, v66
	s_waitcnt vmcnt(0)
	v_mfma_f32_32x32x16_bf16 v[34:49], v[88:91], v[100:103], v[34:49]
	v_or_b32_e32 v128, 17, v120
	v_or_b32_e32 v129, 18, v120
	v_or_b32_e32 v194, 19, v120
	v_or_b32_e32 v193, 24, v120
	v_or_b32_e32 v195, 25, v120
	v_or_b32_e32 v196, 26, v120
	v_mfma_f32_32x32x16_bf16 v[2:17], v[84:87], v[80:83], 0
	v_or_b32_e32 v197, 27, v120
	v_cmp_eq_u32_e64 s[2:3], v121, v119
	v_cmp_eq_u32_e64 s[4:5], v122, v119
	v_cmp_eq_u32_e64 s[6:7], v124, v119
	v_cmp_eq_u32_e64 s[8:9], v123, v119
	v_cmp_eq_u32_e64 s[10:11], v125, v119
	v_cmp_eq_u32_e64 s[16:17], v127, v119
	s_waitcnt vmcnt(0)
	v_mfma_f32_32x32x16_bf16 v[2:17], v[104:107], v[100:103], v[2:17]
	v_cmp_eq_u32_e64 s[18:19], v126, v119
	v_cmp_eq_u32_e64 s[20:21], v128, v119
	v_cmp_eq_u32_e64 s[22:23], v129, v119
	v_cmp_eq_u32_e64 s[24:25], v194, v119
	v_cmp_eq_u32_e64 s[26:27], v193, v119
	s_waitcnt vmcnt(1)
; __device__ __forceinline__ float bflo(unsigned w) { return __uint_as_float(w << 16); }
; __device__ __forceinline__ float bfhi(unsigned w) { return __uint_as_float(w & 0xFFFF0000u); }
; #define R2_ZERO(M) do { _Pragma("unroll") for (int _a = 0; _a < 2; ++_a) _Pragma("unroll") for (int _b = 0; _b < 2; ++_b) _Pragma("unroll") for (int _r = 0; _r < 16; ++_r) M[_a][_b][_r] = 0.f; } while (0)
; #define R2_PACK(Bpk, M) do { _Pragma("unroll") for (int _ks = 0; _ks < 4; ++_ks) _Pragma("unroll") for (int _cb = 0; _cb < 2; ++_cb) Bpk[_ks][_cb] = pack_acc(M[_ks >> 1][_cb], _ks & 1); } while (0)
; #define R2_MASK(M, STRICT) do { _Pragma("unroll") for (int _rb = 0; _rb < 2; ++_rb) _Pragma("unroll") for (int _cb = 0; _cb < 2; ++_cb) _Pragma("unroll") for (int _r = 0; _r < 16; ++_r) { \
;         const int _row = 32 * _rb + (_r & 3) + 8 * (_r >> 2) + 4 * hi, _col = 32 * _cb + l31; if (STRICT ? !(_row < _col) : !(_row <= _col)) M[_rb][_cb][_r] = 0.f; } } while (0)
; __device__ __forceinline__ void ph_rwkv_chunk(const Params& p, int l, LAS unsigned char* lds, const int wvid) {
;     ...
;             M64 B; R2_ZERO(B); R2_MM_GG(B, BTg, RTg); R2_MASK(B, false); R2_PACK(ABR, B);
;         }
;         {
;             M64 G;
; #pragma unroll
;             for (int rb = 0; rb < 2; ++rb)
; #pragma unroll
;                 for (int cb = 0; cb < 2; ++cb)
; #pragma unroll
;                     for (int q = 0; q < 4; ++q) { const u32x2 w = *(const u32x2*)(RTg + TM(32 * cb + l31, 32 * rb + 8 * q + 4 * hi));
;                         G[rb][cb][4 * q] = bflo(w.x); G[rb][cb][4 * q + 1] = bfhi(w.x); G[rb][cb][4 * q + 2] = bflo(w.y); G[rb][cb][4 * q + 3] = bfhi(w.y); }
;             R2_MM_LP(G, X, ABR);
	v_mfma_f32_32x32x16_bf16 v[18:33], v[96:99], v[108:111], v[18:33]
	v_cmp_eq_u32_e64 s[28:29], v195, v119
	v_cmp_eq_u32_e64 s[30:31], v196, v119
	v_cmp_eq_u32_e64 s[34:35], v197, v119
	s_waitcnt vmcnt(0)
	v_mfma_f32_32x32x16_bf16 v[34:49], v[96:99], v[136:139], v[34:49]
	v_mfma_f32_32x32x16_bf16 v[2:17], v[132:135], v[136:139], v[2:17]
	s_waitcnt vmcnt(1)
	v_mfma_f32_32x32x16_bf16 v[18:33], v[140:143], v[144:147], v[18:33]
	s_nop 11
	v_cndmask_b32_e64 v68, 0, v19, s[0:1]
	s_waitcnt vmcnt(0)
	v_mfma_f32_32x32x16_bf16 v[2:17], v[232:235], v[236:239], v[2:17]
	v_cndmask_b32_e64 v54, v18, 0, vcc
	v_cndmask_b32_e64 v67, v54, v18, s[0:1]
	v_cmp_le_u32_e64 s[0:1], v121, v119
	v_or_b32_e32 v18, 0x800, v66
	global_load_dwordx2 v[54:55], v18, s[54:55] offset:16
	v_cndmask_b32_e64 v69, 0, v20, s[0:1]
	v_or_b32_e32 v20, 0x400, v66
	v_cmp_le_u32_e64 s[0:1], v122, v119
	v_mfma_f32_32x32x16_bf16 v[34:49], v[140:143], v[236:239], v[34:49]
	global_load_dwordx2 v[58:59], v66, s[54:55]
	global_load_dwordx2 v[50:51], v66, s[54:55] offset:16
	global_load_dwordx2 v[56:57], v20, s[54:55] offset:16
	global_load_dwordx2 v[52:53], v66, s[54:55] offset:2048
	global_load_dwordx2 v[18:19], v66, s[54:55] offset:1024
	v_cndmask_b32_e64 v70, 0, v21, s[0:1]
	v_cmp_le_u32_e64 s[0:1], v124, v119
	v_or_b32_e32 v20, 0xc00, v66
	global_load_dwordx2 v[60:61], v20, s[54:55] offset:16
	global_load_dwordx2 v[62:63], v66, s[54:55] offset:3072
	v_cndmask_b32_e64 v71, 0, v22, s[0:1]
	v_or_b32_e32 v22, 0x1000, v66
	global_load_dwordx2 v[20:21], v22, s[54:55]
	v_cmp_le_u32_e64 s[0:1], v123, v119
	v_cvt_pk_bf16_f32 v134, v67, v68
	v_cvt_pk_bf16_f32 v135, v69, v70
	v_cndmask_b32_e64 v72, 0, v23, s[0:1]
	v_cmp_le_u32_e64 s[0:1], v125, v119
	v_cvt_pk_bf16_f32 v136, v71, v72
	v_cvt_pk_bf16_f32 v138, v34, v35
	v_cndmask_b32_e64 v73, 0, v24, s[0:1]
	v_cmp_le_u32_e64 s[0:1], v127, v119
	v_cvt_pk_bf16_f32 v139, v36, v37
	v_cvt_pk_bf16_f32 v140, v38, v39
	v_cndmask_b32_e64 v74, 0, v25, s[0:1]
	v_cmp_le_u32_e64 s[0:1], v126, v119
	global_load_dwordx2 v[24:25], v64, s[54:55]
	v_cvt_pk_bf16_f32 v137, v73, v74
	v_cndmask_b32_e64 v130, 0, v26, s[0:1]
	v_or_b32_e32 v26, 0x1400, v66
	global_load_dwordx2 v[100:101], v26, s[54:55]
	global_load_dwordx2 v[104:105], v26, s[54:55] offset:16
	v_cmp_le_u32_e64 s[0:1], v128, v119
	global_load_dwordx2 v[22:23], v22, s[54:55] offset:16
	v_or_b32_e32 v26, 0x1c00, v66
	v_cndmask_b32_e64 v131, 0, v27, s[0:1]
	v_cmp_le_u32_e64 s[0:1], v129, v119
	global_load_dwordx2 v[64:65], v64, s[54:55] offset:16
	v_cvt_pk_bf16_f32 v141, v40, v41
	v_cndmask_b32_e64 v132, 0, v28, s[0:1]
	v_cmp_le_u32_e64 s[0:1], v194, v119
	global_load_dwordx2 v[108:109], v26, s[54:55]
	v_cvt_pk_bf16_f32 v142, v130, v131
	v_cndmask_b32_e64 v133, 0, v29, s[0:1]
	v_cmp_le_u32_e64 s[0:1], v193, v119
	v_cvt_pk_bf16_f32 v143, v132, v133
	v_cvt_pk_bf16_f32 v146, v42, v43
	v_cndmask_b32_e64 v144, 0, v30, s[0:1]
	v_cmp_le_u32_e64 s[0:1], v195, v119
	v_cvt_pk_bf16_f32 v147, v44, v45
	v_cvt_pk_bf16_f32 v148, v46, v47
	v_cndmask_b32_e64 v145, 0, v31, s[0:1]
	global_load_dwordx2 v[30:31], v26, s[54:55] offset:16
	v_cmp_le_u32_e64 s[0:1], v196, v119
	v_cvt_pk_bf16_f32 v144, v144, v145
	v_cvt_pk_bf16_f32 v149, v48, v49
	v_cndmask_b32_e64 v32, 0, v32, s[0:1]
	v_cmp_le_u32_e64 s[0:1], v197, v119
	v_mov_b64_e32 v[132:133], s[42:43]
	v_mov_b64_e32 v[130:131], s[40:41]
	v_or_b32_e32 v34, 48, v120
	v_bfe_u32 v35, v199, 1, 5
	v_mul_u32_u24_e32 v35, 0x90, v35
	s_waitcnt vmcnt(15)
	v_lshlrev_b32_e32 v94, 16, v54
	v_and_b32_e32 v95, 0xffff0000, v54
	v_lshlrev_b32_e32 v96, 16, v55
	v_and_b32_e32 v97, 0xffff0000, v55
	s_waitcnt vmcnt(14)
	v_lshlrev_b32_e32 v82, 16, v58
	s_waitcnt vmcnt(13)
	v_lshlrev_b32_e32 v86, 16, v50
	v_and_b32_e32 v87, 0xffff0000, v50
	v_lshlrev_b32_e32 v88, 16, v51
	s_waitcnt vmcnt(10)
	v_lshlrev_b32_e32 v66, 16, v18
	v_and_b32_e32 v67, 0xffff0000, v18
	v_mul_u32_u24_e32 v18, 0x90, v119
	v_add3_u32 v223, s48, v0, v18
	v_and_b32_e32 v89, 0xffff0000, v51
	v_lshlrev_b32_e32 v90, 16, v52
	v_and_b32_e32 v91, 0xffff0000, v52
	v_lshlrev_b32_e32 v92, 16, v53
	v_and_b32_e32 v93, 0xffff0000, v53
	v_lshlrev_b32_e32 v68, 16, v19
	v_and_b32_e32 v69, 0xffff0000, v19
	s_waitcnt vmcnt(7)
	v_lshlrev_b32_e32 v50, 16, v20
	v_and_b32_e32 v51, 0xffff0000, v20
	v_lshlrev_b32_e32 v52, 16, v21
	v_and_b32_e32 v53, 0xffff0000, v21
	ds_read_b128 v[18:21], v223
	ds_read_b128 v[26:29], v223 offset:4608
	v_and_b32_e32 v83, 0xffff0000, v58
	v_lshlrev_b32_e32 v84, 16, v59
	v_and_b32_e32 v85, 0xffff0000, v59
	v_lshlrev_b32_e32 v70, 16, v56
	v_and_b32_e32 v71, 0xffff0000, v56
	v_lshlrev_b32_e32 v72, 16, v57
	v_and_b32_e32 v73, 0xffff0000, v57
	v_lshlrev_b32_e32 v74, 16, v62
	v_and_b32_e32 v75, 0xffff0000, v62
	v_lshlrev_b32_e32 v76, 16, v63
	v_and_b32_e32 v77, 0xffff0000, v63
	v_lshlrev_b32_e32 v78, 16, v60
	v_and_b32_e32 v79, 0xffff0000, v60
	v_lshlrev_b32_e32 v80, 16, v61
	v_and_b32_e32 v81, 0xffff0000, v61
	s_waitcnt vmcnt(3)
	v_lshlrev_b32_e32 v54, 16, v22
	v_and_b32_e32 v55, 0xffff0000, v22
	v_lshlrev_b32_e32 v56, 16, v23
	v_and_b32_e32 v57, 0xffff0000, v23
	v_lshlrev_b32_e32 v58, 16, v24
	v_and_b32_e32 v59, 0xffff0000, v24
	v_lshlrev_b32_e32 v60, 16, v25
	v_and_b32_e32 v61, 0xffff0000, v25
	ds_read_b128 v[22:25], v223 offset:32
	s_waitcnt lgkmcnt(2)
	v_mfma_f32_32x32x16_bf16 v[82:97], v[18:21], v[134:137], v[82:97]
	s_waitcnt vmcnt(2)
	v_lshlrev_b32_e32 v62, 16, v64
	v_and_b32_e32 v63, 0xffff0000, v64
	v_lshlrev_b32_e32 v64, 16, v65
	v_and_b32_e32 v65, 0xffff0000, v65
	v_lshlrev_b32_e32 v98, 16, v100
	v_and_b32_e32 v99, 0xffff0000, v100
	v_lshlrev_b32_e32 v100, 16, v101
	v_mfma_f32_32x32x16_bf16 v[66:81], v[18:21], v[138:141], v[66:81]
	v_and_b32_e32 v101, 0xffff0000, v101
	v_lshlrev_b32_e32 v102, 16, v104
	v_and_b32_e32 v103, 0xffff0000, v104
	v_lshlrev_b32_e32 v104, 16, v105
	v_and_b32_e32 v105, 0xffff0000, v105
	s_waitcnt vmcnt(1)
; __device__ __forceinline__ void ph_rwkv_chunk(const Params& p, int l, LAS unsigned char* lds, const int wvid) {
;     ...
;             R2_MM_LP(G, X, ABR);
;             R2_STORE_T(GTg, G, true, 1.0f);
;         }
;         {
;             bf16x8 Bp[4][2]; R2_RAW(Y, BTg); R2_PSEUDO_L(Bp, Y);
	v_lshlrev_b32_e32 v106, 16, v108
	v_and_b32_e32 v107, 0xffff0000, v108
	v_lshlrev_b32_e32 v108, 16, v109
	v_and_b32_e32 v109, 0xffff0000, v109
	s_waitcnt vmcnt(0)
	v_lshlrev_b32_e32 v110, 16, v30
	v_and_b32_e32 v111, 0xffff0000, v30
	v_lshlrev_b32_e32 v112, 16, v31
	v_and_b32_e32 v113, 0xffff0000, v31
	v_cndmask_b32_e64 v0, 0, v33, s[0:1]
	s_waitcnt lgkmcnt(1)
	v_mfma_f32_32x32x16_bf16 v[50:65], v[26:29], v[134:137], v[50:65]
	ds_read_b128 v[18:21], v223 offset:4640
	v_cvt_pk_bf16_f32 v145, v32, v0
	v_or_b32_e32 v0, 32, v119
	s_add_u32 s0, s63, s38
	s_addc_u32 s1, s80, s39
	v_mfma_f32_32x32x16_bf16 v[98:113], v[26:29], v[138:141], v[98:113]
	v_or_b32_e32 v26, 33, v120
	v_or_b32_e32 v27, 34, v120
	v_cndmask_b32_e64 v29, v2, 0, vcc
	v_cmp_le_u32_e32 vcc, v26, v0
	v_or_b32_e32 v28, 43, v120
	s_nop 0
	v_cndmask_b32_e32 v26, 0, v3, vcc
	s_waitcnt lgkmcnt(1)
	v_mfma_f32_32x32x16_bf16 v[82:97], v[22:25], v[142:145], v[82:97]
	v_cmp_le_u32_e32 vcc, v27, v0
	v_cvt_pk_bf16_f32 v170, v29, v26
	s_nop 0
	v_cndmask_b32_e32 v27, 0, v4, vcc
	v_mfma_f32_32x32x16_bf16 v[66:81], v[22:25], v[146:149], v[66:81]
	v_or_b32_e32 v22, 35, v120
	v_cmp_le_u32_e32 vcc, v22, v0
	v_or_b32_e32 v23, 40, v120
	v_or_b32_e32 v24, 41, v120
	v_cndmask_b32_e32 v22, 0, v5, vcc
	ds_read_b128 v[2:5], v223 offset:64
	v_cmp_le_u32_e32 vcc, v23, v0
	v_or_b32_e32 v25, 42, v120
	s_waitcnt lgkmcnt(1)
	v_mfma_f32_32x32x16_bf16 v[50:65], v[18:21], v[142:145], v[50:65]
	v_cndmask_b32_e32 v6, 0, v6, vcc
	v_cmp_le_u32_e32 vcc, v24, v0
	v_cvt_pk_bf16_f32 v171, v27, v22
	v_or_b32_e32 v22, 57, v120
	v_cndmask_b32_e32 v7, 0, v7, vcc
	v_cmp_le_u32_e32 vcc, v25, v0
	v_cvt_pk_bf16_f32 v172, v6, v7
	v_mfma_f32_32x32x16_bf16 v[98:113], v[18:21], v[146:149], v[98:113]
	v_cndmask_b32_e32 v8, 0, v8, vcc
	v_cmp_le_u32_e32 vcc, v28, v0
	v_or_b32_e32 v18, 49, v120
	v_or_b32_e32 v19, 50, v120
	v_cndmask_b32_e32 v9, 0, v9, vcc
	v_cvt_pk_bf16_f32 v173, v8, v9
	v_cmp_le_u32_e32 vcc, v34, v0
	s_waitcnt lgkmcnt(0)
	v_mfma_f32_32x32x16_bf16 v[82:97], v[2:5], v[130:133], v[82:97]
	v_or_b32_e32 v20, 51, v120
	v_cndmask_b32_e32 v10, 0, v10, vcc
	v_cmp_le_u32_e32 vcc, v18, v0
	v_or_b32_e32 v21, 56, v120
	v_or_b32_e32 v23, 58, v120
	v_cndmask_b32_e32 v11, 0, v11, vcc
	v_cmp_le_u32_e32 vcc, v19, v0
	v_mfma_f32_32x32x16_bf16 v[66:81], v[2:5], v[170:173], v[66:81]
	ds_read_b128 v[2:5], v223 offset:4672
	ds_read_b128 v[6:9], v223 offset:96
	v_or_b32_e32 v24, 59, v120
	v_cvt_pk_bf16_f32 v174, v10, v11
	s_waitcnt lgkmcnt(1)
	v_mfma_f32_32x32x16_bf16 v[50:65], v[2:5], v[130:133], v[50:65]
	v_mfma_f32_32x32x16_bf16 v[98:113], v[2:5], v[170:173], v[98:113]
	v_cndmask_b32_e32 v2, 0, v12, vcc
	v_cmp_le_u32_e32 vcc, v20, v0
	s_nop 1
	v_cndmask_b32_e32 v3, 0, v13, vcc
	v_cmp_le_u32_e32 vcc, v21, v0
	v_cvt_pk_bf16_f32 v175, v2, v3
	s_waitcnt lgkmcnt(0)
	v_mfma_f32_32x32x16_bf16 v[82:97], v[6:9], v[130:133], v[82:97]
	v_cndmask_b32_e32 v4, 0, v14, vcc
	v_cmp_le_u32_e32 vcc, v22, v0
	s_nop 1
	v_cndmask_b32_e32 v5, 0, v15, vcc
	v_cvt_pk_bf16_f32 v176, v4, v5
	ds_read_b128 v[2:5], v223 offset:4704
	v_cmp_le_u32_e32 vcc, v23, v0
	s_waitcnt lgkmcnt(0)
	v_mfma_f32_32x32x16_bf16 v[50:65], v[2:5], v[130:133], v[50:65]
	v_cndmask_b32_e32 v12, 0, v16, vcc
	v_cmp_le_u32_e32 vcc, v24, v0
	s_nop 1
	v_cndmask_b32_e32 v0, 0, v17, vcc
	v_cvt_pk_bf16_f32 v177, v12, v0
	v_and_b32_e32 v0, 63, v199
	v_lshlrev_b32_e32 v0, 4, v0
	v_mfma_f32_32x32x16_bf16 v[66:81], v[6:9], v[174:177], v[66:81]
	v_lshl_add_u64 v[18:19], s[70:71], 0, v[0:1]
	v_add_co_u32_e32 v30, vcc, s44, v18
	s_nop 1
	v_addc_co_u32_e32 v31, vcc, 0, v19, vcc
	v_cmp_eq_u32_e32 vcc, v120, v119
	v_mfma_f32_32x32x16_bf16 v[98:113], v[2:5], v[174:177], v[98:113]
	v_cvt_pk_bf16_f32 v2, v82, v83
	v_cvt_pk_bf16_f32 v3, v84, v85
	v_cvt_pk_bf16_f32 v4, v86, v87
	v_cvt_pk_bf16_f32 v5, v88, v89
	global_store_dwordx4 v114, v[2:5], s[0:1]
	s_nop 1
	v_cvt_pk_bf16_f32 v2, v90, v91
	v_cvt_pk_bf16_f32 v3, v92, v93
	v_cvt_pk_bf16_f32 v4, v94, v95
	v_cvt_pk_bf16_f32 v5, v96, v97
	global_store_dwordx4 v114, v[2:5], s[0:1] offset:2048
	s_nop 1
	v_cvt_pk_bf16_f32 v2, v66, v67
	v_cvt_pk_bf16_f32 v3, v68, v69
	v_cvt_pk_bf16_f32 v4, v70, v71
	v_cvt_pk_bf16_f32 v5, v72, v73
	global_store_dwordx4 v114, v[2:5], s[0:1] offset:1024
	s_nop 1
	v_cvt_pk_bf16_f32 v2, v74, v75
	v_cvt_pk_bf16_f32 v3, v76, v77
	v_cvt_pk_bf16_f32 v4, v78, v79
	v_cvt_pk_bf16_f32 v5, v80, v81
	global_store_dwordx4 v114, v[2:5], s[0:1] offset:3072
	s_nop 1
	v_cvt_pk_bf16_f32 v2, v50, v51
	v_cvt_pk_bf16_f32 v3, v52, v53
	v_cvt_pk_bf16_f32 v4, v54, v55
	v_cvt_pk_bf16_f32 v5, v56, v57
	global_store_dwordx4 v117, v[2:5], s[0:1]
	s_nop 1
	v_cvt_pk_bf16_f32 v2, v58, v59
	v_cvt_pk_bf16_f32 v3, v60, v61
	v_cvt_pk_bf16_f32 v4, v62, v63
	v_cvt_pk_bf16_f32 v5, v64, v65
	global_store_dwordx4 v118, v[2:5], s[0:1]
	s_nop 1
	v_cvt_pk_bf16_f32 v2, v98, v99
	v_cvt_pk_bf16_f32 v3, v100, v101
	v_cvt_pk_bf16_f32 v4, v102, v103
	v_cvt_pk_bf16_f32 v5, v104, v105
	global_store_dwordx4 v115, v[2:5], s[0:1]
	s_nop 1
	v_cvt_pk_bf16_f32 v2, v106, v107
	v_cvt_pk_bf16_f32 v3, v108, v109
	v_cvt_pk_bf16_f32 v4, v110, v111
	v_cvt_pk_bf16_f32 v5, v112, v113
	global_store_dwordx4 v116, v[2:5], s[0:1]
	global_load_dwordx4 v[2:5], v0, s[70:71]
	s_nop 0
	global_load_dwordx4 v[6:9], v0, s[70:71] offset:1024
	global_load_dwordx4 v[10:13], v0, s[70:71] offset:2048
	global_load_dwordx4 v[14:17], v0, s[70:71] offset:3072
	global_load_dwordx4 v[18:21], v[30:31], off
	global_load_dwordx4 v[22:25], v[30:31], off offset:1024
	global_load_dwordx4 v[26:29], v[30:31], off offset:2048
	s_nop 0
	global_load_dwordx4 v[30:33], v[30:31], off offset:3072
	v_lshlrev_b32_e32 v0, 4, v199
	v_and_b32_e32 v0, 16, v0
	v_add3_u32 v0, s48, v35, v0
	s_waitcnt vmcnt(7)
; #define R2_ZERO(M) do { _Pragma("unroll") for (int _a = 0; _a < 2; ++_a) _Pragma("unroll") for (int _b = 0; _b < 2; ++_b) _Pragma("unroll") for (int _r = 0; _r < 16; ++_r) M[_a][_b][_r] = 0.f; } while (0)
; __device__ __forceinline__ void ph_rwkv_chunk(const Params& p, int l, LAS unsigned char* lds, const int wvid) {
;     ...
;             bf16x8 Bp[4][2]; R2_RAW(Y, BTg); R2_PSEUDO_L(Bp, Y);
;             M64 P; R2_ZERO(P); R2_MM_LP(P, X, Bp);
; #pragma unroll
;             for (int rb = 0; rb < 2; ++rb)
; #pragma unroll
;                 for (int r = 0; r < 16; ++r) if (((r & 3) + 8 * (r >> 2) + 4 * hi) == l31) P[rb][rb][r] += 1.f;
	ds_write_b128 v0, v[2:5] offset:9216
	s_waitcnt vmcnt(6)
	ds_write_b128 v0, v[6:9] offset:13824
	s_waitcnt vmcnt(5)
	ds_write_b128 v0, v[10:13] offset:9248
	s_waitcnt vmcnt(4)
	ds_write_b128 v0, v[14:17] offset:13856
	s_waitcnt vmcnt(3)
	ds_write_b128 v0, v[18:21] offset:9280
	s_waitcnt vmcnt(2)
	ds_write_b128 v0, v[22:25] offset:13888
	s_waitcnt vmcnt(1)
	ds_write_b128 v0, v[26:29] offset:9312
	s_waitcnt vmcnt(0)
	ds_write_b128 v0, v[30:33] offset:13920
	v_lshlrev_b32_e32 v0, 1, v119
	v_mul_u32_u24_e32 v2, 0x240, v198
	v_mul_u32_u24_e32 v3, 0x90, v121
	v_mul_u32_u24_e32 v4, 0x90, v34
	v_add3_u32 v2, s48, v2, v0
	v_add3_u32 v3, s48, v3, v0
	v_add3_u32 v0, s48, v4, v0
	ds_read_u16 v6, v2 offset:9216
	ds_read_u16 v7, v2 offset:9360
	ds_read_u16 v9, v2 offset:10656
	ds_read_u16 v10, v2 offset:10800
	ds_read_u16 v11, v2 offset:10864
	ds_read_u16 v12, v2 offset:10720
	ds_read_u16 v13, v2 offset:9424
	ds_read_u16 v14, v2 offset:9280
	ds_read_u16 v8, v3 offset:9216
	ds_read_u16 v15, v3 offset:9360
	ds_read_u16 v16, v3 offset:10080
	ds_read_u16 v17, v3 offset:10224
	ds_read_u16 v18, v3 offset:10288
	ds_read_u16 v19, v3 offset:10144
	ds_read_u16 v20, v3 offset:9424
	ds_read_u16 v21, v3 offset:9280
	ds_read_u16 v70, v3 offset:11232
	ds_read_u16 v71, v3 offset:11376
	ds_read_u16 v74, v3 offset:11440
	ds_read_u16 v78, v0 offset:9216
	ds_read_u16 v79, v0 offset:9360
	ds_read_u16 v80, v0 offset:9424
	ds_read_u16 v0, v0 offset:9280
	ds_read_u16 v75, v3 offset:11296
	ds_read_u16 v72, v2 offset:11808
	ds_read_u16 v73, v2 offset:11952
	ds_read_u16 v76, v2 offset:12672
	ds_read_u16 v77, v2 offset:12816
	ds_read_u16 v81, v2 offset:12880
	ds_read_u16 v82, v2 offset:12736
	ds_read_u16 v83, v2 offset:12016
	ds_read_u16 v84, v2 offset:11872
	ds_read_u16 v85, v2 offset:12960
	ds_read_u16 v86, v2 offset:13104
	ds_read_u16 v87, v2 offset:13168
	ds_read_u16 v88, v2 offset:13824
	ds_read_u16 v89, v2 offset:13968
	ds_read_u16 v90, v2 offset:14032
	ds_read_u16 v91, v2 offset:13888
	ds_read_u16 v92, v2 offset:13024
	ds_read_u16 v93, v2 offset:14112
	ds_read_u16 v94, v2 offset:14256
	ds_read_u16 v95, v2 offset:14976
	ds_read_u16 v96, v2 offset:15120
	ds_read_u16 v97, v2 offset:15184
	ds_read_u16 v98, v2 offset:15040
	ds_read_u16 v99, v2 offset:14320
	ds_read_u16 v100, v2 offset:14176
	ds_read_u16 v101, v2 offset:15264
	ds_read_u16 v102, v2 offset:15408
	ds_read_u16 v103, v2 offset:15472
	ds_read_u16 v104, v2 offset:16416
	ds_read_u16 v105, v2 offset:16560
	ds_read_u16 v106, v2 offset:16624
	ds_read_u16 v107, v2 offset:16480
	ds_read_u16 v108, v2 offset:15328
	ds_read_u16 v109, v2 offset:17280
	ds_read_u16 v110, v2 offset:17424
	ds_read_u16 v111, v2 offset:17568
	ds_read_u16 v112, v2 offset:17712
	ds_read_u16 v113, v2 offset:17776
	ds_read_u16 v198, v2 offset:17632
	ds_read_u16 v199, v2 offset:17488
	ds_read_u16 v200, v2 offset:17344
	ds_read_b128 v[2:5], v223
	ds_read_b128 v[66:69], v223 offset:32
	s_waitcnt lgkmcnt(14)
	v_lshl_or_b32 v6, v7, 16, v6
	v_lshl_or_b32 v7, v15, 16, v8
	v_lshl_or_b32 v8, v17, 16, v16
	v_lshl_or_b32 v9, v10, 16, v9
	v_lshl_or_b32 v34, v13, 16, v14
	v_lshl_or_b32 v35, v20, 16, v21
	v_lshl_or_b32 v36, v18, 16, v19
	v_lshl_or_b32 v37, v11, 16, v12
	s_waitcnt lgkmcnt(1)
	v_mfma_f32_32x32x16_bf16 v[50:65], v[2:5], v[6:9], 0
	ds_read_b128 v[38:41], v223 offset:4608
	v_lshl_or_b32 v70, v71, 16, v70
	v_lshl_or_b32 v71, v73, 16, v72
	v_lshl_or_b32 v72, v77, 16, v76
	v_lshl_or_b32 v73, v86, 16, v85
	v_lshl_or_b32 v74, v74, 16, v75
	v_lshl_or_b32 v75, v83, 16, v84
	v_mfma_f32_32x32x16_bf16 v[18:33], v[2:5], v[34:37], 0
	v_lshl_or_b32 v76, v81, 16, v82
	v_lshl_or_b32 v77, v87, 16, v92
	s_waitcnt lgkmcnt(1)
	v_mfma_f32_32x32x16_bf16 v[50:65], v[66:69], v[70:73], v[50:65]
	v_mfma_f32_32x32x16_bf16 v[18:33], v[66:69], v[74:77], v[18:33]
	ds_read_b128 v[66:69], v223 offset:4640
	s_waitcnt lgkmcnt(1)
	v_mfma_f32_32x32x16_bf16 v[2:17], v[38:41], v[6:9], 0
	v_mfma_f32_32x32x16_bf16 v[34:49], v[38:41], v[34:37], 0
	s_waitcnt lgkmcnt(0)
	v_mfma_f32_32x32x16_bf16 v[2:17], v[66:69], v[70:73], v[2:17]
	v_lshl_or_b32 v70, v89, 16, v88
	v_lshl_or_b32 v71, v94, 16, v93
	v_lshl_or_b32 v72, v96, 16, v95
	v_lshl_or_b32 v73, v102, 16, v101
	v_mfma_f32_32x32x16_bf16 v[34:49], v[66:69], v[74:77], v[34:49]
	ds_read_b128 v[66:69], v223 offset:64
	v_lshl_or_b32 v74, v90, 16, v91
	v_lshl_or_b32 v75, v99, 16, v100
	v_lshl_or_b32 v76, v97, 16, v98
	v_lshl_or_b32 v77, v103, 16, v108
	s_waitcnt lgkmcnt(0)
	v_mfma_f32_32x32x16_bf16 v[50:65], v[66:69], v[70:73], v[50:65]
	v_mfma_f32_32x32x16_bf16 v[18:33], v[66:69], v[74:77], v[18:33]
	ds_read_b128 v[66:69], v223 offset:4672
	s_waitcnt lgkmcnt(0)
	v_mfma_f32_32x32x16_bf16 v[2:17], v[66:69], v[70:73], v[2:17]
	v_lshl_or_b32 v70, v79, 16, v78
	v_lshl_or_b32 v71, v105, 16, v104
	v_lshl_or_b32 v72, v110, 16, v109
	v_lshl_or_b32 v73, v112, 16, v111
	v_mfma_f32_32x32x16_bf16 v[34:49], v[66:69], v[74:77], v[34:49]
	ds_read_b128 v[66:69], v223 offset:96
	v_lshl_or_b32 v74, v80, 16, v0
	v_lshl_or_b32 v75, v106, 16, v107
	v_lshl_or_b32 v76, v199, 16, v200
	v_lshl_or_b32 v77, v113, 16, v198
	v_or_b32_e32 v0, 1, v120
	v_cmp_eq_u32_e64 s[0:1], v0, v119
	s_waitcnt lgkmcnt(0)
	v_mfma_f32_32x32x16_bf16 v[50:65], v[66:69], v[70:73], v[50:65]
	v_mfma_f32_32x32x16_bf16 v[18:33], v[66:69], v[74:77], v[18:33]
	ds_read_b128 v[66:69], v223 offset:4704
	s_nop 9
	v_add_f32_e32 v0, 1.0, v52
	v_cndmask_b32_e64 v52, v52, v0, s[2:3]
	v_add_f32_e32 v0, 1.0, v53
	v_cndmask_b32_e64 v53, v53, v0, s[4:5]
	v_add_f32_e32 v0, 1.0, v54
	v_cndmask_b32_e64 v54, v54, v0, s[6:7]
	v_add_f32_e32 v0, 1.0, v55
	v_cndmask_b32_e64 v55, v55, v0, s[8:9]
	v_add_f32_e32 v0, 1.0, v56
	v_cndmask_b32_e64 v56, v56, v0, s[10:11]
	v_add_f32_e32 v0, 1.0, v57
	s_waitcnt lgkmcnt(0)
; #define R2_ZERO(M) do { _Pragma("unroll") for (int _a = 0; _a < 2; ++_a) _Pragma("unroll") for (int _b = 0; _b < 2; ++_b) _Pragma("unroll") for (int _r = 0; _r < 16; ++_r) M[_a][_b][_r] = 0.f; } while (0)
; #define R2_MASK(M, STRICT) do { _Pragma("unroll") for (int _rb = 0; _rb < 2; ++_rb) _Pragma("unroll") for (int _cb = 0; _cb < 2; ++_cb) _Pragma("unroll") for (int _r = 0; _r < 16; ++_r) { \
;         const int _row = 32 * _rb + (_r & 3) + 8 * (_r >> 2) + 4 * hi, _col = 32 * _cb + l31; if (STRICT ? !(_row < _col) : !(_row <= _col)) M[_rb][_cb][_r] = 0.f; } } while (0)
; #define R2_RELANE() do { lane = lt_tid(wvid) & 63; l31 = lane & 31; hi = lane >> 5; } while (0)
; __device__ __forceinline__ void ph_rwkv_chunk(const Params& p, int l, LAS unsigned char* lds, const int wvid) {
;     ...
; #pragma unroll
;             for (int rb = 0; rb < 2; ++rb)
; #pragma unroll
;                 for (int r = 0; r < 16; ++r) if (((r & 3) + 8 * (r >> 2) + 4 * hi) == l31) P[rb][rb][r] += 1.f;
; #pragma unroll
;             for (int rb = 0; rb < 2; ++rb)
; #pragma unroll
;                 for (int r = 0; r < 16; ++r) { P[rb][0][r] *= gc0; P[rb][1][r] *= gc1; }
;             R2_STORE_T(PTg, P, true, 1.0f);
;         }
;         R2_RELANE();
;         bf16x8 Zpk[4][2];
;         {
;             M64 A; R2_ZERO(A); R2_MM_GG(A, KTg, ATg); R2_MASK(A, true);
	v_mfma_f32_32x32x16_bf16 v[34:49], v[66:69], v[74:77], v[34:49]
	v_cndmask_b32_e64 v57, v57, v0, s[16:17]
	v_add_f32_e32 v0, 1.0, v58
	v_cndmask_b32_e64 v58, v58, v0, s[18:19]
	v_add_f32_e32 v0, 1.0, v59
	v_cndmask_b32_e64 v59, v59, v0, s[20:21]
	v_add_f32_e32 v0, 1.0, v60
	v_cndmask_b32_e64 v60, v60, v0, s[22:23]
	v_add_f32_e32 v0, 1.0, v61
	v_cndmask_b32_e64 v61, v61, v0, s[24:25]
	v_add_f32_e32 v0, 1.0, v62
	v_cndmask_b32_e64 v62, v62, v0, s[26:27]
	v_add_f32_e32 v0, 1.0, v63
	v_cndmask_b32_e64 v63, v63, v0, s[28:29]
	v_add_f32_e32 v0, 1.0, v64
	v_cndmask_b32_e64 v64, v64, v0, s[30:31]
	v_add_f32_e32 v0, 1.0, v65
	v_cndmask_b32_e64 v65, v65, v0, s[34:35]
	v_add_f32_e32 v0, 1.0, v34
	v_cndmask_b32_e32 v34, v34, v0, vcc
	v_add_f32_e32 v0, 1.0, v35
	v_cndmask_b32_e64 v35, v35, v0, s[0:1]
	v_add_f32_e32 v0, 1.0, v36
	v_mfma_f32_32x32x16_bf16 v[2:17], v[66:69], v[70:73], v[2:17]
	v_cndmask_b32_e64 v36, v36, v0, s[2:3]
	v_add_f32_e32 v0, 1.0, v37
	v_cndmask_b32_e64 v37, v37, v0, s[4:5]
	v_add_f32_e32 v0, 1.0, v38
	v_cndmask_b32_e64 v38, v38, v0, s[6:7]
	v_add_f32_e32 v0, 1.0, v39
	v_cndmask_b32_e64 v39, v39, v0, s[8:9]
	v_add_f32_e32 v0, 1.0, v40
	v_add_f32_e32 v66, 1.0, v50
	v_cndmask_b32_e64 v40, v40, v0, s[10:11]
	v_add_f32_e32 v0, 1.0, v41
	v_cndmask_b32_e32 v50, v50, v66, vcc
	v_add_f32_e32 v66, 1.0, v51
	v_cndmask_b32_e64 v41, v41, v0, s[16:17]
	v_add_f32_e32 v0, 1.0, v42
	v_cndmask_b32_e64 v51, v51, v66, s[0:1]
	v_cndmask_b32_e64 v42, v42, v0, s[18:19]
	v_add_f32_e32 v0, 1.0, v43
	v_cndmask_b32_e64 v43, v43, v0, s[20:21]
	v_add_f32_e32 v0, 1.0, v44
	v_pk_mul_f32 v[50:51], v[192:193], v[50:51] op_sel_hi:[0,1]
	v_pk_mul_f32 v[52:53], v[192:193], v[52:53] op_sel_hi:[0,1]
	v_pk_mul_f32 v[54:55], v[192:193], v[54:55] op_sel_hi:[0,1]
	v_pk_mul_f32 v[56:57], v[192:193], v[56:57] op_sel_hi:[0,1]
	v_cndmask_b32_e64 v44, v44, v0, s[22:23]
	v_add_f32_e32 v0, 1.0, v45
	v_pk_mul_f32 v[58:59], v[192:193], v[58:59] op_sel_hi:[0,1]
	v_pk_mul_f32 v[60:61], v[192:193], v[60:61] op_sel_hi:[0,1]
	v_pk_mul_f32 v[62:63], v[192:193], v[62:63] op_sel_hi:[0,1]
	v_pk_mul_f32 v[64:65], v[192:193], v[64:65] op_sel_hi:[0,1]
	v_pk_mul_f32 v[66:67], v[192:193], v[2:3] op_sel_hi:[0,1]
	v_pk_mul_f32 v[68:69], v[192:193], v[4:5] op_sel_hi:[0,1]
	v_cvt_pk_bf16_f32 v2, v50, v51
	v_cvt_pk_bf16_f32 v3, v52, v53
	v_cvt_pk_bf16_f32 v4, v54, v55
	v_cvt_pk_bf16_f32 v5, v56, v57
	v_cndmask_b32_e64 v45, v45, v0, s[24:25]
	v_add_f32_e32 v0, 1.0, v46
	v_pk_mul_f32 v[18:19], v[190:191], v[18:19] op_sel_hi:[0,1]
	v_pk_mul_f32 v[20:21], v[190:191], v[20:21] op_sel_hi:[0,1]
	v_pk_mul_f32 v[22:23], v[190:191], v[22:23] op_sel_hi:[0,1]
	v_pk_mul_f32 v[24:25], v[190:191], v[24:25] op_sel_hi:[0,1]
	global_store_dwordx4 v114, v[2:5], s[72:73]
	v_cndmask_b32_e64 v46, v46, v0, s[26:27]
	v_add_f32_e32 v0, 1.0, v47
	v_cvt_pk_bf16_f32 v2, v58, v59
	v_cvt_pk_bf16_f32 v3, v60, v61
	v_cvt_pk_bf16_f32 v4, v62, v63
	v_cvt_pk_bf16_f32 v5, v64, v65
	v_pk_mul_f32 v[26:27], v[190:191], v[26:27] op_sel_hi:[0,1]
	v_pk_mul_f32 v[28:29], v[190:191], v[28:29] op_sel_hi:[0,1]
	v_pk_mul_f32 v[30:31], v[190:191], v[30:31] op_sel_hi:[0,1]
	v_pk_mul_f32 v[32:33], v[190:191], v[32:33] op_sel_hi:[0,1]
	global_store_dwordx4 v114, v[2:5], s[72:73] offset:2048
	v_cndmask_b32_e64 v47, v47, v0, s[28:29]
	v_add_f32_e32 v0, 1.0, v48
	v_cvt_pk_bf16_f32 v2, v18, v19
	v_cvt_pk_bf16_f32 v3, v20, v21
	v_cvt_pk_bf16_f32 v4, v22, v23
	v_cvt_pk_bf16_f32 v5, v24, v25
	v_pk_mul_f32 v[6:7], v[192:193], v[6:7] op_sel_hi:[0,1]
	v_pk_mul_f32 v[8:9], v[192:193], v[8:9] op_sel_hi:[0,1]
	global_store_dwordx4 v114, v[2:5], s[72:73] offset:1024
	v_cndmask_b32_e64 v48, v48, v0, s[30:31]
	v_add_f32_e32 v0, 1.0, v49
	v_cvt_pk_bf16_f32 v2, v26, v27
	v_cvt_pk_bf16_f32 v3, v28, v29
	v_cvt_pk_bf16_f32 v4, v30, v31
	v_cvt_pk_bf16_f32 v5, v32, v33
	v_pk_mul_f32 v[10:11], v[192:193], v[10:11] op_sel_hi:[0,1]
	v_pk_mul_f32 v[12:13], v[192:193], v[12:13] op_sel_hi:[0,1]
	v_pk_mul_f32 v[14:15], v[192:193], v[14:15] op_sel_hi:[0,1]
	v_pk_mul_f32 v[16:17], v[192:193], v[16:17] op_sel_hi:[0,1]
	global_store_dwordx4 v114, v[2:5], s[72:73] offset:3072
	v_cndmask_b32_e64 v49, v49, v0, s[34:35]
	v_pk_mul_f32 v[34:35], v[190:191], v[34:35] op_sel_hi:[0,1]
	v_cvt_pk_bf16_f32 v2, v66, v67
	v_cvt_pk_bf16_f32 v3, v68, v69
	v_cvt_pk_bf16_f32 v4, v6, v7
	v_cvt_pk_bf16_f32 v5, v8, v9
	v_pk_mul_f32 v[36:37], v[190:191], v[36:37] op_sel_hi:[0,1]
	v_pk_mul_f32 v[38:39], v[190:191], v[38:39] op_sel_hi:[0,1]
	v_pk_mul_f32 v[40:41], v[190:191], v[40:41] op_sel_hi:[0,1]
	global_store_dwordx4 v117, v[2:5], s[72:73]
	v_pk_mul_f32 v[42:43], v[190:191], v[42:43] op_sel_hi:[0,1]
	v_pk_mul_f32 v[44:45], v[190:191], v[44:45] op_sel_hi:[0,1]
	v_cvt_pk_bf16_f32 v2, v10, v11
	v_cvt_pk_bf16_f32 v3, v12, v13
	v_cvt_pk_bf16_f32 v4, v14, v15
	v_cvt_pk_bf16_f32 v5, v16, v17
	v_pk_mul_f32 v[46:47], v[190:191], v[46:47] op_sel_hi:[0,1]
	v_pk_mul_f32 v[48:49], v[190:191], v[48:49] op_sel_hi:[0,1]
	global_store_dwordx4 v118, v[2:5], s[72:73]
	s_add_u32 s34, s93, s38
	s_addc_u32 s35, s62, s39
	v_cvt_pk_bf16_f32 v2, v34, v35
	v_cvt_pk_bf16_f32 v3, v36, v37
	v_cvt_pk_bf16_f32 v4, v38, v39
	v_cvt_pk_bf16_f32 v5, v40, v41
	global_store_dwordx4 v115, v[2:5], s[72:73]
	s_add_u32 s42, s95, s38
	s_addc_u32 s43, s51, s39
	v_cvt_pk_bf16_f32 v2, v42, v43
	v_cvt_pk_bf16_f32 v3, v44, v45
	v_cvt_pk_bf16_f32 v4, v46, v47
	v_cvt_pk_bf16_f32 v5, v48, v49
	global_store_dwordx4 v116, v[2:5], s[72:73]
	v_mbcnt_lo_u32_b32 v66, -1, 0
	v_mbcnt_hi_u32_b32 v66, -1, v66
	s_nop 0
	v_bfe_u32 v62, v66, 5, 1
	v_and_b32_e32 v0, 31, v66
	v_lshlrev_b32_e32 v63, 4, v62
	v_lshl_or_b32 v64, v0, 5, v63
	v_or_b32_e32 v196, 0x1000, v64
	v_or_b32_e32 v197, 0x1400, v64
	v_or_b32_e32 v198, 0x1800, v64
	v_or_b32_e32 v199, 0x1c00, v64
	global_load_dwordx4 v[68:71], v64, s[36:37]
	global_load_dwordx4 v[72:75], v64, s[86:87]
	global_load_dwordx4 v[76:79], v64, s[86:87] offset:1024
	global_load_dwordx4 v[80:83], v64, s[36:37] offset:1024
	global_load_dwordx4 v[84:87], v64, s[36:37] offset:2048
	global_load_dwordx4 v[88:91], v64, s[86:87] offset:2048
	global_load_dwordx4 v[92:95], v196, s[36:37]
	global_load_dwordx4 v[96:99], v64, s[86:87] offset:3072
	global_load_dwordx4 v[100:103], v64, s[36:37] offset:3072
	global_load_dwordx4 v[104:107], v196, s[86:87]
	global_load_dwordx4 v[108:111], v197, s[86:87]
	global_load_dwordx4 v[112:115], v197, s[36:37]
	global_load_dwordx4 v[116:119], v198, s[36:37]
	global_load_dwordx4 v[120:123], v198, s[86:87]
	global_load_dwordx4 v[124:127], v199, s[86:87]
	global_load_dwordx4 v[232:235], v199, s[36:37]
	s_waitcnt vmcnt(4)
; #define R2_ZERO(M) do { _Pragma("unroll") for (int _a = 0; _a < 2; ++_a) _Pragma("unroll") for (int _b = 0; _b < 2; ++_b) _Pragma("unroll") for (int _r = 0; _r < 16; ++_r) M[_a][_b][_r] = 0.f; } while (0)
; #define R2_MASK(M, STRICT) do { _Pragma("unroll") for (int _rb = 0; _rb < 2; ++_rb) _Pragma("unroll") for (int _cb = 0; _cb < 2; ++_cb) _Pragma("unroll") for (int _r = 0; _r < 16; ++_r) { \
;         const int _row = 32 * _rb + (_r & 3) + 8 * (_r >> 2) + 4 * hi, _col = 32 * _cb + l31; if (STRICT ? !(_row < _col) : !(_row <= _col)) M[_rb][_cb][_r] = 0.f; } } while (0)
; __device__ __forceinline__ void ph_rwkv_chunk(const Params& p, int l, LAS unsigned char* lds, const int wvid) {
;     ...
;             M64 A; R2_ZERO(A); R2_MM_GG(A, KTg, ATg); R2_MASK(A, true);
;             asm volatile("" ::: "memory");
;             R2_TO_LDS(X, A);
	v_mfma_f32_32x32x16_bf16 v[34:49], v[68:71], v[72:75], 0
	v_or_b32_e32 v65, 0x1000, v64
	s_waitcnt vmcnt(1)
	v_mfma_f32_32x32x16_bf16 v[34:49], v[84:87], v[88:91], v[34:49]
	v_mfma_f32_32x32x16_bf16 v[2:17], v[68:71], v[76:79], 0
	s_waitcnt vmcnt(0)
	v_mfma_f32_32x32x16_bf16 v[2:17], v[84:87], v[96:99], v[2:17]
	v_mfma_f32_32x32x16_bf16 v[18:33], v[80:83], v[76:79], 0
	s_waitcnt vmcnt(0)
	v_mfma_f32_32x32x16_bf16 v[18:33], v[100:103], v[96:99], v[18:33]
	v_or_b32_e32 v54, 0x1400, v64
	v_or_b32_e32 v65, 0x1800, v64
	s_waitcnt vmcnt(0)
	v_mfma_f32_32x32x16_bf16 v[34:49], v[92:95], v[104:107], v[34:49]
	s_nop 0
	s_waitcnt vmcnt(1)
	v_mfma_f32_32x32x16_bf16 v[2:17], v[92:95], v[108:111], v[2:17]
	s_waitcnt vmcnt(1)
	v_mfma_f32_32x32x16_bf16 v[18:33], v[112:115], v[108:111], v[18:33]
	v_or_b32_e32 v54, 0x1c00, v64
	s_waitcnt vmcnt(0)
	v_mfma_f32_32x32x16_bf16 v[34:49], v[116:119], v[120:123], v[34:49]
	s_nop 0
	s_waitcnt vmcnt(1)
	v_mfma_f32_32x32x16_bf16 v[2:17], v[116:119], v[124:127], v[2:17]
	s_nop 11
	v_cvt_pk_bf16_f32 v2, v2, v3
	s_waitcnt vmcnt(0)
	v_mfma_f32_32x32x16_bf16 v[18:33], v[232:235], v[124:127], v[18:33]
	v_lshlrev_b32_e32 v50, 2, v62
	v_or_b32_e32 v52, 3, v50
	v_cmp_lt_u32_e64 s[2:3], v52, v0
	v_or_b32_e32 v52, 8, v50
	v_cmp_lt_u32_e64 s[4:5], v52, v0
	v_or_b32_e32 v52, 9, v50
	v_cmp_lt_u32_e64 s[6:7], v52, v0
	v_or_b32_e32 v52, 10, v50
	v_cmp_lt_u32_e64 s[8:9], v52, v0
	v_or_b32_e32 v52, 11, v50
	v_cmp_lt_u32_e64 s[10:11], v52, v0
	v_or_b32_e32 v52, 16, v50
	v_cmp_lt_u32_e64 s[16:17], v52, v0
	v_or_b32_e32 v52, 17, v50
	v_cmp_lt_u32_e64 s[18:19], v52, v0
	v_or_b32_e32 v52, 18, v50
	v_cmp_lt_u32_e64 s[20:21], v52, v0
	v_or_b32_e32 v52, 19, v50
	v_cmp_lt_u32_e64 s[22:23], v52, v0
	v_or_b32_e32 v52, 24, v50
	v_cmp_lt_u32_e64 s[24:25], v52, v0
	v_or_b32_e32 v52, 25, v50
	v_cmp_lt_u32_e64 s[26:27], v52, v0
	v_or_b32_e32 v52, 26, v50
	v_cmp_lt_u32_e64 s[28:29], v52, v0
	v_or_b32_e32 v52, 27, v50
	v_cmp_lt_u32_e64 s[30:31], v52, v0
	s_or_b64 s[28:29], s[30:31], s[28:29]
	s_or_b64 s[26:27], s[28:29], s[26:27]
	s_or_b64 s[24:25], s[26:27], s[24:25]
	s_or_b64 s[22:23], s[24:25], s[22:23]
	s_or_b64 s[20:21], s[22:23], s[20:21]
	s_or_b64 s[18:19], s[20:21], s[18:19]
	s_or_b64 s[16:17], s[18:19], s[16:17]
	s_or_b64 s[10:11], s[16:17], s[10:11]
	s_or_b64 s[8:9], s[10:11], s[8:9]
	v_or_b32_e32 v51, 1, v50
	s_or_b64 s[6:7], s[8:9], s[6:7]
	v_cmp_lt_u32_e32 vcc, v51, v0
	v_or_b32_e32 v51, 2, v50
	s_or_b64 s[4:5], s[6:7], s[4:5]
	v_cmp_lt_u32_e64 s[0:1], v51, v0
	s_or_b64 s[2:3], s[4:5], s[2:3]
	s_or_b64 s[0:1], s[2:3], s[0:1]
	v_cndmask_b32_e64 v36, 0, v36, s[0:1]
	s_or_b64 vcc, s[0:1], vcc
	v_cmp_lt_u32_e64 s[0:1], v50, v0
	v_or_b32_e32 v52, 32, v0
	v_or_b32_e32 v53, 33, v50
	v_or_b32_e32 v54, 34, v50
	v_or_b32_e32 v55, 35, v50
	v_or_b32_e32 v56, 40, v50
	v_or_b32_e32 v57, 41, v50
	v_or_b32_e32 v58, 42, v50
	v_or_b32_e32 v59, 43, v50
	v_or_b32_e32 v60, 48, v50
	v_or_b32_e32 v61, 49, v50
	v_or_b32_e32 v64, 50, v50
	v_or_b32_e32 v65, 51, v50
	v_or_b32_e32 v67, 56, v50
	v_or_b32_e32 v68, 57, v50
	v_or_b32_e32 v69, 58, v50
	v_or_b32_e32 v50, 59, v50
	v_cndmask_b32_e64 v49, 0, v49, s[30:31]
	v_cndmask_b32_e64 v48, 0, v48, s[28:29]
	v_cmp_lt_u32_e64 s[28:29], v69, v52
	v_cmp_lt_u32_e64 s[30:31], v50, v52
	v_cndmask_b32_e64 v47, 0, v47, s[26:27]
	v_cmp_lt_u32_e64 s[26:27], v68, v52
	s_or_b64 s[28:29], s[30:31], s[28:29]
	v_cndmask_b32_e64 v46, 0, v46, s[24:25]
	v_cmp_lt_u32_e64 s[24:25], v67, v52
	s_or_b64 s[26:27], s[28:29], s[26:27]
	v_cndmask_b32_e64 v45, 0, v45, s[22:23]
	v_cmp_lt_u32_e64 s[22:23], v65, v52
	s_or_b64 s[24:25], s[26:27], s[24:25]
	v_cndmask_b32_e64 v44, 0, v44, s[20:21]
	v_cmp_lt_u32_e64 s[20:21], v64, v52
	s_or_b64 s[22:23], s[24:25], s[22:23]
	v_cndmask_b32_e64 v43, 0, v43, s[18:19]
	v_cmp_lt_u32_e64 s[18:19], v61, v52
	s_or_b64 s[20:21], s[22:23], s[20:21]
	v_cndmask_b32_e64 v42, 0, v42, s[16:17]
	v_cmp_lt_u32_e64 s[16:17], v60, v52
	s_or_b64 s[18:19], s[20:21], s[18:19]
	v_cndmask_b32_e64 v41, 0, v41, s[10:11]
	v_cmp_lt_u32_e64 s[10:11], v59, v52
	s_or_b64 s[16:17], s[18:19], s[16:17]
	v_cndmask_b32_e64 v40, 0, v40, s[8:9]
	v_cmp_lt_u32_e64 s[8:9], v58, v52
	s_or_b64 s[10:11], s[16:17], s[10:11]
	v_cndmask_b32_e64 v39, 0, v39, s[6:7]
	v_cmp_lt_u32_e64 s[6:7], v57, v52
	s_or_b64 s[8:9], s[10:11], s[8:9]
	v_cndmask_b32_e64 v38, 0, v38, s[4:5]
	v_cndmask_b32_e32 v35, 0, v35, vcc
	s_or_b64 vcc, vcc, s[0:1]
	v_cmp_lt_u32_e64 s[4:5], v56, v52
	s_or_b64 s[6:7], s[8:9], s[6:7]
	v_cndmask_b32_e64 v37, 0, v37, s[2:3]
	v_cndmask_b32_e64 v18, 0, v18, s[0:1]
	v_cndmask_b32_e32 v34, 0, v34, vcc
	v_cmp_lt_u32_e32 vcc, v53, v52
	v_cmp_lt_u32_e64 s[0:1], v54, v52
	v_cmp_lt_u32_e64 s[2:3], v55, v52
	s_or_b64 s[4:5], s[6:7], s[4:5]
	v_and_b32_e32 v50, 19, v66
	v_lshlrev_b32_e32 v52, 1, v66
	s_or_b64 s[2:3], s[4:5], s[2:3]
	v_and_or_b32 v50, v52, 8, v50
	s_or_b64 s[0:1], s[2:3], s[0:1]
	v_and_b32_e32 v52, 8, v66
	v_lshlrev_b32_e32 v50, 1, v50
	v_cndmask_b32_e64 v20, 0, v20, s[0:1]
	s_or_b64 vcc, s[0:1], vcc
	v_add3_u32 v50, s48, v52, v50
	s_movk_i32 s0, 0x240
	v_cvt_pk_bf16_f32 v34, v34, v35
	v_mad_u32_u24 v193, v62, s0, v50
	ds_write_b16 v193, v34
	ds_write_b16_d16_hi v193, v34 offset:144
	v_cvt_pk_bf16_f32 v34, v36, v37
	v_mad_u32_u24 v195, v51, s83, v50
	ds_write_b16 v195, v34
	ds_write_b16_d16_hi v195, v34 offset:144
	v_cvt_pk_bf16_f32 v34, v38, v39
	ds_write_b16 v195, v34 offset:864
	ds_write_b16_d16_hi v195, v34 offset:1008
	v_cvt_pk_bf16_f32 v34, v40, v41
	ds_write_b16 v195, v34 offset:1152
	ds_write_b16_d16_hi v195, v34 offset:1296
	v_cvt_pk_bf16_f32 v34, v42, v43
	ds_write_b16 v195, v34 offset:2016
	ds_write_b16_d16_hi v195, v34 offset:2160
; #define R2_ZERO(M) do { _Pragma("unroll") for (int _a = 0; _a < 2; ++_a) _Pragma("unroll") for (int _b = 0; _b < 2; ++_b) _Pragma("unroll") for (int _r = 0; _r < 16; ++_r) M[_a][_b][_r] = 0.f; } while (0)
; #define R2_PACK(Bpk, M) do { _Pragma("unroll") for (int _ks = 0; _ks < 4; ++_ks) _Pragma("unroll") for (int _cb = 0; _cb < 2; ++_cb) Bpk[_ks][_cb] = pack_acc(M[_ks >> 1][_cb], _ks & 1); } while (0)
; __device__ __forceinline__ void ph_rwkv_chunk(const Params& p, int l, LAS unsigned char* lds, const int wvid) {
;     ...
;             R2_TO_LDS(X, A);
;             M64 Z; R2_ZERO(Z); R2_MM_LP(Z, X, Tpk); R2_PACK(Zpk, Z);
;         }
;         {
;             R2_RAW(X, VVg); R2_TRANS_L(Y, X);
	v_cvt_pk_bf16_f32 v34, v44, v45
	ds_write_b16 v195, v34 offset:2304
	ds_write_b16_d16_hi v195, v34 offset:2448
	v_cvt_pk_bf16_f32 v34, v46, v47
	ds_write_b16 v195, v34 offset:3168
	ds_write_b16_d16_hi v195, v34 offset:3312
	v_cvt_pk_bf16_f32 v34, v48, v49
	ds_write_b16 v195, v34 offset:3456
	ds_write_b16_d16_hi v195, v34 offset:3600
	ds_write_b16 v193, v2 offset:64
	ds_write_b16_d16_hi v193, v2 offset:208
	v_cvt_pk_bf16_f32 v2, v4, v5
	ds_write_b16 v195, v2 offset:64
	ds_write_b16_d16_hi v195, v2 offset:208
	v_cvt_pk_bf16_f32 v2, v6, v7
	ds_write_b16 v195, v2 offset:928
	ds_write_b16_d16_hi v195, v2 offset:1072
	v_cvt_pk_bf16_f32 v2, v8, v9
	ds_write_b16 v195, v2 offset:1216
	ds_write_b16_d16_hi v195, v2 offset:1360
	v_cvt_pk_bf16_f32 v2, v10, v11
	ds_write_b16 v195, v2 offset:2080
	ds_write_b16_d16_hi v195, v2 offset:2224
	v_cvt_pk_bf16_f32 v2, v12, v13
	ds_write_b16 v195, v2 offset:2368
	ds_write_b16_d16_hi v195, v2 offset:2512
	v_cvt_pk_bf16_f32 v2, v14, v15
	v_cndmask_b32_e32 v19, 0, v19, vcc
	ds_write_b16 v195, v2 offset:3232
	ds_write_b16_d16_hi v195, v2 offset:3376
	v_cvt_pk_bf16_f32 v2, v16, v17
	v_cndmask_b32_e64 v21, 0, v21, s[2:3]
	ds_write_b16 v195, v2 offset:3520
	ds_write_b16_d16_hi v195, v2 offset:3664
	ds_write_b16 v193, v1 offset:4608
	ds_write_b16 v193, v1 offset:4752
	v_mad_u32_u24 v194, v54, s83, v50
	v_cvt_pk_bf16_f32 v2, v18, v19
	v_cndmask_b32_e64 v23, 0, v23, s[6:7]
	v_cndmask_b32_e64 v22, 0, v22, s[4:5]
	ds_write_b16 v194, v1
	ds_write_b16 v194, v1 offset:144
	ds_write_b16 v194, v1 offset:864
	ds_write_b16 v194, v1 offset:1008
	ds_write_b16 v194, v1 offset:1152
	ds_write_b16 v194, v1 offset:1296
	ds_write_b16 v194, v1 offset:2016
	ds_write_b16 v194, v1 offset:2160
	ds_write_b16 v194, v1 offset:2304
	ds_write_b16 v194, v1 offset:2448
	ds_write_b16 v194, v1 offset:3168
	ds_write_b16 v194, v1 offset:3312
	ds_write_b16 v194, v1 offset:3456
	ds_write_b16 v194, v1 offset:3600
	ds_write_b16 v193, v2 offset:4672
	ds_write_b16_d16_hi v193, v2 offset:4816
	v_cvt_pk_bf16_f32 v2, v20, v21
	v_cndmask_b32_e64 v25, 0, v25, s[10:11]
	v_cndmask_b32_e64 v24, 0, v24, s[8:9]
	ds_write_b16 v194, v2 offset:64
	ds_write_b16_d16_hi v194, v2 offset:208
	v_cvt_pk_bf16_f32 v2, v22, v23
	v_cndmask_b32_e64 v27, 0, v27, s[18:19]
	v_cndmask_b32_e64 v26, 0, v26, s[16:17]
	ds_write_b16 v194, v2 offset:928
	ds_write_b16_d16_hi v194, v2 offset:1072
	v_cvt_pk_bf16_f32 v2, v24, v25
	v_cndmask_b32_e64 v29, 0, v29, s[22:23]
	v_cndmask_b32_e64 v28, 0, v28, s[20:21]
	ds_write_b16 v194, v2 offset:1216
	ds_write_b16_d16_hi v194, v2 offset:1360
	v_cvt_pk_bf16_f32 v2, v26, v27
	v_cndmask_b32_e64 v31, 0, v31, s[26:27]
	v_cndmask_b32_e64 v30, 0, v30, s[24:25]
	ds_write_b16 v194, v2 offset:2080
	ds_write_b16_d16_hi v194, v2 offset:2224
	v_cvt_pk_bf16_f32 v2, v28, v29
	v_cndmask_b32_e64 v33, 0, v33, s[30:31]
	v_cndmask_b32_e64 v32, 0, v32, s[28:29]
	ds_write_b16 v194, v2 offset:2368
	ds_write_b16_d16_hi v194, v2 offset:2512
	v_cvt_pk_bf16_f32 v2, v30, v31
	ds_write_b16 v194, v2 offset:3232
	ds_write_b16_d16_hi v194, v2 offset:3376
	v_cvt_pk_bf16_f32 v2, v32, v33
	ds_write_b16 v194, v2 offset:3520
	ds_write_b16_d16_hi v194, v2 offset:3664
	v_mul_u32_u24_e32 v0, 0x90, v0
	v_add3_u32 v196, s48, v63, v0
	ds_read_b128 v[2:5], v196
	ds_read_b128 v[68:71], v196 offset:32
	s_waitcnt lgkmcnt(1)
	v_mfma_f32_32x32x16_bf16 v[50:65], v[2:5], v[162:165], 0
	v_and_b32_e32 v67, 63, v66
	v_lshlrev_b32_e32 v0, 4, v67
	v_lshl_add_u64 v[88:89], s[42:43], 0, v[0:1]
	v_add_co_u32_e32 v100, vcc, s44, v88
	s_nop 1
	v_addc_co_u32_e32 v101, vcc, 0, v89, vcc
	v_mfma_f32_32x32x16_bf16 v[34:49], v[2:5], v[166:169], 0
	ds_read_b128 v[2:5], v196 offset:4608
	s_waitcnt lgkmcnt(1)
	v_mfma_f32_32x32x16_bf16 v[50:65], v[68:71], v[154:157], v[50:65]
	v_mfma_f32_32x32x16_bf16 v[34:49], v[68:71], v[158:161], v[34:49]
	ds_read_b128 v[68:71], v196 offset:4640
	s_waitcnt lgkmcnt(1)
	v_mfma_f32_32x32x16_bf16 v[18:33], v[2:5], v[162:165], 0
	v_mfma_f32_32x32x16_bf16 v[2:17], v[2:5], v[166:169], 0
	s_waitcnt lgkmcnt(0)
	v_mfma_f32_32x32x16_bf16 v[18:33], v[68:71], v[154:157], v[18:33]
	v_mfma_f32_32x32x16_bf16 v[2:17], v[68:71], v[158:161], v[2:17]
	ds_read_b128 v[68:71], v196 offset:64
	s_waitcnt lgkmcnt(0)
	v_mfma_f32_32x32x16_bf16 v[50:65], v[68:71], v[182:185], v[50:65]
	v_mfma_f32_32x32x16_bf16 v[34:49], v[68:71], v[186:189], v[34:49]
	ds_read_b128 v[68:71], v196 offset:4672
	s_waitcnt lgkmcnt(0)
	v_mfma_f32_32x32x16_bf16 v[18:33], v[68:71], v[182:185], v[18:33]
	v_mfma_f32_32x32x16_bf16 v[2:17], v[68:71], v[186:189], v[2:17]
	ds_read_b128 v[68:71], v196 offset:96
	s_waitcnt lgkmcnt(0)
	v_mfma_f32_32x32x16_bf16 v[50:65], v[68:71], v[178:181], v[50:65]
	v_mfma_f32_32x32x16_bf16 v[34:49], v[68:71], v[150:153], v[34:49]
	ds_read_b128 v[68:71], v196 offset:4704
	global_load_dwordx4 v[72:75], v0, s[42:43]
	global_load_dwordx4 v[76:79], v0, s[42:43] offset:1024
	global_load_dwordx4 v[80:83], v0, s[42:43] offset:2048
	global_load_dwordx4 v[84:87], v0, s[42:43] offset:3072
	global_load_dwordx4 v[88:91], v[100:101], off
	global_load_dwordx4 v[92:95], v[100:101], off offset:1024
	global_load_dwordx4 v[96:99], v[100:101], off offset:2048
	s_nop 0
	global_load_dwordx4 v[100:103], v[100:101], off offset:3072
	v_lshlrev_b32_e32 v0, 4, v66
	v_bfe_u32 v66, v66, 1, 5
	v_and_b32_e32 v0, 16, v0
	v_mul_u32_u24_e32 v66, 0x90, v66
	v_add3_u32 v0, s48, v66, v0
	s_waitcnt vmcnt(7)
	ds_write_b128 v0, v[72:75]
	s_waitcnt vmcnt(6)
	ds_write_b128 v0, v[76:79] offset:4608
	s_waitcnt vmcnt(5)
	ds_write_b128 v0, v[80:83] offset:32
	s_waitcnt vmcnt(4)
	ds_write_b128 v0, v[84:87] offset:4640
	s_waitcnt vmcnt(3)
; #define R2_ZERO(M) do { _Pragma("unroll") for (int _a = 0; _a < 2; ++_a) _Pragma("unroll") for (int _b = 0; _b < 2; ++_b) _Pragma("unroll") for (int _r = 0; _r < 16; ++_r) M[_a][_b][_r] = 0.f; } while (0)
; #define R2_PACK(Bpk, M) do { _Pragma("unroll") for (int _ks = 0; _ks < 4; ++_ks) _Pragma("unroll") for (int _cb = 0; _cb < 2; ++_cb) Bpk[_ks][_cb] = pack_acc(M[_ks >> 1][_cb], _ks & 1); } while (0)
; __device__ __forceinline__ void ph_rwkv_chunk(const Params& p, int l, LAS unsigned char* lds, const int wvid) {
;     ...
;             M64 Z; R2_ZERO(Z); R2_MM_LP(Z, X, Tpk); R2_PACK(Zpk, Z);
;         }
;         {
;             R2_RAW(X, VVg); R2_TRANS_L(Y, X);
;             M64 W; R2_ZERO(W); R2_MM_LP(W, Y, Zpk);
	ds_write_b128 v0, v[88:91] offset:64
	s_waitcnt vmcnt(2)
	ds_write_b128 v0, v[92:95] offset:4672
	s_waitcnt vmcnt(1)
	ds_write_b128 v0, v[96:99] offset:96
	s_waitcnt vmcnt(0)
	ds_write_b128 v0, v[100:103] offset:4704
	v_lshl_add_u32 v0, v67, 1, s48
	s_waitcnt lgkmcnt(8)
	v_mfma_f32_32x32x16_bf16 v[18:33], v[68:71], v[178:181], v[18:33]
	v_cvt_pk_bf16_f32 v34, v34, v35
	v_cvt_pk_bf16_f32 v35, v36, v37
	v_cvt_pk_bf16_f32 v36, v38, v39
	v_cvt_pk_bf16_f32 v37, v40, v41
	v_cvt_pk_bf16_f32 v50, v50, v51
	v_cvt_pk_bf16_f32 v51, v52, v53
	v_cvt_pk_bf16_f32 v52, v54, v55
	v_mfma_f32_32x32x16_bf16 v[2:17], v[68:71], v[150:153], v[2:17]
	v_mad_u32_u24 v70, v67, s83, v191
	ds_read_u16 v66, v0
	ds_read_u16 v67, v0 offset:144
	ds_read_u16 v68, v0 offset:288
	ds_read_u16 v69, v0 offset:432
	ds_read_u16 v71, v0 offset:576
	ds_read_u16 v72, v0 offset:720
	ds_read_u16 v73, v0 offset:864
	ds_read_u16 v74, v0 offset:1008
	s_waitcnt lgkmcnt(6)
	v_lshl_or_b32 v66, v67, 16, v66
	s_waitcnt lgkmcnt(4)
	v_lshl_or_b32 v67, v69, 16, v68
	ds_read_u16 v68, v0 offset:1152
	ds_read_u16 v69, v0 offset:1296
	ds_read_u16 v75, v0 offset:1440
	ds_read_u16 v76, v0 offset:1584
	ds_read_u16 v77, v0 offset:1728
	ds_read_u16 v78, v0 offset:1872
	ds_read_u16 v79, v0 offset:2016
	ds_read_u16 v80, v0 offset:2160
	s_waitcnt lgkmcnt(6)
	v_lshl_or_b32 v68, v69, 16, v68
	s_waitcnt lgkmcnt(4)
	v_lshl_or_b32 v69, v76, 16, v75
	ds_write_b128 v70, v[66:69] offset:9216
	v_lshl_or_b32 v66, v72, 16, v71
	v_lshl_or_b32 v67, v74, 16, v73
	s_waitcnt lgkmcnt(3)
	v_lshl_or_b32 v68, v78, 16, v77
	s_waitcnt lgkmcnt(1)
	v_lshl_or_b32 v69, v80, 16, v79
	ds_write_b128 v70, v[66:69] offset:9232
	ds_read_u16 v66, v0 offset:2304
	ds_read_u16 v67, v0 offset:2448
	ds_read_u16 v68, v0 offset:2592
	ds_read_u16 v69, v0 offset:2736
	ds_read_u16 v71, v0 offset:2880
	ds_read_u16 v72, v0 offset:3024
	ds_read_u16 v73, v0 offset:3168
	ds_read_u16 v74, v0 offset:3312
	s_waitcnt lgkmcnt(6)
	v_lshl_or_b32 v66, v67, 16, v66
	s_waitcnt lgkmcnt(4)
	v_lshl_or_b32 v67, v69, 16, v68
	ds_read_u16 v68, v0 offset:3456
	ds_read_u16 v69, v0 offset:3600
	ds_read_u16 v75, v0 offset:3744
	ds_read_u16 v76, v0 offset:3888
	ds_read_u16 v77, v0 offset:4032
	ds_read_u16 v78, v0 offset:4176
	ds_read_u16 v79, v0 offset:4320
	ds_read_u16 v80, v0 offset:4464
	s_waitcnt lgkmcnt(6)
	v_lshl_or_b32 v68, v69, 16, v68
	s_waitcnt lgkmcnt(4)
	v_lshl_or_b32 v69, v76, 16, v75
	ds_write_b128 v70, v[66:69] offset:9248
	v_lshl_or_b32 v66, v72, 16, v71
	v_lshl_or_b32 v67, v74, 16, v73
	s_waitcnt lgkmcnt(3)
	v_lshl_or_b32 v68, v78, 16, v77
	s_waitcnt lgkmcnt(1)
	v_lshl_or_b32 v69, v80, 16, v79
	ds_write_b128 v70, v[66:69] offset:9264
	ds_read_u16 v66, v0 offset:4608
	ds_read_u16 v67, v0 offset:4752
	ds_read_u16 v68, v0 offset:4896
	ds_read_u16 v69, v0 offset:5040
	ds_read_u16 v71, v0 offset:5184
	ds_read_u16 v72, v0 offset:5328
	ds_read_u16 v73, v0 offset:5472
	ds_read_u16 v74, v0 offset:5616
	s_waitcnt lgkmcnt(6)
	v_lshl_or_b32 v66, v67, 16, v66
	s_waitcnt lgkmcnt(4)
	v_lshl_or_b32 v67, v69, 16, v68
	ds_read_u16 v68, v0 offset:5760
	ds_read_u16 v69, v0 offset:5904
	ds_read_u16 v75, v0 offset:6048
	ds_read_u16 v76, v0 offset:6192
	ds_read_u16 v77, v0 offset:6336
	ds_read_u16 v78, v0 offset:6480
	ds_read_u16 v79, v0 offset:6624
	ds_read_u16 v80, v0 offset:6768
	s_waitcnt lgkmcnt(6)
	v_lshl_or_b32 v68, v69, 16, v68
	s_waitcnt lgkmcnt(4)
	v_lshl_or_b32 v69, v76, 16, v75
	ds_write_b128 v70, v[66:69] offset:9280
	v_lshl_or_b32 v66, v72, 16, v71
	v_lshl_or_b32 v67, v74, 16, v73
	s_waitcnt lgkmcnt(3)
	v_lshl_or_b32 v68, v78, 16, v77
	s_waitcnt lgkmcnt(1)
	v_lshl_or_b32 v69, v80, 16, v79
	ds_write_b128 v70, v[66:69] offset:9296
	ds_read_u16 v66, v0 offset:6912
	ds_read_u16 v67, v0 offset:7056
	ds_read_u16 v68, v0 offset:7200
	ds_read_u16 v69, v0 offset:7344
	ds_read_u16 v71, v0 offset:7488
	ds_read_u16 v72, v0 offset:7632
	ds_read_u16 v73, v0 offset:7776
	ds_read_u16 v74, v0 offset:7920
	s_waitcnt lgkmcnt(6)
	v_lshl_or_b32 v66, v67, 16, v66
	s_waitcnt lgkmcnt(4)
	v_lshl_or_b32 v67, v69, 16, v68
	ds_read_u16 v68, v0 offset:8064
	ds_read_u16 v69, v0 offset:8208
	ds_read_u16 v75, v0 offset:8352
	ds_read_u16 v76, v0 offset:8496
	ds_read_u16 v77, v0 offset:8640
	ds_read_u16 v78, v0 offset:8784
	ds_read_u16 v79, v0 offset:8928
	ds_read_u16 v0, v0 offset:9072
	s_waitcnt lgkmcnt(6)
	v_lshl_or_b32 v68, v69, 16, v68
	s_waitcnt lgkmcnt(4)
	v_lshl_or_b32 v69, v76, 16, v75
	ds_write_b128 v70, v[66:69] offset:9312
	v_lshl_or_b32 v66, v72, 16, v71
	v_lshl_or_b32 v67, v74, 16, v73
	s_waitcnt lgkmcnt(3)
	v_lshl_or_b32 v68, v78, 16, v77
	s_waitcnt lgkmcnt(1)
	v_lshl_or_b32 v69, v0, 16, v79
	ds_write_b128 v70, v[66:69] offset:9328
	ds_read_b128 v[66:69], v196 offset:9216
	ds_read_b128 v[38:41], v196 offset:13824
	v_cvt_pk_bf16_f32 v53, v56, v57
	s_waitcnt lgkmcnt(1)
	v_mfma_f32_32x32x16_bf16 v[98:113], v[66:69], v[34:37], 0
	v_cvt_pk_bf16_f32 v42, v42, v43
	v_cvt_pk_bf16_f32 v43, v44, v45
	v_cvt_pk_bf16_f32 v44, v46, v47
	v_cvt_pk_bf16_f32 v45, v48, v49
	v_cvt_pk_bf16_f32 v2, v2, v3
	v_cvt_pk_bf16_f32 v3, v4, v5
	v_cvt_pk_bf16_f32 v4, v6, v7
	v_mfma_f32_32x32x16_bf16 v[114:129], v[66:69], v[50:53], 0
	v_cvt_pk_bf16_f32 v5, v8, v9
	ds_read_b128 v[6:9], v196 offset:13888
	v_cvt_pk_bf16_f32 v18, v18, v19
	v_cvt_pk_bf16_f32 v19, v20, v21
	v_cvt_pk_bf16_f32 v20, v22, v23
	v_cvt_pk_bf16_f32 v21, v24, v25
	v_cvt_pk_bf16_f32 v10, v10, v11
	s_waitcnt lgkmcnt(1)
	v_mfma_f32_32x32x16_bf16 v[66:81], v[38:41], v[34:37], 0
	ds_read_b128 v[34:37], v196 offset:9248
	v_cvt_pk_bf16_f32 v11, v12, v13
	v_cvt_pk_bf16_f32 v12, v14, v15
	v_cvt_pk_bf16_f32 v13, v16, v17
	v_mfma_f32_32x32x16_bf16 v[82:97], v[38:41], v[50:53], 0
	v_cvt_pk_bf16_f32 v38, v58, v59
	v_cvt_pk_bf16_f32 v39, v60, v61
	v_cvt_pk_bf16_f32 v40, v62, v63
	v_cvt_pk_bf16_f32 v41, v64, v65
	s_waitcnt lgkmcnt(0)
; #define R2_ZERO(M) do { _Pragma("unroll") for (int _a = 0; _a < 2; ++_a) _Pragma("unroll") for (int _b = 0; _b < 2; ++_b) _Pragma("unroll") for (int _r = 0; _r < 16; ++_r) M[_a][_b][_r] = 0.f; } while (0)
; #define R2_PACK(Bpk, M) do { _Pragma("unroll") for (int _ks = 0; _ks < 4; ++_ks) _Pragma("unroll") for (int _cb = 0; _cb < 2; ++_cb) Bpk[_ks][_cb] = pack_acc(M[_ks >> 1][_cb], _ks & 1); } while (0)
; #define R2_MASK(M, STRICT) do { _Pragma("unroll") for (int _rb = 0; _rb < 2; ++_rb) _Pragma("unroll") for (int _cb = 0; _cb < 2; ++_cb) _Pragma("unroll") for (int _r = 0; _r < 16; ++_r) { \
;         const int _row = 32 * _rb + (_r & 3) + 8 * (_r >> 2) + 4 * hi, _col = 32 * _cb + l31; if (STRICT ? !(_row < _col) : !(_row <= _col)) M[_rb][_cb][_r] = 0.f; } } while (0)
; #define R2_RELANE() do { lane = lt_tid(wvid) & 63; l31 = lane & 31; hi = lane >> 5; } while (0)
; __device__ __forceinline__ void ph_rwkv_chunk(const Params& p, int l, LAS unsigned char* lds, const int wvid) {
;     ...
;             M64 W; R2_ZERO(W); R2_MM_LP(W, Y, Zpk);
;             asm volatile("" ::: "memory");
;             R2_TO_LDS(X, W);
;         }
;         R2_RELANE();
;         {
;             bf16x8 AKR[4][2];
;             { M64 B; R2_ZERO(B); R2_MM_GG(B, KTg, RTg); R2_MASK(B, false); R2_PACK(AKR, B); }
	s_nop 0
	v_mfma_f32_32x32x16_bf16 v[114:129], v[34:37], v[38:41], v[114:129]
	v_mfma_f32_32x32x16_bf16 v[98:113], v[34:37], v[42:45], v[98:113]
	ds_read_b128 v[34:37], v196 offset:13856
	s_waitcnt lgkmcnt(0)
	v_mfma_f32_32x32x16_bf16 v[82:97], v[34:37], v[38:41], v[82:97]
	v_mfma_f32_32x32x16_bf16 v[66:81], v[34:37], v[42:45], v[66:81]
	ds_read_b128 v[34:37], v196 offset:9280
	s_waitcnt lgkmcnt(0)
	v_mfma_f32_32x32x16_bf16 v[98:113], v[34:37], v[2:5], v[98:113]
	v_mfma_f32_32x32x16_bf16 v[66:81], v[6:9], v[2:5], v[66:81]
	ds_read_b128 v[2:5], v196 offset:9312
	v_mfma_f32_32x32x16_bf16 v[114:129], v[34:37], v[18:21], v[114:129]
	v_mfma_f32_32x32x16_bf16 v[82:97], v[6:9], v[18:21], v[82:97]
	v_cvt_pk_bf16_f32 v6, v26, v27
	v_cvt_pk_bf16_f32 v7, v28, v29
	v_cvt_pk_bf16_f32 v8, v30, v31
	v_cvt_pk_bf16_f32 v9, v32, v33
	s_waitcnt lgkmcnt(0)
	s_nop 0
	v_mfma_f32_32x32x16_bf16 v[114:129], v[2:5], v[6:9], v[114:129]
	v_mfma_f32_32x32x16_bf16 v[98:113], v[2:5], v[10:13], v[98:113]
	ds_read_b128 v[2:5], v196 offset:13920
	s_nop 9
	v_cvt_pk_bf16_f32 v0, v114, v115
	ds_write_b16 v193, v0
	ds_write_b16_d16_hi v193, v0 offset:144
	v_cvt_pk_bf16_f32 v0, v116, v117
	ds_write_b16 v195, v0
	ds_write_b16_d16_hi v195, v0 offset:144
	v_cvt_pk_bf16_f32 v0, v118, v119
	ds_write_b16 v195, v0 offset:864
	ds_write_b16_d16_hi v195, v0 offset:1008
	v_cvt_pk_bf16_f32 v0, v120, v121
	ds_write_b16 v195, v0 offset:1152
	ds_write_b16_d16_hi v195, v0 offset:1296
	v_cvt_pk_bf16_f32 v0, v122, v123
	ds_write_b16 v195, v0 offset:2016
	ds_write_b16_d16_hi v195, v0 offset:2160
	v_cvt_pk_bf16_f32 v0, v124, v125
	ds_write_b16 v195, v0 offset:2304
	ds_write_b16_d16_hi v195, v0 offset:2448
	v_cvt_pk_bf16_f32 v0, v126, v127
	ds_write_b16 v195, v0 offset:3168
	ds_write_b16_d16_hi v195, v0 offset:3312
	v_cvt_pk_bf16_f32 v0, v128, v129
	s_waitcnt lgkmcnt(14)
	v_mfma_f32_32x32x16_bf16 v[82:97], v[2:5], v[6:9], v[82:97]
	ds_write_b16 v195, v0 offset:3456
	ds_write_b16_d16_hi v195, v0 offset:3600
	v_cvt_pk_bf16_f32 v0, v98, v99
	ds_write_b16 v193, v0 offset:64
	ds_write_b16_d16_hi v193, v0 offset:208
	v_cvt_pk_bf16_f32 v0, v100, v101
	ds_write_b16 v195, v0 offset:64
	ds_write_b16_d16_hi v195, v0 offset:208
	v_cvt_pk_bf16_f32 v0, v102, v103
	ds_write_b16 v195, v0 offset:928
	ds_write_b16_d16_hi v195, v0 offset:1072
	v_cvt_pk_bf16_f32 v0, v104, v105
	ds_write_b16 v195, v0 offset:1216
	ds_write_b16_d16_hi v195, v0 offset:1360
	v_cvt_pk_bf16_f32 v0, v106, v107
	ds_write_b16 v195, v0 offset:2080
	ds_write_b16_d16_hi v195, v0 offset:2224
	v_cvt_pk_bf16_f32 v0, v108, v109
	ds_write_b16 v195, v0 offset:2368
	ds_write_b16_d16_hi v195, v0 offset:2512
	v_cvt_pk_bf16_f32 v0, v110, v111
	ds_write_b16 v195, v0 offset:3232
	ds_write_b16_d16_hi v195, v0 offset:3376
	v_cvt_pk_bf16_f32 v0, v112, v113
	v_mfma_f32_32x32x16_bf16 v[66:81], v[2:5], v[10:13], v[66:81]
	ds_write_b16 v195, v0 offset:3520
	ds_write_b16_d16_hi v195, v0 offset:3664
	v_cvt_pk_bf16_f32 v0, v82, v83
	ds_write_b16 v193, v0 offset:4608
	ds_write_b16_d16_hi v193, v0 offset:4752
	v_cvt_pk_bf16_f32 v0, v84, v85
	ds_write_b16 v194, v0
	ds_write_b16_d16_hi v194, v0 offset:144
	v_cvt_pk_bf16_f32 v0, v86, v87
	ds_write_b16 v194, v0 offset:864
	ds_write_b16_d16_hi v194, v0 offset:1008
	v_cvt_pk_bf16_f32 v0, v88, v89
	ds_write_b16 v194, v0 offset:1152
	ds_write_b16_d16_hi v194, v0 offset:1296
	v_cvt_pk_bf16_f32 v0, v90, v91
	ds_write_b16 v194, v0 offset:2016
	ds_write_b16_d16_hi v194, v0 offset:2160
	v_cvt_pk_bf16_f32 v0, v92, v93
	ds_write_b16 v194, v0 offset:2304
	ds_write_b16_d16_hi v194, v0 offset:2448
	v_cvt_pk_bf16_f32 v0, v94, v95
	ds_write_b16 v194, v0 offset:3168
	ds_write_b16_d16_hi v194, v0 offset:3312
	v_cvt_pk_bf16_f32 v0, v96, v97
	ds_write_b16 v194, v0 offset:3456
	ds_write_b16_d16_hi v194, v0 offset:3600
	v_cvt_pk_bf16_f32 v0, v66, v67
	ds_write_b16 v193, v0 offset:4672
	ds_write_b16_d16_hi v193, v0 offset:4816
	v_cvt_pk_bf16_f32 v0, v68, v69
	ds_write_b16 v194, v0 offset:64
	ds_write_b16_d16_hi v194, v0 offset:208
	v_cvt_pk_bf16_f32 v0, v70, v71
	ds_write_b16 v194, v0 offset:928
	ds_write_b16_d16_hi v194, v0 offset:1072
	v_cvt_pk_bf16_f32 v0, v72, v73
	ds_write_b16 v194, v0 offset:1216
	ds_write_b16_d16_hi v194, v0 offset:1360
	v_cvt_pk_bf16_f32 v0, v74, v75
	ds_write_b16 v194, v0 offset:2080
	ds_write_b16_d16_hi v194, v0 offset:2224
	v_cvt_pk_bf16_f32 v0, v76, v77
	ds_write_b16 v194, v0 offset:2368
	ds_write_b16_d16_hi v194, v0 offset:2512
	v_cvt_pk_bf16_f32 v0, v78, v79
	ds_write_b16 v194, v0 offset:3232
	ds_write_b16_d16_hi v194, v0 offset:3376
	v_cvt_pk_bf16_f32 v0, v80, v81
	ds_write_b16 v194, v0 offset:3520
	ds_write_b16_d16_hi v194, v0 offset:3664
	v_mbcnt_lo_u32_b32 v2, -1, 0
	v_mbcnt_hi_u32_b32 v2, -1, v2
	s_nop 0
	v_or_b32_e32 v0, s75, v2
	v_and_b32_e32 v115, 31, v2
	v_bfe_u32 v124, v0, 5, 1
	v_lshlrev_b32_e32 v114, 5, v115
	v_lshlrev_b32_e32 v14, 4, v124
	v_or_b32_e32 v15, v14, v114
	v_or_b32_e32 v184, 0x1000, v15
	v_or_b32_e32 v185, 0x1400, v15
	v_or_b32_e32 v186, 0x1800, v15
	v_or_b32_e32 v187, 0x1c00, v15
	global_load_dwordx4 v[36:39], v15, s[36:37]
	global_load_dwordx4 v[40:43], v15, s[54:55]
	global_load_dwordx4 v[44:47], v15, s[54:55] offset:1024
	global_load_dwordx4 v[48:51], v15, s[36:37] offset:1024
	global_load_dwordx4 v[52:55], v15, s[36:37] offset:2048
	global_load_dwordx4 v[56:59], v15, s[54:55] offset:2048
	global_load_dwordx4 v[60:63], v15, s[36:37] offset:3072
	global_load_dwordx4 v[64:67], v15, s[54:55] offset:3072
	global_load_dwordx4 v[68:71], v184, s[36:37]
	global_load_dwordx4 v[72:75], v184, s[54:55]
	global_load_dwordx4 v[76:79], v185, s[54:55]
	global_load_dwordx4 v[116:119], v185, s[36:37]
	global_load_dwordx4 v[120:123], v186, s[36:37]
	global_load_dwordx4 v[232:235], v186, s[54:55]
	global_load_dwordx4 v[236:239], v187, s[54:55]
	global_load_dwordx4 v[240:243], v187, s[36:37]
	s_waitcnt vmcnt(0)
; #define R2_ZERO(M) do { _Pragma("unroll") for (int _a = 0; _a < 2; ++_a) _Pragma("unroll") for (int _b = 0; _b < 2; ++_b) _Pragma("unroll") for (int _r = 0; _r < 16; ++_r) M[_a][_b][_r] = 0.f; } while (0)
; #define R2_PACK(Bpk, M) do { _Pragma("unroll") for (int _ks = 0; _ks < 4; ++_ks) _Pragma("unroll") for (int _cb = 0; _cb < 2; ++_cb) Bpk[_ks][_cb] = pack_acc(M[_ks >> 1][_cb], _ks & 1); } while (0)
; #define R2_MASK(M, STRICT) do { _Pragma("unroll") for (int _rb = 0; _rb < 2; ++_rb) _Pragma("unroll") for (int _cb = 0; _cb < 2; ++_cb) _Pragma("unroll") for (int _r = 0; _r < 16; ++_r) { \
;         const int _row = 32 * _rb + (_r & 3) + 8 * (_r >> 2) + 4 * hi, _col = 32 * _cb + l31; if (STRICT ? !(_row < _col) : !(_row <= _col)) M[_rb][_cb][_r] = 0.f; } } while (0)
; __device__ __forceinline__ void ph_rwkv_chunk(const Params& p, int l, LAS unsigned char* lds, const int wvid) {
;     ...
;             { M64 B; R2_ZERO(B); R2_MM_GG(B, KTg, RTg); R2_MASK(B, false); R2_PACK(AKR, B); }
;             M64 Yl; R2_ZERO(Yl); R2_MM_LP(Yl, X, ABR); R2_MM_LP(Yl, Y, AKR);
	v_mfma_f32_32x32x16_bf16 v[82:97], v[36:39], v[40:43], 0
	v_or_b32_e32 v16, 0x1000, v15
	v_lshlrev_b32_e32 v124, 2, v124
	v_cmp_gt_u32_e32 vcc, v124, v115
	v_cmp_lt_u32_e64 s[0:1], v124, v115
	v_lshrrev_b32_e32 v0, 1, v0
	v_and_or_b32 v0, v0, 16, v114
	s_waitcnt vmcnt(0)
	v_mfma_f32_32x32x16_bf16 v[98:113], v[36:39], v[44:47], 0
	s_waitcnt vmcnt(1)
	v_mfma_f32_32x32x16_bf16 v[18:33], v[48:51], v[44:47], 0
	s_waitcnt vmcnt(1)
	v_mfma_f32_32x32x16_bf16 v[82:97], v[52:55], v[56:59], v[82:97]
	s_waitcnt vmcnt(0)
	v_mfma_f32_32x32x16_bf16 v[98:113], v[52:55], v[64:67], v[98:113]
	v_mfma_f32_32x32x16_bf16 v[18:33], v[60:63], v[64:67], v[18:33]
	v_or_b32_e32 v6, 0x1400, v15
	v_or_b32_e32 v16, 0x1800, v15
	s_waitcnt vmcnt(0)
	v_mfma_f32_32x32x16_bf16 v[82:97], v[68:71], v[72:75], v[82:97]
	s_nop 0
	s_waitcnt vmcnt(1)
	v_mfma_f32_32x32x16_bf16 v[98:113], v[68:71], v[76:79], v[98:113]
	s_waitcnt vmcnt(1)
	v_mfma_f32_32x32x16_bf16 v[18:33], v[116:119], v[76:79], v[18:33]
	v_or_b32_e32 v6, 0x1c00, v15
	s_waitcnt vmcnt(0)
	v_mfma_f32_32x32x16_bf16 v[82:97], v[120:123], v[232:235], v[82:97]
	s_nop 11
	v_cndmask_b32_e64 v126, v82, 0, vcc
	s_waitcnt vmcnt(1)
	v_mfma_f32_32x32x16_bf16 v[98:113], v[120:123], v[236:239], v[98:113]
	v_cndmask_b32_e64 v126, v126, v82, s[0:1]
	v_or_b32_e32 v82, 2, v124
	v_cndmask_b32_e64 v127, 0, v83, s[0:1]
	v_cmp_le_u32_e64 s[0:1], v82, v115
	v_or_b32_e32 v82, 3, v124
	s_waitcnt vmcnt(0)
	v_mfma_f32_32x32x16_bf16 v[18:33], v[240:243], v[236:239], v[18:33]
	v_mul_u32_u24_e32 v2, 0x90, v115
	v_add3_u32 v125, s48, v14, v2
	ds_read_b128 v[2:5], v125
	ds_read_b128 v[116:119], v125 offset:32
	v_cndmask_b32_e64 v128, 0, v84, s[0:1]
	v_cmp_le_u32_e64 s[0:1], v82, v115
	v_or_b32_e32 v82, 8, v124
	s_waitcnt lgkmcnt(1)
	v_mfma_f32_32x32x16_bf16 v[66:81], v[2:5], v[134:137], 0
	v_cvt_pk_bf16_f32 v98, v98, v99
	v_cvt_pk_bf16_f32 v99, v100, v101
	v_cvt_pk_bf16_f32 v100, v102, v103
	v_cvt_pk_bf16_f32 v101, v104, v105
	v_cndmask_b32_e64 v18, v18, 0, vcc
	v_mfma_f32_32x32x16_bf16 v[50:65], v[2:5], v[138:141], 0
	ds_read_b128 v[2:5], v125 offset:4608
	s_waitcnt lgkmcnt(1)
	v_mfma_f32_32x32x16_bf16 v[66:81], v[116:119], v[142:145], v[66:81]
	v_mfma_f32_32x32x16_bf16 v[50:65], v[116:119], v[146:149], v[50:65]
	ds_read_b128 v[116:119], v125 offset:4640
	s_waitcnt lgkmcnt(1)
	v_mfma_f32_32x32x16_bf16 v[34:49], v[2:5], v[134:137], 0
	v_mfma_f32_32x32x16_bf16 v[2:17], v[2:5], v[138:141], 0
	s_waitcnt lgkmcnt(0)
	v_mfma_f32_32x32x16_bf16 v[34:49], v[116:119], v[142:145], v[34:49]
	v_mfma_f32_32x32x16_bf16 v[2:17], v[116:119], v[146:149], v[2:17]
	ds_read_b128 v[116:119], v125 offset:64
	s_waitcnt lgkmcnt(0)
	v_mfma_f32_32x32x16_bf16 v[66:81], v[116:119], v[130:133], v[66:81]
	v_mfma_f32_32x32x16_bf16 v[50:65], v[116:119], v[170:173], v[50:65]
	ds_read_b128 v[116:119], v125 offset:4672
	s_waitcnt lgkmcnt(0)
	v_mfma_f32_32x32x16_bf16 v[34:49], v[116:119], v[130:133], v[34:49]
	v_mfma_f32_32x32x16_bf16 v[2:17], v[116:119], v[170:173], v[2:17]
	ds_read_b128 v[116:119], v125 offset:96
	ds_read_b128 v[120:123], v125 offset:4704
	ds_read_b128 v[102:105], v125 offset:13824
	s_waitcnt lgkmcnt(2)
	v_mfma_f32_32x32x16_bf16 v[66:81], v[116:119], v[130:133], v[66:81]
	v_mfma_f32_32x32x16_bf16 v[50:65], v[116:119], v[174:177], v[50:65]
	v_cndmask_b32_e64 v116, 0, v85, s[0:1]
	v_cmp_le_u32_e64 s[0:1], v82, v115
	v_or_b32_e32 v82, 9, v124
	s_nop 0
	v_cndmask_b32_e64 v117, 0, v86, s[0:1]
	v_cmp_le_u32_e64 s[0:1], v82, v115
	v_or_b32_e32 v82, 10, v124
	s_waitcnt lgkmcnt(1)
	v_mfma_f32_32x32x16_bf16 v[34:49], v[120:123], v[130:133], v[34:49]
	v_cndmask_b32_e64 v118, 0, v87, s[0:1]
	v_cmp_le_u32_e64 s[0:1], v82, v115
	v_or_b32_e32 v82, 11, v124
	v_or_b32_e32 v86, 16, v124
	v_cndmask_b32_e64 v119, 0, v88, s[0:1]
	v_cmp_le_u32_e64 s[0:1], v82, v115
	ds_read_b128 v[82:85], v125 offset:9216
	v_mfma_f32_32x32x16_bf16 v[2:17], v[120:123], v[174:177], v[2:17]
	v_cndmask_b32_e64 v89, 0, v89, s[0:1]
	v_cmp_le_u32_e64 s[0:1], v86, v115
	v_or_b32_e32 v120, 17, v124
	v_cvt_pk_bf16_f32 v86, v126, v127
	v_cvt_pk_bf16_f32 v87, v128, v116
	v_cvt_pk_bf16_f32 v88, v117, v118
	v_cvt_pk_bf16_f32 v89, v119, v89
	v_cndmask_b32_e64 v90, 0, v90, s[0:1]
	ds_read_b128 v[116:119], v125 offset:9248
	s_waitcnt lgkmcnt(1)
	v_mfma_f32_32x32x16_bf16 v[66:81], v[82:85], v[86:89], v[66:81]
	v_cmp_le_u32_e64 s[0:1], v120, v115
	s_nop 1
	v_cndmask_b32_e64 v91, 0, v91, s[0:1]
	v_mfma_f32_32x32x16_bf16 v[50:65], v[82:85], v[98:101], v[50:65]
	v_or_b32_e32 v82, 18, v124
	v_cmp_le_u32_e64 s[0:1], v82, v115
	v_or_b32_e32 v82, 19, v124
	s_nop 0
	v_cndmask_b32_e64 v83, 0, v92, s[0:1]
	v_cmp_le_u32_e64 s[0:1], v82, v115
	v_or_b32_e32 v82, 24, v124
	v_mfma_f32_32x32x16_bf16 v[34:49], v[102:105], v[86:89], v[34:49]
	v_cndmask_b32_e64 v84, 0, v93, s[0:1]
	v_cmp_le_u32_e64 s[0:1], v82, v115
	v_or_b32_e32 v82, 25, v124
	v_cvt_pk_bf16_f32 v83, v83, v84
	v_cndmask_b32_e64 v85, 0, v94, s[0:1]
	v_cmp_le_u32_e64 s[0:1], v82, v115
	v_or_b32_e32 v82, 26, v124
	v_mfma_f32_32x32x16_bf16 v[2:17], v[102:105], v[98:101], v[2:17]
	v_cndmask_b32_e64 v86, 0, v95, s[0:1]
	v_cmp_le_u32_e64 s[0:1], v82, v115
	v_or_b32_e32 v82, 27, v124
	v_cvt_pk_bf16_f32 v84, v85, v86
	v_cndmask_b32_e64 v87, 0, v96, s[0:1]
	v_cmp_le_u32_e64 s[0:1], v82, v115
	v_cvt_pk_bf16_f32 v82, v90, v91
	ds_read_b128 v[90:93], v125 offset:13856
	v_cndmask_b32_e64 v88, 0, v97, s[0:1]
	v_cvt_pk_bf16_f32 v85, v87, v88
	v_or_b32_e32 v94, 32, v115
	v_or_b32_e32 v95, 33, v124
	s_waitcnt lgkmcnt(1)
	v_mfma_f32_32x32x16_bf16 v[66:81], v[116:119], v[82:85], v[66:81]
	v_cvt_pk_bf16_f32 v86, v106, v107
	v_cvt_pk_bf16_f32 v87, v108, v109
	v_cvt_pk_bf16_f32 v88, v110, v111
	v_cvt_pk_bf16_f32 v89, v112, v113
	v_or_b32_e32 v96, 34, v124
	v_cmp_le_u32_e32 vcc, v95, v94
	v_or_b32_e32 v97, 35, v124
	s_waitcnt lgkmcnt(0)
; #define R2_ZERO(M) do { _Pragma("unroll") for (int _a = 0; _a < 2; ++_a) _Pragma("unroll") for (int _b = 0; _b < 2; ++_b) _Pragma("unroll") for (int _r = 0; _r < 16; ++_r) M[_a][_b][_r] = 0.f; } while (0)
; #define R2_PACK(Bpk, M) do { _Pragma("unroll") for (int _ks = 0; _ks < 4; ++_ks) _Pragma("unroll") for (int _cb = 0; _cb < 2; ++_cb) Bpk[_ks][_cb] = pack_acc(M[_ks >> 1][_cb], _ks & 1); } while (0)
; #define R2_MASK(M, STRICT) do { _Pragma("unroll") for (int _rb = 0; _rb < 2; ++_rb) _Pragma("unroll") for (int _cb = 0; _cb < 2; ++_cb) _Pragma("unroll") for (int _r = 0; _r < 16; ++_r) { \
;         const int _row = 32 * _rb + (_r & 3) + 8 * (_r >> 2) + 4 * hi, _col = 32 * _cb + l31; if (STRICT ? !(_row < _col) : !(_row <= _col)) M[_rb][_cb][_r] = 0.f; } } while (0)
; #define R2_RELANE() do { lane = lt_tid(wvid) & 63; l31 = lane & 31; hi = lane >> 5; } while (0)
; __device__ __forceinline__ void ph_rwkv_chunk(const Params& p, int l, LAS unsigned char* lds, const int wvid) {
;     ...
;             bf16x8 AKR[4][2];
;             { M64 B; R2_ZERO(B); R2_MM_GG(B, KTg, RTg); R2_MASK(B, false); R2_PACK(AKR, B); }
;             M64 Yl; R2_ZERO(Yl); R2_MM_LP(Yl, X, ABR); R2_MM_LP(Yl, Y, AKR);
;             R2_STORE_T(YLg, Yl, false, 1.0f);
;         }
;         R2_RELANE();
;         {
;             M64 Q; R2_ZERO(Q);
;             { bf16x8 Bp[4][2]; R2_PSEUDO(Bp, BTg); R2_MM_LP(Q, X, Bp); }
	v_mfma_f32_32x32x16_bf16 v[34:49], v[90:93], v[82:85], v[34:49]
	ds_read_b128 v[82:85], v125 offset:9280
	v_cndmask_b32_e32 v19, 0, v19, vcc
	v_cmp_le_u32_e32 vcc, v96, v94
	v_or_b32_e32 v98, 40, v124
	v_or_b32_e32 v99, 41, v124
	v_cndmask_b32_e32 v20, 0, v20, vcc
	v_cmp_le_u32_e32 vcc, v97, v94
	v_mfma_f32_32x32x16_bf16 v[50:65], v[116:119], v[86:89], v[50:65]
	v_or_b32_e32 v100, 42, v124
	v_cndmask_b32_e32 v21, 0, v21, vcc
	v_cmp_le_u32_e32 vcc, v98, v94
	v_or_b32_e32 v101, 43, v124
	v_cvt_pk_bf16_f32 v18, v18, v19
	v_cndmask_b32_e32 v22, 0, v22, vcc
	v_cmp_le_u32_e32 vcc, v99, v94
	v_mfma_f32_32x32x16_bf16 v[2:17], v[90:93], v[86:89], v[2:17]
	v_cvt_pk_bf16_f32 v19, v20, v21
	v_cndmask_b32_e32 v23, 0, v23, vcc
	v_cmp_le_u32_e32 vcc, v100, v94
	v_cvt_pk_bf16_f32 v20, v22, v23
	v_or_b32_e32 v86, 48, v124
	v_cndmask_b32_e32 v24, 0, v24, vcc
	v_cmp_le_u32_e32 vcc, v101, v94
	s_waitcnt lgkmcnt(0)
	v_mfma_f32_32x32x16_bf16 v[66:81], v[82:85], v[130:133], v[66:81]
	v_or_b32_e32 v87, 49, v124
	v_cndmask_b32_e32 v25, 0, v25, vcc
	v_cvt_pk_bf16_f32 v21, v24, v25
	v_cmp_le_u32_e32 vcc, v86, v94
	v_or_b32_e32 v88, 50, v124
	v_or_b32_e32 v89, 51, v124
	v_cndmask_b32_e32 v26, 0, v26, vcc
	v_mfma_f32_32x32x16_bf16 v[50:65], v[82:85], v[18:21], v[50:65]
	ds_read_b128 v[22:25], v125 offset:13888
	ds_read_b128 v[82:85], v125 offset:9312
	v_cmp_le_u32_e32 vcc, v87, v94
	v_or_b32_e32 v90, 56, v124
	v_or_b32_e32 v91, 57, v124
	v_cndmask_b32_e32 v27, 0, v27, vcc
	v_cmp_le_u32_e32 vcc, v88, v94
	v_or_b32_e32 v92, 58, v124
	s_waitcnt lgkmcnt(1)
	v_mfma_f32_32x32x16_bf16 v[2:17], v[22:25], v[18:21], v[2:17]
	v_cndmask_b32_e32 v19, 0, v28, vcc
	v_cmp_le_u32_e32 vcc, v89, v94
	v_or_b32_e32 v93, 59, v124
	v_cvt_pk_bf16_f32 v18, v26, v27
	v_cndmask_b32_e32 v20, 0, v29, vcc
	v_cmp_le_u32_e32 vcc, v90, v94
	v_cvt_pk_bf16_f32 v19, v19, v20
	v_mfma_f32_32x32x16_bf16 v[34:49], v[22:25], v[130:133], v[34:49]
	v_cndmask_b32_e32 v21, 0, v30, vcc
	v_cmp_le_u32_e32 vcc, v91, v94
	s_add_u32 s0, s81, s38
	s_addc_u32 s1, s58, s39
	v_cndmask_b32_e32 v22, 0, v31, vcc
	v_cmp_le_u32_e32 vcc, v92, v94
	v_cvt_pk_bf16_f32 v20, v21, v22
	s_waitcnt lgkmcnt(0)
	v_mfma_f32_32x32x16_bf16 v[66:81], v[82:85], v[130:133], v[66:81]
	v_cndmask_b32_e32 v23, 0, v32, vcc
	v_cmp_le_u32_e32 vcc, v93, v94
	s_nop 1
	v_cndmask_b32_e32 v24, 0, v33, vcc
	v_cvt_pk_bf16_f32 v21, v23, v24
	ds_read_b128 v[22:25], v125 offset:13920
	s_waitcnt lgkmcnt(0)
	v_mfma_f32_32x32x16_bf16 v[34:49], v[22:25], v[130:133], v[34:49]
	v_mfma_f32_32x32x16_bf16 v[50:65], v[82:85], v[18:21], v[50:65]
	v_mfma_f32_32x32x16_bf16 v[2:17], v[22:25], v[18:21], v[2:17]
	s_nop 0
	v_cvt_pk_bf16_f32 v18, v66, v67
	v_cvt_pk_bf16_f32 v19, v68, v69
	v_cvt_pk_bf16_f32 v20, v70, v71
	v_cvt_pk_bf16_f32 v21, v72, v73
	s_nop 0
	v_permlane32_swap_b32_e32 v18, v20
	v_permlane32_swap_b32_e32 v19, v21
	global_store_dwordx4 v0, v[18:21], s[0:1]
	v_lshl_add_u64 v[22:23], s[0:1], 0, v[0:1]
	v_add_co_u32_e32 v22, vcc, s44, v22
	v_cvt_pk_bf16_f32 v18, v74, v75
	v_cvt_pk_bf16_f32 v19, v76, v77
	v_cvt_pk_bf16_f32 v20, v78, v79
	v_cvt_pk_bf16_f32 v21, v80, v81
	s_nop 0
	v_permlane32_swap_b32_e32 v18, v20
	v_permlane32_swap_b32_e32 v19, v21
	global_store_dwordx4 v0, v[18:21], s[0:1] offset:2048
	v_cvt_pk_bf16_f32 v2, v2, v3
	v_cvt_pk_bf16_f32 v3, v4, v5
	v_cvt_pk_bf16_f32 v18, v50, v51
	v_cvt_pk_bf16_f32 v19, v52, v53
	v_cvt_pk_bf16_f32 v20, v54, v55
	v_cvt_pk_bf16_f32 v21, v56, v57
	s_nop 0
	v_permlane32_swap_b32_e32 v18, v20
	v_permlane32_swap_b32_e32 v19, v21
	global_store_dwordx4 v0, v[18:21], s[0:1] offset:1024
	v_cvt_pk_bf16_f32 v4, v6, v7
	v_cvt_pk_bf16_f32 v5, v8, v9
	v_cvt_pk_bf16_f32 v18, v58, v59
	v_cvt_pk_bf16_f32 v19, v60, v61
	v_cvt_pk_bf16_f32 v20, v62, v63
	v_cvt_pk_bf16_f32 v21, v64, v65
	s_nop 0
	v_permlane32_swap_b32_e32 v18, v20
	v_permlane32_swap_b32_e32 v19, v21
	global_store_dwordx4 v0, v[18:21], s[0:1] offset:3072
	v_addc_co_u32_e32 v23, vcc, 0, v23, vcc
	s_nop 0
	v_cvt_pk_bf16_f32 v18, v34, v35
	v_cvt_pk_bf16_f32 v19, v36, v37
	v_cvt_pk_bf16_f32 v20, v38, v39
	v_cvt_pk_bf16_f32 v21, v40, v41
	s_nop 0
	v_permlane32_swap_b32_e32 v18, v20
	v_permlane32_swap_b32_e32 v19, v21
	v_permlane32_swap_b32_e32 v2, v4
	v_permlane32_swap_b32_e32 v3, v5
	global_store_dwordx4 v[22:23], v[18:21], off
	global_store_dwordx4 v[22:23], v[2:5], off offset:1024
	s_movk_i32 s0, 0x400
	v_cvt_pk_bf16_f32 v18, v42, v43
	v_cvt_pk_bf16_f32 v19, v44, v45
	v_cvt_pk_bf16_f32 v20, v46, v47
	v_cvt_pk_bf16_f32 v21, v48, v49
	v_cvt_pk_bf16_f32 v2, v10, v11
	v_cvt_pk_bf16_f32 v3, v12, v13
	v_cvt_pk_bf16_f32 v4, v14, v15
	v_cvt_pk_bf16_f32 v5, v16, v17
	v_permlane32_swap_b32_e32 v18, v20
	v_permlane32_swap_b32_e32 v19, v21
	v_permlane32_swap_b32_e32 v2, v4
	v_permlane32_swap_b32_e32 v3, v5
	global_store_dwordx4 v[22:23], v[18:21], off offset:2048
	global_store_dwordx4 v[22:23], v[2:5], off offset:3072
	v_mbcnt_lo_u32_b32 v71, -1, 0
	v_mbcnt_hi_u32_b32 v71, -1, v71
	s_nop 0
	v_bfe_u32 v69, v71, 5, 1
	v_lshlrev_b32_e32 v0, 6, v71
	v_and_b32_e32 v2, 15, v71
	v_lshlrev_b32_e32 v3, 6, v69
	v_and_or_b32 v0, v0, s0, v2
	v_lshl_or_b32 v70, v69, 2, 2
	v_or_b32_e32 v7, 0x80, v3
	v_or_b32_e32 v9, 0xa0, v3
	v_or_b32_e32 v4, v0, v3
	v_lshlrev_b32_e32 v5, 4, v70
	v_or_b32_e32 v8, v7, v0
	v_or_b32_e32 v10, v9, v0
	v_lshlrev_b32_e32 v4, 1, v4
	v_or_b32_e32 v6, v5, v0
	v_lshlrev_b32_e32 v8, 1, v8
	v_lshlrev_b32_e32 v10, 1, v10
	v_or_b32_e32 v2, 0x800, v0
	v_lshlrev_b32_e32 v6, 1, v6
	global_load_ushort v11, v4, s[70:71]
	global_load_ushort v12, v4, s[70:71] offset:32
	global_load_ushort v13, v6, s[70:71]
	global_load_ushort v14, v6, s[70:71] offset:32
	global_load_ushort v15, v8, s[70:71]
; #define R2_ZERO(M) do { _Pragma("unroll") for (int _a = 0; _a < 2; ++_a) _Pragma("unroll") for (int _b = 0; _b < 2; ++_b) _Pragma("unroll") for (int _r = 0; _r < 16; ++_r) M[_a][_b][_r] = 0.f; } while (0)
; __device__ __forceinline__ void ph_rwkv_chunk(const Params& p, int l, LAS unsigned char* lds, const int wvid) {
;     ...
;         {
;             M64 Q; R2_ZERO(Q);
;             { bf16x8 Bp[4][2]; R2_PSEUDO(Bp, BTg); R2_MM_LP(Q, X, Bp); }
	s_nop 0
	global_load_ushort v8, v8, s[70:71] offset:32
	s_nop 0
	global_load_ushort v16, v10, s[70:71]
	s_nop 0
	global_load_ushort v10, v10, s[70:71] offset:32
	v_or_b32_e32 v4, 0x810, v0
	v_or_b32_e32 v6, v2, v3
	v_or_b32_e32 v17, v4, v3
	v_or_b32_e32 v18, v2, v5
	v_or_b32_e32 v19, v2, v7
	v_or_b32_e32 v20, v2, v9
	v_lshlrev_b32_e32 v6, 1, v6
	v_lshlrev_b32_e32 v17, 1, v17
	v_lshlrev_b32_e32 v18, 1, v18
	v_or_b32_e32 v5, v4, v5
	v_lshlrev_b32_e32 v19, 1, v19
	v_or_b32_e32 v7, v4, v7
	v_lshlrev_b32_e32 v20, 1, v20
	v_or_b32_e32 v9, v4, v9
	v_lshlrev_b32_e32 v5, 1, v5
	v_lshlrev_b32_e32 v7, 1, v7
	v_lshlrev_b32_e32 v9, 1, v9
	global_load_ushort v21, v6, s[70:71]
	s_nop 0
	global_load_ushort v17, v17, s[70:71]
	s_nop 0
	global_load_ushort v18, v18, s[70:71]
	s_nop 0
	global_load_ushort v22, v5, s[70:71]
	s_nop 0
	global_load_ushort v19, v19, s[70:71]
	s_nop 0
	global_load_ushort v23, v7, s[70:71]
	s_nop 0
	global_load_ushort v20, v20, s[70:71]
	s_nop 0
	global_load_ushort v24, v9, s[70:71]
	v_or_b32_e32 v5, 0x100, v3
	v_or_b32_e32 v6, v5, v0
	v_or_b32_e32 v7, 0x120, v3
	v_or_b32_e32 v25, 0x180, v3
	v_or_b32_e32 v27, 0x1a0, v3
	v_lshlrev_b32_e32 v6, 1, v6
	v_or_b32_e32 v9, v7, v0
	v_or_b32_e32 v26, v25, v0
	v_or_b32_e32 v28, v27, v0
	v_lshlrev_b32_e32 v9, 1, v9
	v_lshlrev_b32_e32 v26, 1, v26
	v_lshlrev_b32_e32 v28, 1, v28
	global_load_ushort v76, v6, s[70:71]
	global_load_ushort v77, v6, s[70:71] offset:32
	global_load_ushort v78, v9, s[70:71]
	global_load_ushort v79, v9, s[70:71] offset:32
	global_load_ushort v80, v26, s[70:71]
	global_load_ushort v81, v26, s[70:71] offset:32
	global_load_ushort v82, v28, s[70:71]
	global_load_ushort v83, v28, s[70:71] offset:32
	v_or_b32_e32 v6, v2, v5
	v_lshlrev_b32_e32 v6, 1, v6
	v_or_b32_e32 v5, v4, v5
	v_or_b32_e32 v9, v2, v7
	v_or_b32_e32 v7, v4, v7
	v_or_b32_e32 v26, v2, v25
	v_or_b32_e32 v25, v4, v25
	v_or_b32_e32 v28, v2, v27
	v_or_b32_e32 v27, v4, v27
	v_lshlrev_b32_e32 v5, 1, v5
	v_lshlrev_b32_e32 v9, 1, v9
	v_lshlrev_b32_e32 v7, 1, v7
	v_lshlrev_b32_e32 v26, 1, v26
	v_lshlrev_b32_e32 v25, 1, v25
	v_lshlrev_b32_e32 v28, 1, v28
	v_lshlrev_b32_e32 v27, 1, v27
	global_load_ushort v84, v6, s[70:71]
	global_load_ushort v85, v5, s[70:71]
	global_load_ushort v86, v9, s[70:71]
	global_load_ushort v87, v7, s[70:71]
	global_load_ushort v88, v26, s[70:71]
	global_load_ushort v89, v25, s[70:71]
	global_load_ushort v90, v28, s[70:71]
	global_load_ushort v91, v27, s[70:71]
	v_or_b32_e32 v5, 0x200, v3
	v_or_b32_e32 v6, v5, v0
	v_or_b32_e32 v7, 0x220, v3
	v_or_b32_e32 v25, 0x280, v3
	v_or_b32_e32 v27, 0x2a0, v3
	v_lshlrev_b32_e32 v6, 1, v6
	v_or_b32_e32 v9, v7, v0
	v_or_b32_e32 v26, v25, v0
	v_or_b32_e32 v28, v27, v0
	v_lshlrev_b32_e32 v9, 1, v9
	v_lshlrev_b32_e32 v26, 1, v26
	v_lshlrev_b32_e32 v28, 1, v28
	global_load_ushort v92, v6, s[70:71]
	global_load_ushort v93, v6, s[70:71] offset:32
	global_load_ushort v94, v9, s[70:71]
	global_load_ushort v95, v9, s[70:71] offset:32
	global_load_ushort v96, v26, s[70:71]
	global_load_ushort v97, v26, s[70:71] offset:32
	global_load_ushort v98, v28, s[70:71]
	global_load_ushort v99, v28, s[70:71] offset:32
	v_or_b32_e32 v6, v2, v5
	v_lshlrev_b32_e32 v6, 1, v6
	v_or_b32_e32 v5, v4, v5
	v_or_b32_e32 v9, v2, v7
	v_or_b32_e32 v7, v4, v7
	v_or_b32_e32 v26, v2, v25
	v_or_b32_e32 v25, v4, v25
	v_or_b32_e32 v28, v2, v27
	v_or_b32_e32 v27, v4, v27
	v_lshlrev_b32_e32 v5, 1, v5
	v_lshlrev_b32_e32 v9, 1, v9
	v_lshlrev_b32_e32 v7, 1, v7
	v_lshlrev_b32_e32 v26, 1, v26
	v_lshlrev_b32_e32 v25, 1, v25
	v_lshlrev_b32_e32 v28, 1, v28
	v_lshlrev_b32_e32 v27, 1, v27
	global_load_ushort v100, v6, s[70:71]
	global_load_ushort v101, v5, s[70:71]
	global_load_ushort v102, v9, s[70:71]
	global_load_ushort v103, v7, s[70:71]
	global_load_ushort v104, v26, s[70:71]
	global_load_ushort v105, v25, s[70:71]
	global_load_ushort v106, v28, s[70:71]
	global_load_ushort v107, v27, s[70:71]
	v_or_b32_e32 v5, 0x300, v3
	v_or_b32_e32 v7, 0x320, v3
	v_or_b32_e32 v25, 0x380, v3
	v_or_b32_e32 v3, 0x3a0, v3
	v_or_b32_e32 v6, v5, v0
	v_or_b32_e32 v9, v7, v0
	v_or_b32_e32 v26, v25, v0
	v_or_b32_e32 v0, v3, v0
	v_lshlrev_b32_e32 v6, 1, v6
	v_lshlrev_b32_e32 v0, 1, v0
	v_lshlrev_b32_e32 v9, 1, v9
	v_lshlrev_b32_e32 v26, 1, v26
	global_load_ushort v108, v6, s[70:71]
	global_load_ushort v109, v6, s[70:71] offset:32
	global_load_ushort v110, v9, s[70:71]
	global_load_ushort v111, v9, s[70:71] offset:32
	global_load_ushort v112, v26, s[70:71]
	global_load_ushort v113, v26, s[70:71] offset:32
	global_load_ushort v114, v0, s[70:71]
	s_nop 0
	global_load_ushort v0, v0, s[70:71] offset:32
	v_or_b32_e32 v6, v2, v5
	v_lshlrev_b32_e32 v6, 1, v6
	v_or_b32_e32 v5, v4, v5
	v_or_b32_e32 v9, v2, v7
	v_or_b32_e32 v7, v4, v7
	v_or_b32_e32 v26, v2, v25
	v_or_b32_e32 v25, v4, v25
	v_or_b32_e32 v2, v2, v3
	v_or_b32_e32 v3, v4, v3
	v_lshlrev_b32_e32 v5, 1, v5
	v_lshlrev_b32_e32 v9, 1, v9
	v_lshlrev_b32_e32 v7, 1, v7
	v_lshlrev_b32_e32 v26, 1, v26
	v_lshlrev_b32_e32 v25, 1, v25
	v_lshlrev_b32_e32 v2, 1, v2
	v_lshlrev_b32_e32 v3, 1, v3
	global_load_ushort v115, v6, s[70:71]
	global_load_ushort v116, v5, s[70:71]
	global_load_ushort v117, v9, s[70:71]
	global_load_ushort v118, v7, s[70:71]
	global_load_ushort v119, v26, s[70:71]
	global_load_ushort v120, v25, s[70:71]
	global_load_ushort v121, v2, s[70:71]
	global_load_ushort v122, v3, s[70:71]
	v_and_b32_e32 v66, 31, v71
	v_lshlrev_b32_e32 v67, 4, v69
	v_mul_u32_u24_e32 v2, 0x90, v66
	v_add3_u32 v68, s48, v67, v2
	ds_read_b128 v[2:5], v68
	ds_read_b128 v[72:75], v68 offset:32
	s_waitcnt vmcnt(62)
	v_lshl_or_b32 v6, v12, 16, v11
	s_waitcnt vmcnt(60)
	v_lshl_or_b32 v7, v14, 16, v13
	s_waitcnt vmcnt(58)
; #define R2_ZERO(M) do { _Pragma("unroll") for (int _a = 0; _a < 2; ++_a) _Pragma("unroll") for (int _b = 0; _b < 2; ++_b) _Pragma("unroll") for (int _r = 0; _r < 16; ++_r) M[_a][_b][_r] = 0.f; } while (0)
; __device__ __forceinline__ void ph_rwkv_chunk(const Params& p, int l, LAS unsigned char* lds, const int wvid) {
;     ...
;             M64 Q; R2_ZERO(Q);
;             { bf16x8 Bp[4][2]; R2_PSEUDO(Bp, BTg); R2_MM_LP(Q, X, Bp); }
;             { bf16x8 Kp[4][2]; asm volatile("" ::: "memory"); R2_RAW(X, KTg); R2_PSEUDO_L(Kp, X); R2_MM_LP(Q, Y, Kp); }
	v_lshl_or_b32 v8, v8, 16, v15
	s_waitcnt vmcnt(56)
	v_lshl_or_b32 v9, v10, 16, v16
	s_waitcnt vmcnt(54)
	v_lshl_or_b32 v10, v17, 16, v21
	s_waitcnt vmcnt(52)
	v_lshl_or_b32 v11, v22, 16, v18
	s_waitcnt vmcnt(50)
	v_lshl_or_b32 v12, v23, 16, v19
	s_waitcnt vmcnt(48)
	v_lshl_or_b32 v13, v24, 16, v20
	s_waitcnt lgkmcnt(1)
	v_mfma_f32_32x32x16_bf16 v[34:49], v[2:5], v[6:9], 0
	s_waitcnt vmcnt(46)
	v_lshl_or_b32 v76, v77, 16, v76
	s_waitcnt vmcnt(44)
	v_lshl_or_b32 v77, v79, 16, v78
	s_waitcnt vmcnt(42)
	v_lshl_or_b32 v78, v81, 16, v80
	s_waitcnt vmcnt(40)
	v_lshl_or_b32 v79, v83, 16, v82
	s_waitcnt vmcnt(38)
	v_lshl_or_b32 v80, v85, 16, v84
	s_waitcnt vmcnt(36)
	v_lshl_or_b32 v81, v87, 16, v86
	s_waitcnt vmcnt(34)
	v_lshl_or_b32 v82, v89, 16, v88
	v_mfma_f32_32x32x16_bf16 v[50:65], v[2:5], v[10:13], 0
	ds_read_b128 v[2:5], v68 offset:4608
	s_waitcnt vmcnt(32)
	v_lshl_or_b32 v83, v91, 16, v90
	v_mul_u32_u24_e32 v69, 0x240, v69
	v_mul_u32_u24_e32 v70, 0x90, v70
	s_movk_i32 s70, 0x1000
	s_waitcnt lgkmcnt(1)
	v_mfma_f32_32x32x16_bf16 v[34:49], v[72:75], v[76:79], v[34:49]
	v_mfma_f32_32x32x16_bf16 v[50:65], v[72:75], v[80:83], v[50:65]
	ds_read_b128 v[72:75], v68 offset:4640
	s_waitcnt lgkmcnt(1)
	v_mfma_f32_32x32x16_bf16 v[18:33], v[2:5], v[6:9], 0
	v_mfma_f32_32x32x16_bf16 v[2:17], v[2:5], v[10:13], 0
	s_waitcnt lgkmcnt(0)
	v_mfma_f32_32x32x16_bf16 v[18:33], v[72:75], v[76:79], v[18:33]
	s_waitcnt vmcnt(30)
	v_lshl_or_b32 v76, v93, 16, v92
	s_waitcnt vmcnt(28)
	v_lshl_or_b32 v77, v95, 16, v94
	s_waitcnt vmcnt(26)
	v_lshl_or_b32 v78, v97, 16, v96
	s_waitcnt vmcnt(24)
	v_lshl_or_b32 v79, v99, 16, v98
	v_mfma_f32_32x32x16_bf16 v[2:17], v[72:75], v[80:83], v[2:17]
	ds_read_b128 v[72:75], v68 offset:64
	s_waitcnt vmcnt(22)
	v_lshl_or_b32 v80, v101, 16, v100
	s_waitcnt vmcnt(20)
	v_lshl_or_b32 v81, v103, 16, v102
	s_waitcnt vmcnt(18)
	v_lshl_or_b32 v82, v105, 16, v104
	s_waitcnt vmcnt(16)
	v_lshl_or_b32 v83, v107, 16, v106
	s_waitcnt lgkmcnt(0)
	v_mfma_f32_32x32x16_bf16 v[34:49], v[72:75], v[76:79], v[34:49]
	v_mfma_f32_32x32x16_bf16 v[50:65], v[72:75], v[80:83], v[50:65]
	ds_read_b128 v[72:75], v68 offset:4672
	s_waitcnt lgkmcnt(0)
	v_mfma_f32_32x32x16_bf16 v[18:33], v[72:75], v[76:79], v[18:33]
	s_waitcnt vmcnt(14)
	v_lshl_or_b32 v76, v109, 16, v108
	s_waitcnt vmcnt(12)
	v_lshl_or_b32 v77, v111, 16, v110
	s_waitcnt vmcnt(10)
	v_lshl_or_b32 v78, v113, 16, v112
	s_waitcnt vmcnt(8)
	v_lshl_or_b32 v79, v0, 16, v114
	v_and_b32_e32 v0, 63, v71
	v_lshlrev_b32_e32 v0, 4, v0
	v_lshl_add_u64 v[96:97], s[36:37], 0, v[0:1]
	v_mfma_f32_32x32x16_bf16 v[2:17], v[72:75], v[80:83], v[2:17]
	ds_read_b128 v[72:75], v68 offset:96
	s_waitcnt vmcnt(6)
	v_lshl_or_b32 v80, v116, 16, v115
	s_waitcnt vmcnt(4)
	v_lshl_or_b32 v81, v118, 16, v117
	s_waitcnt vmcnt(2)
	v_lshl_or_b32 v82, v120, 16, v119
	s_waitcnt vmcnt(0)
	v_lshl_or_b32 v83, v122, 16, v121
	v_add_co_u32_e32 v108, vcc, s44, v96
	s_waitcnt lgkmcnt(0)
	v_mfma_f32_32x32x16_bf16 v[34:49], v[72:75], v[76:79], v[34:49]
	v_addc_co_u32_e32 v109, vcc, 0, v97, vcc
	v_mfma_f32_32x32x16_bf16 v[50:65], v[72:75], v[80:83], v[50:65]
	ds_read_b128 v[72:75], v68 offset:4704
	s_waitcnt lgkmcnt(0)
	v_mfma_f32_32x32x16_bf16 v[18:33], v[72:75], v[76:79], v[18:33]
	global_load_dwordx4 v[76:79], v0, s[36:37]
	global_load_dwordx4 v[84:87], v0, s[36:37] offset:1024
	global_load_dwordx4 v[88:91], v0, s[36:37] offset:2048
	global_load_dwordx4 v[92:95], v0, s[36:37] offset:3072
	global_load_dwordx4 v[96:99], v[108:109], off
	global_load_dwordx4 v[100:103], v[108:109], off offset:1024
	global_load_dwordx4 v[104:107], v[108:109], off offset:2048
	s_nop 0
	global_load_dwordx4 v[108:111], v[108:109], off offset:3072
	v_lshlrev_b32_e32 v0, 4, v71
	v_bfe_u32 v71, v71, 1, 5
	v_and_b32_e32 v0, 16, v0
	v_mul_u32_u24_e32 v71, 0x90, v71
	v_add3_u32 v0, s48, v71, v0
	s_waitcnt vmcnt(7)
	ds_write_b128 v0, v[76:79]
	s_waitcnt vmcnt(6)
	ds_write_b128 v0, v[84:87] offset:4608
	s_waitcnt vmcnt(5)
	ds_write_b128 v0, v[88:91] offset:32
	s_waitcnt vmcnt(4)
	ds_write_b128 v0, v[92:95] offset:4640
	s_waitcnt vmcnt(3)
	ds_write_b128 v0, v[96:99] offset:64
	s_waitcnt vmcnt(2)
	ds_write_b128 v0, v[100:103] offset:4672
	s_waitcnt vmcnt(1)
	ds_write_b128 v0, v[104:107] offset:96
	s_waitcnt vmcnt(0)
	ds_write_b128 v0, v[108:111] offset:4704
	v_lshlrev_b32_e32 v0, 1, v66
	v_add3_u32 v69, s48, v69, v0
	v_add3_u32 v0, s48, v70, v0
	v_mfma_f32_32x32x16_bf16 v[2:17], v[72:75], v[80:83], v[2:17]
	ds_read_u16 v74, v69
	ds_read_u16 v75, v69 offset:144
	ds_read_u16 v76, v0
	ds_read_u16 v77, v0 offset:144
	ds_read_u16 v79, v0 offset:208
	ds_read_u16 v80, v0 offset:64
	ds_read_u16 v78, v69 offset:208
	ds_read_u16 v69, v69 offset:64
	ds_read_u16 v81, v0 offset:864
	ds_read_u16 v82, v0 offset:1008
	ds_read_u16 v83, v0 offset:1152
	ds_read_u16 v84, v0 offset:1296
	ds_read_u16 v85, v0 offset:1360
	ds_read_u16 v86, v0 offset:1216
	ds_read_u16 v87, v0 offset:1072
	ds_read_u16 v88, v0 offset:928
	ds_read_u16 v89, v0 offset:2016
	ds_read_u16 v90, v0 offset:2160
	ds_read_u16 v91, v0 offset:2304
	ds_read_u16 v92, v0 offset:2448
	ds_read_u16 v93, v0 offset:2512
	ds_read_u16 v94, v0 offset:2368
	ds_read_u16 v95, v0 offset:2224
	ds_read_u16 v96, v0 offset:2080
	ds_read_u16 v97, v0 offset:3168
	ds_read_u16 v98, v0 offset:3312
	ds_read_u16 v99, v0 offset:3456
	ds_read_u16 v100, v0 offset:3600
	ds_read_u16 v101, v0 offset:3664
	ds_read_u16 v102, v0 offset:3520
	ds_read_u16 v103, v0 offset:3376
	ds_read_u16 v104, v0 offset:3232
	ds_read_u16 v105, v0 offset:4320
	ds_read_u16 v106, v0 offset:4464
	ds_read_u16 v107, v0 offset:4608
	ds_read_u16 v108, v0 offset:4752
	ds_read_u16 v109, v0 offset:4816
	ds_read_u16 v110, v0 offset:4672
	ds_read_u16 v111, v0 offset:4528
	ds_read_u16 v112, v0 offset:4384
	ds_read_u16 v113, v0 offset:5472
	ds_read_u16 v114, v0 offset:5616
	ds_read_u16 v115, v0 offset:5760
	ds_read_u16 v116, v0 offset:5904
	ds_read_u16 v117, v0 offset:5968
	ds_read_u16 v118, v0 offset:5824
	ds_read_u16 v119, v0 offset:5680
	ds_read_u16 v120, v0 offset:5536
	ds_read_u16 v121, v0 offset:6624
	ds_read_u16 v122, v0 offset:6768
	ds_read_u16 v123, v0 offset:6912
	ds_read_u16 v124, v0 offset:7056
	ds_read_u16 v125, v0 offset:7120
	ds_read_u16 v126, v0 offset:6976
	ds_read_u16 v127, v0 offset:6832
	ds_read_u16 v128, v0 offset:6688
	ds_read_u16 v129, v0 offset:7776
	ds_read_u16 v130, v0 offset:7920
	ds_read_u16 v131, v0 offset:8064
	ds_read_u16 v132, v0 offset:8208
	ds_read_u16 v133, v0 offset:8272
	ds_read_u16 v134, v0 offset:8128
	ds_read_u16 v135, v0 offset:7984
	ds_read_u16 v0, v0 offset:7840
	ds_read_b128 v[70:73], v68 offset:9216
	s_waitcnt lgkmcnt(14)
; __device__ __forceinline__ void ph_rwkv_chunk(const Params& p, int l, LAS unsigned char* lds, const int wvid) {
;     ...
;             { bf16x8 Kp[4][2]; asm volatile("" ::: "memory"); R2_RAW(X, KTg); R2_PSEUDO_L(Kp, X); R2_MM_LP(Q, Y, Kp); }
; #pragma unroll
;             for (int rb = 0; rb < 2; ++rb)
; #pragma unroll
;                 for (int r = 0; r < 16; ++r) { Q[rb][0][r] *= gc0; Q[rb][1][r] *= gc1; }
;             R2_STORE_T(QTg, Q, false, 1.0f);
;         }
;         asm volatile("" ::: "memory");
;     }
	v_lshl_or_b32 v74, v75, 16, v74
	v_lshl_or_b32 v75, v77, 16, v76
	v_lshl_or_b32 v76, v82, 16, v81
	v_lshl_or_b32 v77, v84, 16, v83
	v_lshl_or_b32 v78, v78, 16, v69
	v_lshl_or_b32 v79, v79, 16, v80
	v_lshl_or_b32 v80, v87, 16, v88
	v_lshl_or_b32 v81, v85, 16, v86
	s_waitcnt lgkmcnt(0)
	v_mfma_f32_32x32x16_bf16 v[34:49], v[70:73], v[74:77], v[34:49]
	v_mfma_f32_32x32x16_bf16 v[50:65], v[70:73], v[78:81], v[50:65]
	ds_read_b128 v[70:73], v68 offset:13824
	s_waitcnt lgkmcnt(0)
	v_mfma_f32_32x32x16_bf16 v[18:33], v[70:73], v[74:77], v[18:33]
	v_lshl_or_b32 v74, v90, 16, v89
	v_lshl_or_b32 v75, v92, 16, v91
	v_lshl_or_b32 v76, v98, 16, v97
	v_lshl_or_b32 v77, v100, 16, v99
	v_mfma_f32_32x32x16_bf16 v[2:17], v[70:73], v[78:81], v[2:17]
	ds_read_b128 v[70:73], v68 offset:9248
	v_lshl_or_b32 v78, v95, 16, v96
	v_lshl_or_b32 v79, v93, 16, v94
	v_lshl_or_b32 v80, v103, 16, v104
	v_lshl_or_b32 v81, v101, 16, v102
	s_waitcnt lgkmcnt(0)
	v_mfma_f32_32x32x16_bf16 v[34:49], v[70:73], v[74:77], v[34:49]
	v_mfma_f32_32x32x16_bf16 v[50:65], v[70:73], v[78:81], v[50:65]
	ds_read_b128 v[70:73], v68 offset:13856
	s_waitcnt lgkmcnt(0)
	v_mfma_f32_32x32x16_bf16 v[18:33], v[70:73], v[74:77], v[18:33]
	v_lshl_or_b32 v74, v106, 16, v105
	v_lshl_or_b32 v75, v108, 16, v107
	v_lshl_or_b32 v76, v114, 16, v113
	v_lshl_or_b32 v77, v116, 16, v115
	v_mfma_f32_32x32x16_bf16 v[2:17], v[70:73], v[78:81], v[2:17]
	ds_read_b128 v[70:73], v68 offset:9280
	v_lshl_or_b32 v78, v111, 16, v112
	v_lshl_or_b32 v79, v109, 16, v110
	v_lshl_or_b32 v80, v119, 16, v120
	v_lshl_or_b32 v81, v117, 16, v118
	s_waitcnt lgkmcnt(0)
	v_mfma_f32_32x32x16_bf16 v[34:49], v[70:73], v[74:77], v[34:49]
	v_mfma_f32_32x32x16_bf16 v[50:65], v[70:73], v[78:81], v[50:65]
	ds_read_b128 v[70:73], v68 offset:13888
	s_waitcnt lgkmcnt(0)
	v_mfma_f32_32x32x16_bf16 v[18:33], v[70:73], v[74:77], v[18:33]
	v_lshl_or_b32 v74, v122, 16, v121
	v_lshl_or_b32 v75, v124, 16, v123
	v_lshl_or_b32 v76, v130, 16, v129
	v_lshl_or_b32 v77, v132, 16, v131
	v_mfma_f32_32x32x16_bf16 v[2:17], v[70:73], v[78:81], v[2:17]
	ds_read_b128 v[70:73], v68 offset:9312
	v_lshl_or_b32 v78, v127, 16, v128
	v_lshl_or_b32 v79, v125, 16, v126
	v_lshl_or_b32 v80, v135, 16, v0
	v_lshl_or_b32 v81, v133, 16, v134
	v_lshl_or_b32 v0, v66, 5, v67
	s_waitcnt lgkmcnt(0)
	v_mfma_f32_32x32x16_bf16 v[34:49], v[70:73], v[74:77], v[34:49]
	v_mfma_f32_32x32x16_bf16 v[50:65], v[70:73], v[78:81], v[50:65]
	ds_read_b128 v[68:71], v68 offset:13920
	s_nop 9
	v_mul_f32_e64 v34, v192, v34
	v_mul_f32_e64 v35, v192, v35
	v_mul_f32_e64 v36, v192, v36
	v_mul_f32_e64 v37, v192, v37
	v_pk_mul_f32 v[38:39], v[192:193], v[38:39] op_sel_hi:[0,1]
	v_pk_mul_f32 v[40:41], v[192:193], v[40:41] op_sel_hi:[0,1]
	v_pk_mul_f32 v[42:43], v[192:193], v[42:43] op_sel_hi:[0,1]
	v_pk_mul_f32 v[44:45], v[192:193], v[44:45] op_sel_hi:[0,1]
	s_waitcnt lgkmcnt(0)
	v_mfma_f32_32x32x16_bf16 v[2:17], v[68:71], v[78:81], v[2:17]
	v_mul_f32_e64 v46, v192, v46
	v_mul_f32_e64 v47, v192, v47
	v_mul_f32_e64 v48, v192, v48
	v_mul_f32_e64 v49, v192, v49
	v_mul_f32_e64 v50, v190, v50
	v_mul_f32_e64 v51, v190, v51
	v_pk_mul_f32 v[52:53], v[190:191], v[52:53] op_sel_hi:[0,1]
	v_pk_mul_f32 v[54:55], v[190:191], v[54:55] op_sel_hi:[0,1]
	v_pk_mul_f32 v[56:57], v[190:191], v[56:57] op_sel_hi:[0,1]
	v_pk_mul_f32 v[58:59], v[190:191], v[58:59] op_sel_hi:[0,1]
	v_mfma_f32_32x32x16_bf16 v[18:33], v[68:71], v[74:77], v[18:33]
	s_nop 0
	v_mul_f32_e64 v68, v190, v2
	v_mul_f32_e64 v69, v190, v3
	v_mul_f32_e64 v70, v190, v4
	v_mul_f32_e64 v71, v190, v5
	v_cvt_pk_bf16_f32 v2, v34, v35
	v_cvt_pk_bf16_f32 v3, v36, v37
	v_cvt_pk_bf16_f32 v4, v38, v39
	v_cvt_pk_bf16_f32 v5, v40, v41
	s_nop 0
	v_permlane32_swap_b32_e32 v2, v4
	v_permlane32_swap_b32_e32 v3, v5
	global_store_dwordx4 v0, v[2:5], s[34:35]
	v_pk_mul_f32 v[60:61], v[190:191], v[60:61] op_sel_hi:[0,1]
	v_pk_mul_f32 v[62:63], v[190:191], v[62:63] op_sel_hi:[0,1]
	v_cvt_pk_bf16_f32 v2, v42, v43
	v_cvt_pk_bf16_f32 v3, v44, v45
	v_cvt_pk_bf16_f32 v4, v46, v47
	v_cvt_pk_bf16_f32 v5, v48, v49
	s_nop 0
	v_permlane32_swap_b32_e32 v2, v4
	v_permlane32_swap_b32_e32 v3, v5
	global_store_dwordx4 v0, v[2:5], s[34:35] offset:2048
	v_pk_mul_f32 v[64:65], v[190:191], v[64:65] op_sel_hi:[0,1]
	v_pk_mul_f32 v[18:19], v[192:193], v[18:19] op_sel_hi:[0,1]
	v_cvt_pk_bf16_f32 v2, v50, v51
	v_cvt_pk_bf16_f32 v3, v52, v53
	v_cvt_pk_bf16_f32 v4, v54, v55
	v_cvt_pk_bf16_f32 v5, v56, v57
	s_nop 0
	v_permlane32_swap_b32_e32 v2, v4
	v_permlane32_swap_b32_e32 v3, v5
	global_store_dwordx4 v0, v[2:5], s[34:35] offset:1024
	v_pk_mul_f32 v[20:21], v[192:193], v[20:21] op_sel_hi:[0,1]
	v_pk_mul_f32 v[22:23], v[192:193], v[22:23] op_sel_hi:[0,1]
	v_cvt_pk_bf16_f32 v2, v58, v59
	v_cvt_pk_bf16_f32 v3, v60, v61
	v_cvt_pk_bf16_f32 v4, v62, v63
	v_cvt_pk_bf16_f32 v5, v64, v65
	v_pk_mul_f32 v[24:25], v[192:193], v[24:25] op_sel_hi:[0,1]
	v_lshl_add_u64 v[34:35], s[34:35], 0, v[0:1]
	v_permlane32_swap_b32_e32 v2, v4
	v_permlane32_swap_b32_e32 v3, v5
	global_store_dwordx4 v0, v[2:5], s[34:35] offset:3072
	v_pk_mul_f32 v[26:27], v[192:193], v[26:27] op_sel_hi:[0,1]
	v_pk_mul_f32 v[28:29], v[192:193], v[28:29] op_sel_hi:[0,1]
	v_cvt_pk_bf16_f32 v2, v18, v19
	v_cvt_pk_bf16_f32 v3, v20, v21
	v_cvt_pk_bf16_f32 v4, v22, v23
	v_cvt_pk_bf16_f32 v5, v24, v25
	v_add_co_u32_e32 v18, vcc, s44, v34
	v_pk_mul_f32 v[30:31], v[192:193], v[30:31] op_sel_hi:[0,1]
	v_pk_mul_f32 v[32:33], v[192:193], v[32:33] op_sel_hi:[0,1]
	v_permlane32_swap_b32_e32 v2, v4
	v_permlane32_swap_b32_e32 v3, v5
	v_addc_co_u32_e32 v19, vcc, 0, v35, vcc
	global_store_dwordx4 v[18:19], v[2:5], off
	v_pk_mul_f32 v[6:7], v[190:191], v[6:7] op_sel_hi:[0,1]
	v_pk_mul_f32 v[8:9], v[190:191], v[8:9] op_sel_hi:[0,1]
	v_cvt_pk_bf16_f32 v2, v26, v27
	v_cvt_pk_bf16_f32 v3, v28, v29
	v_cvt_pk_bf16_f32 v4, v30, v31
	v_cvt_pk_bf16_f32 v5, v32, v33
	s_nop 0
	v_permlane32_swap_b32_e32 v2, v4
	v_permlane32_swap_b32_e32 v3, v5
	global_store_dwordx4 v[18:19], v[2:5], off offset:2048
	v_pk_mul_f32 v[10:11], v[190:191], v[10:11] op_sel_hi:[0,1]
	v_pk_mul_f32 v[12:13], v[190:191], v[12:13] op_sel_hi:[0,1]
	v_cvt_pk_bf16_f32 v2, v68, v69
	v_cvt_pk_bf16_f32 v3, v70, v71
	v_cvt_pk_bf16_f32 v4, v6, v7
	v_cvt_pk_bf16_f32 v5, v8, v9
	v_pk_mul_f32 v[14:15], v[190:191], v[14:15] op_sel_hi:[0,1]
	v_pk_mul_f32 v[16:17], v[190:191], v[16:17] op_sel_hi:[0,1]
	v_permlane32_swap_b32_e32 v2, v4
	v_permlane32_swap_b32_e32 v3, v5
	global_store_dwordx4 v[18:19], v[2:5], off offset:1024
	s_mov_b32 s44, 0x939a85c5
	s_nop 0
	v_cvt_pk_bf16_f32 v2, v10, v11
	v_cvt_pk_bf16_f32 v3, v12, v13
	v_cvt_pk_bf16_f32 v4, v14, v15
	v_cvt_pk_bf16_f32 v5, v16, v17
	s_nop 0
	v_permlane32_swap_b32_e32 v2, v4
	v_permlane32_swap_b32_e32 v3, v5
	global_store_dwordx4 v[18:19], v[2:5], off offset:3072
	s_branch .LBB0_646

; #define LAS __attribute__((address_space(3)))
; __device__ __forceinline__ float bflo(unsigned w) { return __uint_as_float(w << 16); }
; __device__ __forceinline__ float bfhi(unsigned w) { return __uint_as_float(w & 0xFFFF0000u); }
; __device__ __forceinline__ unsigned pkbf(float lo, float hi) { f32x2_t v = {lo, hi}; bf16x2_t b = __builtin_convertvector(v, bf16x2_t); return __builtin_bit_cast(unsigned, b); }
; __device__ __forceinline__ void swa_tile(const LAS unsigned char* Kb, const LAS unsigned char* Vb, const LAS float* btab, const bf16x8 (&Qf)[4], const bf16x8 qx, f32x16 (&O)[2],
;                                          float& lsum, int qpos, int k0, int l31, int hi) {
;     ...
;     f32x16 S[2];
; #pragma unroll
;     for (int kb = 0; kb < 2; ++kb) {
;         f32x16 acc;
; #pragma unroll
;         for (int r = 0; r < 16; ++r) acc[r] = 0.f;
; #pragma unroll
;         for (int s = 0; s < 4; ++s) { const bf16x8 kf = *(const LAS bf16x8*)(Kb + (32 * kb + l31) * DF_PITCH + s * 32 + hi * 16);
;             acc = __builtin_amdgcn_mfma_f32_32x32x16_bf16(kf, Qf[s], acc, 0, 0, 0); }
;         acc = __builtin_amdgcn_mfma_f32_32x32x16_bf16(kx, qx, acc, 0, 0, 0);
;         S[kb] = acc;
;     }
;     float ls = 0.f;
;     bf16x8 Pf[4];
; #pragma unroll
;     for (int kb = 0; kb < 2; ++kb) {
; #pragma unroll
;         for (int r = 0; r < 16; ++r) { const int j = k0 + 32 * kb + (r & 3) + 8 * (r >> 2) + 4 * hi, dist = qpos - j;
;             const LAS float* tb = (k0 == 0 && kb == 0 && r < 8) ? btab + 4 * 132 : btab;
;             const float pv = __builtin_amdgcn_exp2f(S[kb][r] + tb[min(max(dist + 1, 0), 129)]); ls += pv; S[kb][r] = pv; }
;     ...
;           for (int s = 0; s < 4; ++s) { const unsigned qw[4] = {qraw[s].x, qraw[s].y, qraw[s].z, qraw[s].w}; u32x4 qs;
; #pragma unroll
;               for (int e = 0; e < 4; ++e) qn2 += bflo(qw[e]) * bflo(qw[e]) + bfhi(qw[e]) * bfhi(qw[e]);
;               qs.x = pkbf(bflo(qw[0]) * c2, bfhi(qw[0]) * c2); qs.y = pkbf(bflo(qw[1]) * c2, bfhi(qw[1]) * c2); qs.z = pkbf(bflo(qw[2]) * c2, bfhi(qw[2]) * c2); qs.w = pkbf(bflo(qw[3]) * c2, bfhi(qw[3]) * c2);
;               Qf[s] = __builtin_bit_cast(bf16x8, qs); }
.LBB0_817:
	s_mov_b32 s0, 0x3e38aa3b
	v_pk_mul_f32 v[20:21], v[20:21], s[0:1] op_sel_hi:[1,0]
	v_pk_mul_f32 v[18:19], v[18:19], s[0:1] op_sel_hi:[1,0]
	v_pk_mul_f32 v[16:17], v[16:17], s[0:1] op_sel_hi:[1,0]
	s_mov_b64 vcc, s[4:5]
	v_cvt_pk_bf16_f32 v82, v20, v21
	v_pk_mul_f32 v[20:21], v[26:27], s[0:1] op_sel_hi:[1,0]
	v_cvt_pk_bf16_f32 v86, v18, v19
	v_pk_mul_f32 v[18:19], v[24:25], s[0:1] op_sel_hi:[1,0]
	v_cvt_pk_bf16_f32 v90, v16, v17
	v_pk_mul_f32 v[16:17], v[22:23], s[0:1] op_sel_hi:[1,0]
	v_mov_b32_e32 v5, v7
	v_cndmask_b32_sdwa v78, v1, v3, vcc dst_sel:DWORD dst_unused:UNUSED_PAD src0_sel:DWORD src1_sel:WORD_0
	v_cvt_pk_bf16_f32 v83, v20, v21
	v_pk_mul_f32 v[20:21], v[32:33], s[0:1] op_sel_hi:[1,0]
	v_cvt_pk_bf16_f32 v87, v18, v19
	v_pk_mul_f32 v[18:19], v[30:31], s[0:1] op_sel_hi:[1,0]
	v_cvt_pk_bf16_f32 v91, v16, v17
	v_pk_mul_f32 v[16:17], v[28:29], s[0:1] op_sel_hi:[1,0]
	v_mov_b32_e32 v11, v15
	v_pk_mul_f32 v[4:5], v[4:5], s[0:1] op_sel_hi:[1,0]
	v_mov_b32_e32 v7, v13
	v_mov_b32_e32 v3, v9
	v_cvt_pk_bf16_f32 v84, v20, v21
	v_pk_mul_f32 v[20:21], v[38:39], s[0:1] op_sel_hi:[1,0]
	v_cvt_pk_bf16_f32 v88, v18, v19
	v_pk_mul_f32 v[18:19], v[36:37], s[0:1] op_sel_hi:[1,0]
	v_cvt_pk_bf16_f32 v92, v16, v17
	v_pk_mul_f32 v[16:17], v[34:35], s[0:1] op_sel_hi:[1,0]
	v_pk_mul_f32 v[10:11], v[10:11], s[0:1] op_sel_hi:[1,0]
	v_cvt_pk_bf16_f32 v95, v4, v5
	v_pk_mul_f32 v[4:5], v[6:7], s[0:1] op_sel_hi:[1,0]
	v_pk_mul_f32 v[2:3], v[2:3], s[0:1] op_sel_hi:[1,0]
	v_cndmask_b32_e64 v0, 0, 1, s[28:29]
	v_mov_b32_e32 v79, v1
	v_mov_b32_e32 v80, v1
	v_mov_b32_e32 v81, v1
	v_cvt_pk_bf16_f32 v85, v20, v21
	v_cvt_pk_bf16_f32 v89, v18, v19
	v_cvt_pk_bf16_f32 v93, v16, v17
	v_cvt_pk_bf16_f32 v94, v10, v11
	v_cvt_pk_bf16_f32 v96, v4, v5
	v_cvt_pk_bf16_f32 v97, v2, v3
	v_cmp_ne_u32_e64 s[8:9], 1, v0
	s_andn2_b64 vcc, exec, s[28:29]
	v_mov_b32_e32 v18, 0
	s_cbranch_vccnz .LBB0_820
	v_sub_u32_e32 v0, v40, v114
	ds_read_b128 v[136:139], v115 offset:8192
	ds_read_b128 v[140:143], v115 offset:8224
	ds_read_b128 v[144:147], v115 offset:8256
	ds_read_b128 v[148:151], v115 offset:8288
	ds_read_b128 v[196:199], v115 offset:12800
	ds_read_b128 v[200:203], v115 offset:12832
	ds_read_b128 v[206:209], v115 offset:12864
	ds_read_b128 v[210:213], v115 offset:12896
	v_max_i32_e32 v184, -1, v0
	v_add_u32_e32 v184, 1, v184
	v_min_u32_e32 v184, 0x81, v184
	v_lshl_add_u32 v184, v184, 2, v122
	ds_read_b32 v184, v184 offset:2112
	v_add_u32_e32 v185, v40, v116
	v_max_i32_e32 v185, -1, v185
	v_add_u32_e32 v185, 1, v185
	v_min_u32_e32 v185, 0x81, v185
	v_lshl_add_u32 v185, v185, 2, v122
	ds_read_b32 v185, v185 offset:2112
	v_add_u32_e32 v186, -2, v0
	v_max_i32_e32 v186, -1, v186
	v_add_u32_e32 v186, 1, v186
	v_min_u32_e32 v186, 0x81, v186
	v_lshl_add_u32 v186, v186, 2, v122
	ds_read_b32 v186, v186 offset:2112
	v_add_u32_e32 v187, -3, v0
	v_max_i32_e32 v187, -1, v187
	v_add_u32_e32 v187, 1, v187
	v_min_u32_e32 v187, 0x81, v187
	v_lshl_add_u32 v187, v187, 2, v122
	ds_read_b32 v187, v187 offset:2112
	s_waitcnt lgkmcnt(11)
	v_mfma_f32_32x32x16_bf16 v[18:33], v[136:139], v[82:85], 0
	v_add_u32_e32 v188, -8, v0
	v_max_i32_e32 v188, -1, v188
	v_add_u32_e32 v188, 1, v188
	v_min_u32_e32 v188, 0x81, v188
	v_lshl_add_u32 v188, v188, 2, v122
	ds_read_b32 v188, v188 offset:2112
	s_waitcnt lgkmcnt(11)
	v_mfma_f32_32x32x16_bf16 v[18:33], v[140:143], v[86:89], v[18:33]
	v_add_u32_e32 v189, -9, v0
	v_max_i32_e32 v189, -1, v189
	v_add_u32_e32 v189, 1, v189
	v_min_u32_e32 v189, 0x81, v189
	v_lshl_add_u32 v189, v189, 2, v122
	ds_read_b32 v189, v189 offset:2112
	s_waitcnt lgkmcnt(11)
	v_mfma_f32_32x32x16_bf16 v[18:33], v[144:147], v[90:93], v[18:33]
	v_add_u32_e32 v194, -10, v0
	v_max_i32_e32 v194, -1, v194
	v_add_u32_e32 v194, 1, v194
	v_min_u32_e32 v194, 0x81, v194
	v_lshl_add_u32 v194, v194, 2, v122
	ds_read_b32 v194, v194 offset:2112
	s_waitcnt lgkmcnt(11)
	v_mfma_f32_32x32x16_bf16 v[18:33], v[148:151], v[94:97], v[18:33]
	v_subrev_u32_e32 v195, 32, v0
	v_max_i32_e32 v195, -1, v195
	v_add_u32_e32 v195, 1, v195
	v_min_u32_e32 v195, 0x81, v195
	v_lshl_add_u32 v195, v195, 2, v122
	ds_read_b32 v195, v195
	s_waitcnt lgkmcnt(11)
	v_mfma_f32_32x32x16_bf16 v[2:17], v[196:199], v[82:85], 0
	v_add_u32_e32 v229, -11, v0
	v_max_i32_e32 v229, -1, v229
	v_add_u32_e32 v229, 1, v229
	v_min_u32_e32 v229, 0x81, v229
	v_lshl_add_u32 v229, v229, 2, v122
	ds_read_b32 v229, v229 offset:2112
	s_waitcnt lgkmcnt(11)
	v_mfma_f32_32x32x16_bf16 v[2:17], v[200:203], v[86:89], v[2:17]
	v_add_u32_e32 v230, -16, v0
	v_max_i32_e32 v230, -1, v230
	v_add_u32_e32 v230, 1, v230
	v_min_u32_e32 v230, 0x81, v230
	v_lshl_add_u32 v230, v230, 2, v122
	ds_read_b32 v230, v230
	s_waitcnt lgkmcnt(11)
	v_mfma_f32_32x32x16_bf16 v[2:17], v[206:209], v[90:93], v[2:17]
	v_subrev_u32_e32 v231, 33, v0
	v_max_i32_e32 v231, -1, v231
	v_add_u32_e32 v231, 1, v231
	v_min_u32_e32 v231, 0x81, v231
	v_lshl_add_u32 v231, v231, 2, v122
	ds_read_b32 v231, v231
	s_waitcnt lgkmcnt(11)
	v_mfma_f32_32x32x16_bf16 v[2:17], v[210:213], v[94:97], v[2:17]
	v_subrev_u32_e32 v248, 17, v0
	v_max_i32_e32 v248, -1, v248
	v_add_u32_e32 v248, 1, v248
	v_min_u32_e32 v248, 0x81, v248
	v_lshl_add_u32 v248, v248, 2, v122
	ds_read_b32 v248, v248
	v_mfma_f32_32x32x16_bf16 v[18:33], v[66:69], v[78:81], v[18:33]
	v_mfma_f32_32x32x16_bf16 v[2:17], v[66:69], v[78:81], v[2:17]
	s_nop 9
	s_waitcnt lgkmcnt(11)
	v_add_f32_e32 v18, v18, v184
	v_subrev_u32_e32 v184, 18, v0
	v_max_i32_e32 v184, -1, v184
	v_add_u32_e32 v184, 1, v184
	v_min_u32_e32 v184, 0x81, v184
	v_lshl_add_u32 v184, v184, 2, v122
	ds_read_b32 v184, v184
	v_exp_f32_e32 v18, v18
	s_waitcnt lgkmcnt(11)
; #define LAS __attribute__((address_space(3)))
; __device__ __forceinline__ void swa_tile(const LAS unsigned char* Kb, const LAS unsigned char* Vb, const LAS float* btab, const bf16x8 (&Qf)[4], const bf16x8 qx, f32x16 (&O)[2],
;                                          float& lsum, int qpos, int k0, int l31, int hi) {
;     ...
;     float ls = 0.f;
;     bf16x8 Pf[4];
; #pragma unroll
;     for (int kb = 0; kb < 2; ++kb) {
; #pragma unroll
;         for (int r = 0; r < 16; ++r) { const int j = k0 + 32 * kb + (r & 3) + 8 * (r >> 2) + 4 * hi, dist = qpos - j;
;             const LAS float* tb = (k0 == 0 && kb == 0 && r < 8) ? btab + 4 * 132 : btab;
;             const float pv = __builtin_amdgcn_exp2f(S[kb][r] + tb[min(max(dist + 1, 0), 129)]); ls += pv; S[kb][r] = pv; }
	v_add_f32_e32 v19, v19, v185
	v_subrev_u32_e32 v185, 34, v0
	v_max_i32_e32 v185, -1, v185
	v_add_u32_e32 v185, 1, v185
	v_min_u32_e32 v185, 0x81, v185
	v_lshl_add_u32 v185, v185, 2, v122
	ds_read_b32 v185, v185
	v_exp_f32_e32 v19, v19
	s_waitcnt lgkmcnt(11)
	v_add_f32_e32 v20, v20, v186
	v_subrev_u32_e32 v186, 19, v0
	v_max_i32_e32 v186, -1, v186
	v_add_u32_e32 v186, 1, v186
	v_min_u32_e32 v186, 0x81, v186
	v_lshl_add_u32 v186, v186, 2, v122
	ds_read_b32 v186, v186
	v_cvt_pk_bf16_f32 v38, v18, v19
	v_add_f32_e32 v18, 0, v18
	v_add_f32_e32 v18, v18, v19
	s_waitcnt lgkmcnt(11)
	v_add_f32_e32 v21, v21, v187
	v_subrev_u32_e32 v187, 35, v0
	v_max_i32_e32 v187, -1, v187
	v_add_u32_e32 v187, 1, v187
	v_min_u32_e32 v187, 0x81, v187
	v_lshl_add_u32 v187, v187, 2, v122
	ds_read_b32 v187, v187
	s_waitcnt lgkmcnt(11)
	v_add_f32_e32 v22, v22, v188
	v_subrev_u32_e32 v188, 24, v0
	v_max_i32_e32 v188, -1, v188
	v_add_u32_e32 v188, 1, v188
	v_min_u32_e32 v188, 0x81, v188
	v_lshl_add_u32 v188, v188, 2, v122
	ds_read_b32 v188, v188
	v_exp_f32_e32 v20, v20
	v_exp_f32_e32 v21, v21
	v_exp_f32_e32 v22, v22
	s_waitcnt lgkmcnt(11)
	v_add_f32_e32 v23, v23, v189
	v_subrev_u32_e32 v189, 40, v0
	v_max_i32_e32 v189, -1, v189
	v_add_u32_e32 v189, 1, v189
	v_min_u32_e32 v189, 0x81, v189
	v_lshl_add_u32 v189, v189, 2, v122
	ds_read_b32 v189, v189
	v_exp_f32_e32 v23, v23
	v_add_f32_e32 v18, v18, v20
	v_add_f32_e32 v18, v18, v21
	v_add_f32_e32 v18, v18, v22
	s_waitcnt lgkmcnt(11)
	v_add_f32_e32 v24, v24, v194
	v_subrev_u32_e32 v194, 25, v0
	v_max_i32_e32 v194, -1, v194
	v_add_u32_e32 v194, 1, v194
	v_min_u32_e32 v194, 0x81, v194
	v_lshl_add_u32 v194, v194, 2, v122
	ds_read_b32 v194, v194
	s_waitcnt lgkmcnt(11)
	v_add_f32_e32 v2, v2, v195
	v_subrev_u32_e32 v195, 41, v0
	v_max_i32_e32 v195, -1, v195
	v_add_u32_e32 v195, 1, v195
	v_min_u32_e32 v195, 0x81, v195
	v_lshl_add_u32 v195, v195, 2, v122
	ds_read_b32 v195, v195
	s_waitcnt lgkmcnt(11)
	v_add_f32_e32 v25, v25, v229
	v_subrev_u32_e32 v229, 26, v0
	v_max_i32_e32 v229, -1, v229
	v_add_u32_e32 v229, 1, v229
	v_min_u32_e32 v229, 0x81, v229
	v_lshl_add_u32 v229, v229, 2, v122
	ds_read_b32 v229, v229
	v_exp_f32_e32 v24, v24
	s_waitcnt lgkmcnt(11)
	v_add_f32_e32 v26, v26, v230
	v_subrev_u32_e32 v230, 42, v0
	v_max_i32_e32 v230, -1, v230
	v_add_u32_e32 v230, 1, v230
	v_min_u32_e32 v230, 0x81, v230
	v_lshl_add_u32 v230, v230, 2, v122
	ds_read_b32 v230, v230
	s_waitcnt lgkmcnt(11)
	v_add_f32_e32 v3, v3, v231
	v_subrev_u32_e32 v231, 27, v0
	v_max_i32_e32 v231, -1, v231
	v_add_u32_e32 v231, 1, v231
	v_min_u32_e32 v231, 0x81, v231
	v_lshl_add_u32 v231, v231, 2, v122
	ds_read_b32 v231, v231
	s_waitcnt lgkmcnt(11)
	v_add_f32_e32 v27, v27, v248
	v_subrev_u32_e32 v248, 43, v0
	v_max_i32_e32 v248, -1, v248
	v_add_u32_e32 v248, 1, v248
	v_min_u32_e32 v248, 0x81, v248
	v_lshl_add_u32 v248, v248, 2, v122
	ds_read_b32 v248, v248
	v_exp_f32_e32 v25, v25
	v_exp_f32_e32 v26, v26
	v_exp_f32_e32 v27, v27
	s_waitcnt lgkmcnt(11)
	v_add_f32_e32 v28, v28, v184
	v_subrev_u32_e32 v184, 48, v0
	v_max_i32_e32 v184, -1, v184
	v_add_u32_e32 v184, 1, v184
	v_min_u32_e32 v184, 0x81, v184
	v_lshl_add_u32 v184, v184, 2, v122
	ds_read_b32 v184, v184
	s_waitcnt lgkmcnt(11)
	v_add_f32_e32 v4, v4, v185
	v_subrev_u32_e32 v185, 49, v0
	v_max_i32_e32 v185, -1, v185
	v_add_u32_e32 v185, 1, v185
	v_min_u32_e32 v185, 0x81, v185
	v_lshl_add_u32 v185, v185, 2, v122
	ds_read_b32 v185, v185
	v_add_f32_e32 v18, v18, v23
	v_exp_f32_e32 v28, v28
	v_add_f32_e32 v18, v18, v24
	s_waitcnt lgkmcnt(11)
	v_add_f32_e32 v29, v29, v186
	v_subrev_u32_e32 v186, 50, v0
	v_max_i32_e32 v186, -1, v186
	v_add_u32_e32 v186, 1, v186
	v_min_u32_e32 v186, 0x81, v186
	v_lshl_add_u32 v186, v186, 2, v122
	ds_read_b32 v186, v186
	s_waitcnt lgkmcnt(11)
	v_add_f32_e32 v5, v5, v187
	v_subrev_u32_e32 v187, 51, v0
	v_max_i32_e32 v187, -1, v187
	v_add_u32_e32 v187, 1, v187
	v_min_u32_e32 v187, 0x81, v187
	v_lshl_add_u32 v187, v187, 2, v122
	ds_read_b32 v187, v187
	v_exp_f32_e32 v29, v29
	v_add_f32_e32 v18, v18, v25
	v_add_f32_e32 v18, v18, v26
	s_waitcnt lgkmcnt(11)
	v_add_f32_e32 v30, v30, v188
	v_subrev_u32_e32 v188, 56, v0
	v_max_i32_e32 v188, -1, v188
	v_add_u32_e32 v188, 1, v188
	v_min_u32_e32 v188, 0x81, v188
	v_lshl_add_u32 v188, v188, 2, v122
	ds_read_b32 v188, v188
	s_waitcnt lgkmcnt(11)
; #define LAS __attribute__((address_space(3)))
; __device__ __forceinline__ void swa_tile(const LAS unsigned char* Kb, const LAS unsigned char* Vb, const LAS float* btab, const bf16x8 (&Qf)[4], const bf16x8 qx, f32x16 (&O)[2],
;                                          float& lsum, int qpos, int k0, int l31, int hi) {
;     ...
;     float ls = 0.f;
;     bf16x8 Pf[4];
; #pragma unroll
;     for (int kb = 0; kb < 2; ++kb) {
; #pragma unroll
;         for (int r = 0; r < 16; ++r) { const int j = k0 + 32 * kb + (r & 3) + 8 * (r >> 2) + 4 * hi, dist = qpos - j;
;             const LAS float* tb = (k0 == 0 && kb == 0 && r < 8) ? btab + 4 * 132 : btab;
;             const float pv = __builtin_amdgcn_exp2f(S[kb][r] + tb[min(max(dist + 1, 0), 129)]); ls += pv; S[kb][r] = pv; }
; #pragma unroll
;         for (int s = 0; s < 2; ++s) Pf[2 * kb + s] = pack_acc(S[kb], s);
;     }
;     lsum += ls;
; #pragma unroll
;     for (int st = 0; st < 4; ++st) { asm volatile("" ::: "memory");
; #pragma unroll
;         for (int dvb = 0; dvb < 2; ++dvb) { const bf16x8 vf = *(const LAS bf16x8*)(Vb + (32 * dvb + l31) * DF_PITCH + st * 32 + hi * 16);
;             O[dvb] = __builtin_amdgcn_mfma_f32_32x32x16_bf16(vf, Pf[st], O[dvb], 0, 0, 0); } }
;     asm volatile("" ::: "memory");
	v_add_f32_e32 v6, v6, v189
	v_subrev_u32_e32 v189, 57, v0
	v_max_i32_e32 v189, -1, v189
	v_add_u32_e32 v189, 1, v189
	v_min_u32_e32 v189, 0x81, v189
	v_lshl_add_u32 v189, v189, 2, v122
	ds_read_b32 v189, v189
	v_exp_f32_e32 v30, v30
	v_add_f32_e32 v18, v18, v27
	v_add_f32_e32 v18, v18, v28
	s_waitcnt lgkmcnt(11)
	v_add_f32_e32 v31, v31, v194
	v_subrev_u32_e32 v194, 58, v0
	v_max_i32_e32 v194, -1, v194
	v_add_u32_e32 v194, 1, v194
	v_min_u32_e32 v194, 0x81, v194
	v_lshl_add_u32 v194, v194, 2, v122
	ds_read_b32 v194, v194
	s_waitcnt lgkmcnt(11)
	v_add_f32_e32 v7, v7, v195
	v_subrev_u32_e32 v195, 59, v0
	v_max_i32_e32 v195, -1, v195
	v_add_u32_e32 v195, 1, v195
	v_min_u32_e32 v195, 0x81, v195
	v_lshl_add_u32 v195, v195, 2, v122
	ds_read_b32 v195, v195
	v_exp_f32_e32 v31, v31
	v_add_f32_e32 v18, v18, v29
	v_add_f32_e32 v18, v18, v30
	s_waitcnt lgkmcnt(11)
	v_add_f32_e32 v32, v32, v229
	ds_read_b128 v[232:235], v115 offset:26624
	s_waitcnt lgkmcnt(11)
	v_add_f32_e32 v8, v8, v230
	ds_read_b128 v[236:239], v115 offset:31232
	v_exp_f32_e32 v32, v32
	v_exp_f32_e32 v2, v2
	v_exp_f32_e32 v3, v3
	s_waitcnt lgkmcnt(11)
	v_add_f32_e32 v33, v33, v231
	ds_read_b128 v[240:243], v115 offset:26656
	s_waitcnt lgkmcnt(11)
	v_add_f32_e32 v9, v9, v248
	ds_read_b128 v[244:247], v115 offset:31264
	v_exp_f32_e32 v33, v33
	v_add_f32_e32 v18, v18, v31
	v_add_f32_e32 v18, v18, v32
	v_exp_f32_e32 v4, v4
	s_waitcnt lgkmcnt(11)
	v_add_f32_e32 v10, v10, v184
	ds_read_b128 v[136:139], v115 offset:26688
	v_add_f32_e32 v18, v18, v33
	v_exp_f32_e32 v5, v5
	v_exp_f32_e32 v6, v6
	v_cvt_pk_bf16_f32 v46, v2, v3
	s_waitcnt lgkmcnt(11)
	v_add_f32_e32 v11, v11, v185
	ds_read_b128 v[140:143], v115 offset:31296
	v_add_f32_e32 v2, v18, v2
	v_exp_f32_e32 v7, v7
	v_add_f32_e32 v2, v2, v3
	v_exp_f32_e32 v8, v8
	s_waitcnt lgkmcnt(11)
	v_add_f32_e32 v12, v12, v186
	ds_read_b128 v[144:147], v115 offset:26720
	v_add_f32_e32 v2, v2, v4
	v_exp_f32_e32 v9, v9
	v_add_f32_e32 v2, v2, v5
	v_exp_f32_e32 v10, v10
	s_waitcnt lgkmcnt(11)
	v_add_f32_e32 v13, v13, v187
	ds_read_b128 v[148:151], v115 offset:31328
	v_add_f32_e32 v2, v2, v6
	v_exp_f32_e32 v11, v11
	v_add_f32_e32 v2, v2, v7
	v_exp_f32_e32 v12, v12
	s_waitcnt lgkmcnt(11)
	v_add_f32_e32 v14, v14, v188
	v_add_f32_e32 v2, v2, v8
	v_exp_f32_e32 v13, v13
	v_add_f32_e32 v2, v2, v9
	v_exp_f32_e32 v14, v14
	s_waitcnt lgkmcnt(10)
	v_add_f32_e32 v15, v15, v189
	v_add_f32_e32 v2, v2, v10
	v_exp_f32_e32 v15, v15
	s_waitcnt lgkmcnt(9)
	v_add_f32_e32 v16, v16, v194
	v_add_f32_e32 v2, v2, v11
	v_exp_f32_e32 v16, v16
	s_waitcnt lgkmcnt(8)
	v_add_f32_e32 v0, v17, v195
	v_add_f32_e32 v2, v2, v12
	v_exp_f32_e32 v0, v0
	v_add_f32_e32 v2, v2, v13
	v_add_f32_e32 v2, v2, v14
	v_add_f32_e32 v2, v2, v15
	v_add_f32_e32 v2, v2, v16
	v_cvt_pk_bf16_f32 v47, v4, v5
	v_cvt_pk_bf16_f32 v45, v16, v0
	v_add_f32_e32 v0, v2, v0
	v_cvt_pk_bf16_f32 v39, v20, v21
	v_cvt_pk_bf16_f32 v40, v22, v23
	v_cvt_pk_bf16_f32 v41, v24, v25
	v_cvt_pk_bf16_f32 v34, v26, v27
	v_cvt_pk_bf16_f32 v35, v28, v29
	v_cvt_pk_bf16_f32 v36, v30, v31
	v_cvt_pk_bf16_f32 v37, v32, v33
	s_waitcnt lgkmcnt(7)
	v_mfma_f32_32x32x16_bf16 v[18:33], v[232:235], v[38:41], 0
	v_cvt_pk_bf16_f32 v48, v6, v7
	v_cvt_pk_bf16_f32 v49, v8, v9
	v_cvt_pk_bf16_f32 v42, v10, v11
	v_cvt_pk_bf16_f32 v43, v12, v13
	v_cvt_pk_bf16_f32 v44, v14, v15
	s_waitcnt lgkmcnt(6)
	v_mfma_f32_32x32x16_bf16 v[2:17], v[236:239], v[38:41], 0
	v_add_f32_e32 v121, v121, v0
	s_waitcnt lgkmcnt(5)
	v_mfma_f32_32x32x16_bf16 v[18:33], v[240:243], v[34:37], v[18:33]
	s_waitcnt lgkmcnt(4)
	v_mfma_f32_32x32x16_bf16 v[2:17], v[244:247], v[34:37], v[2:17]
	s_waitcnt lgkmcnt(3)
	v_mfma_f32_32x32x16_bf16 v[18:33], v[136:139], v[46:49], v[18:33]
	s_waitcnt lgkmcnt(2)
	v_mfma_f32_32x32x16_bf16 v[2:17], v[140:143], v[46:49], v[2:17]
	s_waitcnt lgkmcnt(1)
	v_mfma_f32_32x32x16_bf16 v[18:33], v[144:147], v[42:45], v[18:33]
	s_waitcnt lgkmcnt(0)
	v_mfma_f32_32x32x16_bf16 v[2:17], v[148:151], v[42:45], v[2:17]
	v_cndmask_b32_e64 v0, 0, 1, s[30:31]
	v_cmp_ne_u32_e64 s[0:1], 1, v0
	s_andn2_b64 vcc, exec, s[30:31]
	s_cbranch_vccz .LBB0_821
	s_branch .LBB0_822

; #define LAS __attribute__((address_space(3)))
; __device__ __forceinline__ void swa_tile(const LAS unsigned char* Kb, const LAS unsigned char* Vb, const LAS float* btab, const bf16x8 (&Qf)[4], const bf16x8 qx, f32x16 (&O)[2],
;                                          float& lsum, int qpos, int k0, int l31, int hi) {
;     ...
;     f32x16 S[2];
; #pragma unroll
;     for (int kb = 0; kb < 2; ++kb) {
;         f32x16 acc;
; #pragma unroll
;         for (int r = 0; r < 16; ++r) acc[r] = 0.f;
; #pragma unroll
;         for (int s = 0; s < 4; ++s) { const bf16x8 kf = *(const LAS bf16x8*)(Kb + (32 * kb + l31) * DF_PITCH + s * 32 + hi * 16);
;             acc = __builtin_amdgcn_mfma_f32_32x32x16_bf16(kf, Qf[s], acc, 0, 0, 0); }
;         acc = __builtin_amdgcn_mfma_f32_32x32x16_bf16(kx, qx, acc, 0, 0, 0);
;         S[kb] = acc;
;     }
;     float ls = 0.f;
;     bf16x8 Pf[4];
; #pragma unroll
;     for (int kb = 0; kb < 2; ++kb) {
; #pragma unroll
;         for (int r = 0; r < 16; ++r) { const int j = k0 + 32 * kb + (r & 3) + 8 * (r >> 2) + 4 * hi, dist = qpos - j;
;             const LAS float* tb = (k0 == 0 && kb == 0 && r < 8) ? btab + 4 * 132 : btab;
;             const float pv = __builtin_amdgcn_exp2f(S[kb][r] + tb[min(max(dist + 1, 0), 129)]); ls += pv; S[kb][r] = pv; }
;     ...
;         for (int ti = 0; ti < ntile; ++ti) {
;             const int kt = ti == 0 ? 0 : ktlo + ti - 1, k0 = kt * 64, cur = ti & 1;
;             if (ti + 1 < ntile) { const int kn = (ktlo + ti) * 64; kreg = *(const u32x4*)(kbase + (koff + (unsigned)(kn * INW))); vreg = *(const u32x4*)(vbase + (voff + (unsigned)kn)); }
;             if (wave_on && (kt == 0 || (k0 <= q0w + 31 && k0 + 63 >= q0w - 127)))
;                 swa_tile(KV + cur * DF_KB, KV + (2 + cur) * DF_KB, btab + hq * 132, Qf, qx, O, lsum, qpos, k0, l31, hi);
.LBB0_826:
	s_and_b64 vcc, exec, s[8:9]
	s_and_b32 s39, s0, 1
	s_cbranch_vccnz .LBB0_829
	v_add_u32_e32 v34, 63, v125
	v_cmp_gt_i32_e32 vcc, v125, v123
	v_cmp_lt_i32_e64 s[0:1], v34, v124
	s_or_b64 s[0:1], vcc, s[0:1]
	s_and_b64 vcc, exec, s[0:1]
	s_cbranch_vccnz .LBB0_829
	s_mul_i32 s0, s39, 0x2400
	v_add_u32_e32 v127, s0, v115
	ds_read_b128 v[136:139], v127 offset:8192
	ds_read_b128 v[140:143], v127 offset:8224
	ds_read_b128 v[144:147], v127 offset:8256
	ds_read_b128 v[148:151], v127 offset:8288
	ds_read_b128 v[196:199], v127 offset:12800
	ds_read_b128 v[200:203], v127 offset:12832
	ds_read_b128 v[206:209], v127 offset:12864
	ds_read_b128 v[210:213], v127 offset:12896
	v_add_u32_e32 v184, 59, v126
	v_max_i32_e32 v184, -1, v184
	v_add_u32_e32 v184, 1, v184
	v_min_u32_e32 v184, 0x81, v184
	v_lshl_add_u32 v184, v184, 2, v122
	ds_read_b32 v184, v184
	v_add_u32_e32 v185, 58, v126
	v_max_i32_e32 v185, -1, v185
	v_add_u32_e32 v185, 1, v185
	v_min_u32_e32 v185, 0x81, v185
	v_lshl_add_u32 v185, v185, 2, v122
	ds_read_b32 v185, v185
	v_add_u32_e32 v186, 57, v126
	v_max_i32_e32 v186, -1, v186
	v_add_u32_e32 v186, 1, v186
	v_min_u32_e32 v186, 0x81, v186
	v_lshl_add_u32 v186, v186, 2, v122
	ds_read_b32 v186, v186
	v_add_u32_e32 v187, 56, v126
	v_max_i32_e32 v187, -1, v187
	v_add_u32_e32 v187, 1, v187
	v_min_u32_e32 v187, 0x81, v187
	v_lshl_add_u32 v187, v187, 2, v122
	ds_read_b32 v187, v187
	s_waitcnt lgkmcnt(11)
	v_mfma_f32_32x32x16_bf16 v[50:65], v[136:139], v[82:85], 0
	v_add_u32_e32 v188, 51, v126
	v_max_i32_e32 v188, -1, v188
	v_add_u32_e32 v188, 1, v188
	v_min_u32_e32 v188, 0x81, v188
	v_lshl_add_u32 v188, v188, 2, v122
	ds_read_b32 v188, v188
	s_waitcnt lgkmcnt(11)
	v_mfma_f32_32x32x16_bf16 v[50:65], v[140:143], v[86:89], v[50:65]
	v_add_u32_e32 v189, 50, v126
	v_max_i32_e32 v189, -1, v189
	v_add_u32_e32 v189, 1, v189
	v_min_u32_e32 v189, 0x81, v189
	v_lshl_add_u32 v189, v189, 2, v122
	ds_read_b32 v189, v189
	s_waitcnt lgkmcnt(11)
	v_mfma_f32_32x32x16_bf16 v[50:65], v[144:147], v[90:93], v[50:65]
	v_add_u32_e32 v194, 49, v126
	v_max_i32_e32 v194, -1, v194
	v_add_u32_e32 v194, 1, v194
	v_min_u32_e32 v194, 0x81, v194
	v_lshl_add_u32 v194, v194, 2, v122
	ds_read_b32 v194, v194
	s_waitcnt lgkmcnt(11)
	v_mfma_f32_32x32x16_bf16 v[50:65], v[148:151], v[94:97], v[50:65]
	v_add_u32_e32 v195, 48, v126
	v_max_i32_e32 v195, -1, v195
	v_add_u32_e32 v195, 1, v195
	v_min_u32_e32 v195, 0x81, v195
	v_lshl_add_u32 v195, v195, 2, v122
	ds_read_b32 v195, v195
	s_waitcnt lgkmcnt(11)
	v_mfma_f32_32x32x16_bf16 v[34:49], v[196:199], v[82:85], 0
	v_add_u32_e32 v229, 43, v126
	v_max_i32_e32 v229, -1, v229
	v_add_u32_e32 v229, 1, v229
	v_min_u32_e32 v229, 0x81, v229
	v_lshl_add_u32 v229, v229, 2, v122
	ds_read_b32 v229, v229
	s_waitcnt lgkmcnt(11)
	v_mfma_f32_32x32x16_bf16 v[34:49], v[200:203], v[86:89], v[34:49]
	v_add_u32_e32 v230, 42, v126
	v_max_i32_e32 v230, -1, v230
	v_add_u32_e32 v230, 1, v230
	v_min_u32_e32 v230, 0x81, v230
	v_lshl_add_u32 v230, v230, 2, v122
	ds_read_b32 v230, v230
	s_waitcnt lgkmcnt(11)
	v_mfma_f32_32x32x16_bf16 v[34:49], v[206:209], v[90:93], v[34:49]
	v_add_u32_e32 v231, 41, v126
	v_max_i32_e32 v231, -1, v231
	v_add_u32_e32 v231, 1, v231
	v_min_u32_e32 v231, 0x81, v231
	v_lshl_add_u32 v231, v231, 2, v122
	ds_read_b32 v231, v231
	s_waitcnt lgkmcnt(11)
	v_mfma_f32_32x32x16_bf16 v[34:49], v[210:213], v[94:97], v[34:49]
	v_add_u32_e32 v248, 40, v126
	v_max_i32_e32 v248, -1, v248
	v_add_u32_e32 v248, 1, v248
	v_min_u32_e32 v248, 0x81, v248
	v_lshl_add_u32 v248, v248, 2, v122
	ds_read_b32 v248, v248
	v_mfma_f32_32x32x16_bf16 v[50:65], v[66:69], v[78:81], v[50:65]
	v_mfma_f32_32x32x16_bf16 v[34:49], v[66:69], v[78:81], v[34:49]
	s_nop 9
	s_waitcnt lgkmcnt(11)
	v_add_f32_e32 v50, v50, v184
	v_add_u32_e32 v184, 35, v126
	v_max_i32_e32 v184, -1, v184
	v_add_u32_e32 v184, 1, v184
	v_min_u32_e32 v184, 0x81, v184
	v_lshl_add_u32 v184, v184, 2, v122
	ds_read_b32 v184, v184
	v_exp_f32_e32 v128, v50
	s_waitcnt lgkmcnt(11)
	v_add_f32_e32 v50, v51, v185
	v_add_u32_e32 v185, 34, v126
	v_max_i32_e32 v185, -1, v185
	v_add_u32_e32 v185, 1, v185
	v_min_u32_e32 v185, 0x81, v185
	v_lshl_add_u32 v185, v185, 2, v122
	ds_read_b32 v185, v185
	v_exp_f32_e32 v129, v50
	s_waitcnt lgkmcnt(11)
	v_add_f32_e32 v50, v52, v186
	v_add_u32_e32 v186, 33, v126
	v_max_i32_e32 v186, -1, v186
	v_add_u32_e32 v186, 1, v186
	v_min_u32_e32 v186, 0x81, v186
	v_lshl_add_u32 v186, v186, 2, v122
	ds_read_b32 v186, v186
	v_exp_f32_e32 v130, v50
	s_waitcnt lgkmcnt(11)
	v_add_f32_e32 v50, v53, v187
	v_add_u32_e32 v187, 32, v126
	v_max_i32_e32 v187, -1, v187
	v_add_u32_e32 v187, 1, v187
	v_min_u32_e32 v187, 0x81, v187
	v_lshl_add_u32 v187, v187, 2, v122
	ds_read_b32 v187, v187
	v_exp_f32_e32 v131, v50
	s_waitcnt lgkmcnt(11)
	v_add_f32_e32 v50, v54, v188
	v_add_u32_e32 v188, 27, v126
	v_max_i32_e32 v188, -1, v188
	v_add_u32_e32 v188, 1, v188
	v_min_u32_e32 v188, 0x81, v188
	v_lshl_add_u32 v188, v188, 2, v122
	ds_read_b32 v188, v188
	v_exp_f32_e32 v132, v50
	v_cvt_pk_bf16_f32 v54, v128, v129
	v_add_f32_e32 v128, 0, v128
	v_add_f32_e32 v128, v128, v129
	v_add_f32_e32 v128, v128, v130
	s_waitcnt lgkmcnt(11)
	v_add_f32_e32 v50, v55, v189
	v_add_u32_e32 v189, 26, v126
	v_max_i32_e32 v189, -1, v189
	v_add_u32_e32 v189, 1, v189
	v_min_u32_e32 v189, 0x81, v189
	v_lshl_add_u32 v189, v189, 2, v122
	ds_read_b32 v189, v189
	v_exp_f32_e32 v133, v50
	v_add_f32_e32 v128, v128, v131
	v_add_f32_e32 v128, v128, v132
	v_add_f32_e32 v128, v128, v133
	v_cvt_pk_bf16_f32 v55, v130, v131
	s_waitcnt lgkmcnt(11)
; #define LAS __attribute__((address_space(3)))
; __device__ __forceinline__ void swa_tile(const LAS unsigned char* Kb, const LAS unsigned char* Vb, const LAS float* btab, const bf16x8 (&Qf)[4], const bf16x8 qx, f32x16 (&O)[2],
;                                          float& lsum, int qpos, int k0, int l31, int hi) {
;     ...
;     float ls = 0.f;
;     bf16x8 Pf[4];
; #pragma unroll
;     for (int kb = 0; kb < 2; ++kb) {
; #pragma unroll
;         for (int r = 0; r < 16; ++r) { const int j = k0 + 32 * kb + (r & 3) + 8 * (r >> 2) + 4 * hi, dist = qpos - j;
;             const LAS float* tb = (k0 == 0 && kb == 0 && r < 8) ? btab + 4 * 132 : btab;
;             const float pv = __builtin_amdgcn_exp2f(S[kb][r] + tb[min(max(dist + 1, 0), 129)]); ls += pv; S[kb][r] = pv; }
; #pragma unroll
;         for (int s = 0; s < 2; ++s) Pf[2 * kb + s] = pack_acc(S[kb], s);
;     }
;     lsum += ls;
; #pragma unroll
;     for (int st = 0; st < 4; ++st) { asm volatile("" ::: "memory");
; #pragma unroll
;         for (int dvb = 0; dvb < 2; ++dvb) { const bf16x8 vf = *(const LAS bf16x8*)(Vb + (32 * dvb + l31) * DF_PITCH + st * 32 + hi * 16);
;             O[dvb] = __builtin_amdgcn_mfma_f32_32x32x16_bf16(vf, Pf[st], O[dvb], 0, 0, 0); } }
;     asm volatile("" ::: "memory");
	v_add_f32_e32 v50, v56, v194
	v_add_u32_e32 v194, 25, v126
	v_max_i32_e32 v194, -1, v194
	v_add_u32_e32 v194, 1, v194
	v_min_u32_e32 v194, 0x81, v194
	v_lshl_add_u32 v194, v194, 2, v122
	ds_read_b32 v194, v194
	v_exp_f32_e32 v134, v50
	s_nop 0
	v_add_f32_e32 v128, v128, v134
	v_cvt_pk_bf16_f32 v56, v132, v133
	s_waitcnt lgkmcnt(11)
	v_add_f32_e32 v50, v57, v195
	v_add_u32_e32 v195, 24, v126
	v_max_i32_e32 v195, -1, v195
	v_add_u32_e32 v195, 1, v195
	v_min_u32_e32 v195, 0x81, v195
	v_lshl_add_u32 v195, v195, 2, v122
	ds_read_b32 v195, v195
	v_exp_f32_e32 v135, v50
	s_nop 0
	v_add_f32_e32 v128, v128, v135
	v_cvt_pk_bf16_f32 v57, v134, v135
	s_waitcnt lgkmcnt(11)
	v_add_f32_e32 v50, v58, v229
	v_add_u32_e32 v229, 19, v126
	v_max_i32_e32 v229, -1, v229
	v_add_u32_e32 v229, 1, v229
	v_min_u32_e32 v229, 0x81, v229
	v_lshl_add_u32 v229, v229, 2, v122
	ds_read_b32 v229, v229
	v_exp_f32_e32 v58, v50
	s_waitcnt lgkmcnt(11)
	v_add_f32_e32 v50, v59, v230
	v_add_u32_e32 v230, 18, v126
	v_max_i32_e32 v230, -1, v230
	v_add_u32_e32 v230, 1, v230
	v_min_u32_e32 v230, 0x81, v230
	v_lshl_add_u32 v230, v230, 2, v122
	ds_read_b32 v230, v230
	v_exp_f32_e32 v59, v50
	s_waitcnt lgkmcnt(11)
	v_add_f32_e32 v50, v60, v231
	v_add_u32_e32 v231, 17, v126
	v_max_i32_e32 v231, -1, v231
	v_add_u32_e32 v231, 1, v231
	v_min_u32_e32 v231, 0x81, v231
	v_lshl_add_u32 v231, v231, 2, v122
	ds_read_b32 v231, v231
	v_exp_f32_e32 v60, v50
	s_waitcnt lgkmcnt(11)
	v_add_f32_e32 v50, v61, v248
	v_add_u32_e32 v248, 16, v126
	v_max_i32_e32 v248, -1, v248
	v_add_u32_e32 v248, 1, v248
	v_min_u32_e32 v248, 0x81, v248
	v_lshl_add_u32 v248, v248, 2, v122
	ds_read_b32 v248, v248
	v_exp_f32_e32 v61, v50
	s_nop 0
	v_cvt_pk_bf16_f32 v51, v60, v61
	s_waitcnt lgkmcnt(11)
	v_add_f32_e32 v50, v62, v184
	v_add_u32_e32 v184, 11, v126
	v_max_i32_e32 v184, -1, v184
	v_add_u32_e32 v184, 1, v184
	v_min_u32_e32 v184, 0x81, v184
	v_lshl_add_u32 v184, v184, 2, v122
	ds_read_b32 v184, v184
	v_exp_f32_e32 v62, v50
	s_waitcnt lgkmcnt(11)
	v_add_f32_e32 v50, v63, v185
	v_add_u32_e32 v185, 10, v126
	v_max_i32_e32 v185, -1, v185
	v_add_u32_e32 v185, 1, v185
	v_min_u32_e32 v185, 0x81, v185
	v_lshl_add_u32 v185, v185, 2, v122
	ds_read_b32 v185, v185
	v_exp_f32_e32 v63, v50
	s_nop 0
	v_cvt_pk_bf16_f32 v52, v62, v63
	s_waitcnt lgkmcnt(11)
	v_add_f32_e32 v50, v64, v186
	v_add_u32_e32 v186, 9, v126
	v_max_i32_e32 v186, -1, v186
	v_add_u32_e32 v186, 1, v186
	v_min_u32_e32 v186, 0x81, v186
	v_lshl_add_u32 v186, v186, 2, v122
	ds_read_b32 v186, v186
	v_exp_f32_e32 v64, v50
	s_waitcnt lgkmcnt(11)
	v_add_f32_e32 v50, v65, v187
	v_add_u32_e32 v187, 8, v126
	v_max_i32_e32 v187, -1, v187
	v_add_u32_e32 v187, 1, v187
	v_min_u32_e32 v187, 0x81, v187
	v_lshl_add_u32 v187, v187, 2, v122
	ds_read_b32 v187, v187
	v_exp_f32_e32 v65, v50
	v_cvt_pk_bf16_f32 v50, v58, v59
	v_add_f32_e32 v58, v128, v58
	v_add_f32_e32 v58, v58, v59
	v_add_f32_e32 v58, v58, v60
	v_add_f32_e32 v58, v58, v61
	v_add_f32_e32 v58, v58, v62
	v_add_f32_e32 v58, v58, v63
	s_waitcnt lgkmcnt(11)
	v_add_f32_e32 v34, v34, v188
	v_add_u32_e32 v188, 3, v126
	v_max_i32_e32 v188, -1, v188
	v_add_u32_e32 v188, 1, v188
	v_min_u32_e32 v188, 0x81, v188
	v_lshl_add_u32 v188, v188, 2, v122
	ds_read_b32 v188, v188
	v_exp_f32_e32 v59, v34
	v_cvt_pk_bf16_f32 v53, v64, v65
	v_add_f32_e32 v58, v58, v64
	v_add_f32_e32 v58, v58, v65
	v_add_f32_e32 v58, v58, v59
	s_waitcnt lgkmcnt(11)
	v_add_f32_e32 v34, v35, v189
	v_add_u32_e32 v189, 2, v126
	v_max_i32_e32 v189, -1, v189
	v_add_u32_e32 v189, 1, v189
	v_min_u32_e32 v189, 0x81, v189
	v_lshl_add_u32 v189, v189, 2, v122
	ds_read_b32 v189, v189
	v_exp_f32_e32 v60, v34
	s_nop 0
	v_add_f32_e32 v58, v58, v60
	s_waitcnt lgkmcnt(11)
	v_add_f32_e32 v34, v36, v194
	v_add_u32_e32 v194, 1, v126
	v_max_i32_e32 v194, -1, v194
	v_add_u32_e32 v194, 1, v194
	v_min_u32_e32 v194, 0x81, v194
	v_lshl_add_u32 v194, v194, 2, v122
	ds_read_b32 v194, v194
	v_exp_f32_e32 v61, v34
	s_nop 0
	v_add_f32_e32 v58, v58, v61
	s_waitcnt lgkmcnt(11)
	v_add_f32_e32 v34, v37, v195
	v_max_i32_e32 v195, -1, v126
	v_add_u32_e32 v195, 1, v195
	v_min_u32_e32 v195, 0x81, v195
	v_lshl_add_u32 v195, v195, 2, v122
	ds_read_b32 v195, v195
	v_exp_f32_e32 v62, v34
	s_nop 0
	v_add_f32_e32 v58, v58, v62
	s_waitcnt lgkmcnt(11)
	v_add_f32_e32 v34, v38, v229
	ds_read_b128 v[232:235], v127 offset:26624
	v_exp_f32_e32 v63, v34
	s_nop 0
	v_add_f32_e32 v58, v58, v63
	v_cvt_pk_bf16_f32 v38, v59, v60
	s_waitcnt lgkmcnt(11)
	v_add_f32_e32 v34, v39, v230
	ds_read_b128 v[236:239], v127 offset:31232
	v_exp_f32_e32 v64, v34
	s_nop 0
	v_add_f32_e32 v58, v58, v64
	v_cvt_pk_bf16_f32 v39, v61, v62
	s_waitcnt lgkmcnt(11)
	v_add_f32_e32 v34, v40, v231
	ds_read_b128 v[240:243], v127 offset:26656
	v_exp_f32_e32 v65, v34
	s_nop 0
	v_add_f32_e32 v58, v58, v65
	v_cvt_pk_bf16_f32 v40, v63, v64
	s_waitcnt lgkmcnt(11)
	v_add_f32_e32 v34, v41, v248
	ds_read_b128 v[244:247], v127 offset:31264
	v_exp_f32_e32 v128, v34
	s_nop 0
	v_add_f32_e32 v58, v58, v128
	v_cvt_pk_bf16_f32 v41, v65, v128
	s_waitcnt lgkmcnt(11)
	v_add_f32_e32 v34, v42, v184
	ds_read_b128 v[136:139], v127 offset:26688
	v_exp_f32_e32 v42, v34
	s_waitcnt lgkmcnt(11)
	v_add_f32_e32 v34, v43, v185
	ds_read_b128 v[140:143], v127 offset:31296
	v_exp_f32_e32 v43, v34
	s_waitcnt lgkmcnt(11)
	v_add_f32_e32 v34, v44, v186
	ds_read_b128 v[144:147], v127 offset:26720
	v_exp_f32_e32 v44, v34
	s_waitcnt lgkmcnt(11)
	v_add_f32_e32 v34, v45, v187
	ds_read_b128 v[148:151], v127 offset:31328
	v_exp_f32_e32 v45, v34
	s_nop 0
	v_cvt_pk_bf16_f32 v35, v44, v45
	s_waitcnt lgkmcnt(11)
	v_add_f32_e32 v34, v46, v188
	v_exp_f32_e32 v46, v34
	s_waitcnt lgkmcnt(10)
	v_add_f32_e32 v34, v47, v189
	v_exp_f32_e32 v47, v34
	s_nop 0
	v_cvt_pk_bf16_f32 v36, v46, v47
	s_waitcnt lgkmcnt(9)
	v_add_f32_e32 v34, v48, v194
	v_exp_f32_e32 v48, v34
	s_waitcnt lgkmcnt(8)
	v_add_f32_e32 v34, v49, v195
	v_exp_f32_e32 v49, v34
	v_cvt_pk_bf16_f32 v34, v42, v43
	v_add_f32_e32 v42, v58, v42
	v_add_f32_e32 v42, v42, v43
	v_add_f32_e32 v42, v42, v44
	v_add_f32_e32 v42, v42, v45
	v_add_f32_e32 v42, v42, v46
	v_add_f32_e32 v42, v42, v47
	v_add_f32_e32 v42, v42, v48
	v_add_f32_e32 v42, v42, v49
	v_add_f32_e32 v121, v121, v42
	s_waitcnt lgkmcnt(7)
	v_mfma_f32_32x32x16_bf16 v[18:33], v[232:235], v[54:57], v[18:33]
	v_cvt_pk_bf16_f32 v37, v48, v49
	s_waitcnt lgkmcnt(6)
	v_mfma_f32_32x32x16_bf16 v[2:17], v[236:239], v[54:57], v[2:17]
	s_waitcnt lgkmcnt(5)
	v_mfma_f32_32x32x16_bf16 v[18:33], v[240:243], v[50:53], v[18:33]
	s_waitcnt lgkmcnt(4)
	v_mfma_f32_32x32x16_bf16 v[2:17], v[244:247], v[50:53], v[2:17]
	s_waitcnt lgkmcnt(3)
	v_mfma_f32_32x32x16_bf16 v[18:33], v[136:139], v[38:41], v[18:33]
	s_waitcnt lgkmcnt(2)
	v_mfma_f32_32x32x16_bf16 v[2:17], v[140:143], v[38:41], v[2:17]
	s_waitcnt lgkmcnt(1)
	v_mfma_f32_32x32x16_bf16 v[18:33], v[144:147], v[34:37], v[18:33]
	s_waitcnt lgkmcnt(0)
	v_mfma_f32_32x32x16_bf16 v[2:17], v[148:151], v[34:37], v[2:17]
